# speedup vs baseline: 1.0108x; 1.0108x over previous
_Z5k_fftPKtPtPKDv2_f:
	s_load_dwordx2 s[6:7], s[0:1], 0x10
	s_load_dwordx2 s[8:9], s[0:1], 0x0
	v_and_b32_e32 v1, 0xf0, v0
	v_and_b32_e32 v18, 15, v0
	v_mul_u32_u24_e32 v1, v1, v18
	v_lshlrev_b32_e32 v1, 3, v1
	s_waitcnt lgkmcnt(0)
	global_load_dwordx2 v[86:87], v1, s[6:7]
	s_lshr_b32 s4, s2, 3
	s_and_b32 s3, s2, 7
	s_and_b32 s4, s4, 0x1ffffff8
	s_or_b32 s4, s4, s3
	s_bfe_u32 s16, s2, 0x30003
	s_lshl_b32 s3, s4, 3
	s_or_b32 s3, s3, s16
	s_mov_b32 s11, 0
	s_lshr_b32 s10, s3, 1
	s_lshl_b64 s[10:11], s[10:11], 14
	s_add_u32 s3, s8, s10
	s_addc_u32 s8, s9, s11
	s_lshr_b32 s2, s2, 2
	s_and_b32 s2, s2, 2
	s_add_u32 s2, s3, s2
	v_mov_b32_e32 v3, 0
	v_lshlrev_b32_e32 v2, 2, v0
	s_addc_u32 s3, s8, 0
	s_movk_i32 s5, 0x1000
	v_lshl_add_u64 v[6:7], s[2:3], 0, v[2:3]
	v_add_co_u32_e32 v8, vcc, s5, v6
	s_movk_i32 s12, 0x2000
	s_nop 0
	v_addc_co_u32_e32 v9, vcc, 0, v7, vcc
	v_add_co_u32_e32 v10, vcc, s12, v6
	s_movk_i32 s13, 0x3000
	s_add_u32 s8, s2, 0x1000000
	v_addc_co_u32_e32 v11, vcc, 0, v7, vcc
	s_addc_u32 s9, s3, 0
	v_add_co_u32_e32 v6, vcc, s13, v6
	v_lshl_add_u64 v[12:13], s[8:9], 0, v[2:3]
	s_nop 0
	v_addc_co_u32_e32 v7, vcc, 0, v7, vcc
	v_add_co_u32_e32 v14, vcc, s5, v12
	v_lshlrev_b32_e32 v1, 3, v0
	s_nop 0
	v_addc_co_u32_e32 v15, vcc, 0, v13, vcc
	v_add_co_u32_e32 v16, vcc, s12, v12
	v_or_b32_e32 v19, 0x1000, v2
	s_nop 0
	v_addc_co_u32_e32 v17, vcc, 0, v13, vcc
	v_add_co_u32_e32 v12, vcc, s13, v12
	v_or_b32_e32 v20, 0x2000, v2
	v_or_b32_e32 v21, 0x3000, v2
	v_addc_co_u32_e32 v13, vcc, 0, v13, vcc
	v_mul_u32_u24_e32 v3, 3, v0
	s_movk_i32 s5, 0x888
	v_lshlrev_b32_e32 v3, 3, v3
	s_mov_b32 s10, 0x3ec3ef15
	s_mov_b32 s11, 0xbf6c835e
	s_mov_b32 s14, s11
	s_mov_b32 s15, s10
	s_mov_b32 s12, 0xbf3504f3
	s_mov_b32 s13, s12
	v_mov_b32_e32 v88, v0
	global_load_ushort v32, v2, s[2:3] nt
	global_load_ushort v33, v2, s[8:9] nt
	global_load_ushort v34, v2, s[2:3] offset:1024 nt
	global_load_ushort v35, v2, s[8:9] offset:1024 nt
	global_load_ushort v36, v2, s[2:3] offset:2048 nt
	global_load_ushort v37, v2, s[8:9] offset:2048 nt
	global_load_ushort v38, v2, s[8:9] offset:3072 nt
	global_load_ushort v39, v2, s[2:3] offset:3072 nt
	global_load_ushort v40, v19, s[2:3] nt
	global_load_ushort v41, v19, s[8:9] nt
	global_load_ushort v42, v[8:9], off offset:1024 nt
	global_load_ushort v43, v[14:15], off offset:1024 nt
	global_load_ushort v44, v[8:9], off offset:2048 nt
	global_load_ushort v45, v[14:15], off offset:2048 nt
	global_load_ushort v46, v[14:15], off offset:3072 nt
	global_load_ushort v47, v[8:9], off offset:3072 nt
	global_load_ushort v48, v20, s[2:3] nt
	global_load_ushort v49, v20, s[8:9] nt
	global_load_ushort v50, v[10:11], off offset:1024 nt
	global_load_ushort v51, v[16:17], off offset:1024 nt
	global_load_ushort v52, v[10:11], off offset:2048 nt
	global_load_ushort v53, v[16:17], off offset:2048 nt
	global_load_ushort v54, v[16:17], off offset:3072 nt
	global_load_ushort v55, v[10:11], off offset:3072 nt
	global_load_ushort v56, v21, s[2:3] nt
	global_load_ushort v57, v21, s[8:9] nt
	global_load_ushort v58, v[6:7], off offset:1024 nt
	global_load_ushort v59, v[12:13], off offset:1024 nt
	global_load_ushort v60, v[6:7], off offset:2048 nt
	global_load_ushort v61, v[12:13], off offset:2048 nt
	global_load_ushort v62, v[12:13], off offset:3072 nt
	global_load_ushort v63, v[6:7], off offset:3072 nt
	v_mul_u32_u24_e32 v5, 5, v0
	v_mul_u32_u24_e32 v6, 6, v0
	v_mul_u32_u24_e32 v7, 7, v0
	v_mul_u32_u24_e32 v9, 9, v0
	v_mul_u32_u24_e32 v10, 10, v0
	v_lshrrev_b32_e32 v16, 1, v0
	v_lshlrev_b32_e32 v2, 4, v0
	v_lshlrev_b32_e32 v4, 5, v0
	v_lshlrev_b32_e32 v8, 6, v0
	v_mul_u32_u24_e32 v11, 11, v0
	v_mul_u32_u24_e32 v12, 12, v0
	v_mul_u32_u24_e32 v13, 13, v0
	v_mul_u32_u24_e32 v14, 14, v0
	v_mul_u32_u24_e32 v15, 15, v0
	v_lshlrev_b32_e32 v5, 3, v5
	v_lshlrev_b32_e32 v6, 3, v6
	v_lshlrev_b32_e32 v7, 3, v7
	v_lshlrev_b32_e32 v9, 3, v9
	v_lshlrev_b32_e32 v64, 3, v10
	v_and_b32_e32 v10, 0x78, v16
	v_lshlrev_b32_e32 v65, 3, v11
	v_lshlrev_b32_e32 v66, 3, v12
	v_lshlrev_b32_e32 v67, 3, v13
	v_lshlrev_b32_e32 v68, 3, v14
	v_lshlrev_b32_e32 v69, 3, v15
	v_mad_u32_u24 v96, v18, s5, v10
	global_load_dwordx2 v[30:31], v1, s[6:7]
	global_load_dwordx2 v[28:29], v2, s[6:7]
	global_load_dwordx2 v[26:27], v3, s[6:7]
	global_load_dwordx2 v[24:25], v4, s[6:7]
	global_load_dwordx2 v[20:21], v5, s[6:7]
	global_load_dwordx2 v[16:17], v6, s[6:7]
	global_load_dwordx2 v[10:11], v7, s[6:7]
	global_load_dwordx2 v[22:23], v8, s[6:7]
	global_load_dwordx2 v[18:19], v9, s[6:7]
	global_load_dwordx2 v[12:13], v64, s[6:7]
	global_load_dwordx2 v[14:15], v65, s[6:7]
	s_nop 0
	global_load_dwordx2 v[6:7], v66, s[6:7]
	global_load_dwordx2 v[8:9], v67, s[6:7]
	global_load_dwordx2 v[4:5], v68, s[6:7]
	global_load_dwordx2 v[2:3], v69, s[6:7]
	s_mov_b32 s6, 0x3f6c835e
	s_mov_b32 s7, 0xbec3ef15
	s_mov_b32 s8, 0x3f3504f3
	s_mov_b32 s9, s8
	s_waitcnt vmcnt(45)
	v_lshl_or_b32 v85, v33, 16, v32
	v_cvt_f32_fp8_e32 v32, v85
	s_waitcnt vmcnt(43)
	v_lshl_or_b32 v84, v35, 16, v34
	v_cvt_f32_fp8_sdwa v33, v85 src0_sel:BYTE_2
	s_waitcnt vmcnt(41)
	v_lshl_or_b32 v83, v37, 16, v36
	v_cvt_f32_fp8_e32 v34, v84
	v_cvt_f32_fp8_sdwa v35, v84 src0_sel:BYTE_2
	s_waitcnt vmcnt(39)
	v_lshl_or_b32 v82, v38, 16, v39
	s_waitcnt vmcnt(37)
	v_lshl_or_b32 v81, v41, 16, v40
	v_cvt_f32_fp8_e32 v40, v81
	s_waitcnt vmcnt(35)
	v_lshl_or_b32 v80, v43, 16, v42
	v_cvt_f32_fp8_sdwa v41, v81 src0_sel:BYTE_2
	s_waitcnt vmcnt(33)
	v_lshl_or_b32 v79, v45, 16, v44
	v_cvt_f32_fp8_e32 v42, v80
	v_cvt_f32_fp8_sdwa v43, v80 src0_sel:BYTE_2
	v_cvt_f32_fp8_e32 v36, v83
	v_cvt_f32_fp8_sdwa v37, v83 src0_sel:BYTE_2
	s_waitcnt vmcnt(31)
	v_lshl_or_b32 v78, v46, 16, v47
	v_cvt_f32_fp8_e32 v44, v79
	s_waitcnt vmcnt(29)
	v_lshl_or_b32 v77, v49, 16, v48
	v_cvt_f32_fp8_e32 v48, v77
	s_waitcnt vmcnt(27)
	v_lshl_or_b32 v76, v51, 16, v50
	v_cvt_f32_fp8_sdwa v49, v77 src0_sel:BYTE_2
	s_waitcnt vmcnt(25)
	v_lshl_or_b32 v75, v53, 16, v52
	v_cvt_f32_fp8_e32 v50, v76
	v_cvt_f32_fp8_sdwa v51, v76 src0_sel:BYTE_2
	s_waitcnt vmcnt(23)
	v_lshl_or_b32 v74, v54, 16, v55
	s_waitcnt vmcnt(21)
	v_lshl_or_b32 v73, v57, 16, v56
	v_cvt_f32_fp8_e32 v56, v73
	s_waitcnt vmcnt(19)
	v_lshl_or_b32 v72, v59, 16, v58
	v_cvt_f32_fp8_sdwa v57, v73 src0_sel:BYTE_2
	s_waitcnt vmcnt(17)
	v_lshl_or_b32 v71, v61, 16, v60
	v_cvt_f32_fp8_e32 v58, v72
	v_cvt_f32_fp8_sdwa v59, v72 src0_sel:BYTE_2
	v_cvt_f32_fp8_sdwa v45, v79 src0_sel:BYTE_2
	v_cvt_f32_fp8_e32 v52, v75
	v_cvt_f32_fp8_sdwa v53, v75 src0_sel:BYTE_2
	v_cvt_f32_fp8_e32 v60, v71
	v_cvt_f32_fp8_sdwa v61, v71 src0_sel:BYTE_2
	s_waitcnt vmcnt(15)
	v_lshl_or_b32 v70, v62, 16, v63
	v_cvt_f32_fp8_e32 v38, v82
	v_cvt_f32_fp8_sdwa v39, v82 src0_sel:BYTE_2
	v_cvt_f32_fp8_e32 v46, v78
	v_cvt_f32_fp8_sdwa v47, v78 src0_sel:BYTE_2
	v_cvt_f32_fp8_e32 v54, v74
	v_cvt_f32_fp8_sdwa v55, v74 src0_sel:BYTE_2
	v_cvt_f32_fp8_e32 v62, v70
	v_cvt_f32_fp8_sdwa v63, v70 src0_sel:BYTE_2
	v_pk_add_f32 v[64:65], v[32:33], v[48:49]
	v_pk_add_f32 v[32:33], v[32:33], v[48:49] neg_lo:[0,1] neg_hi:[0,1]
	v_pk_add_f32 v[48:49], v[40:41], v[56:57]
	v_pk_add_f32 v[40:41], v[40:41], v[56:57] neg_lo:[0,1] neg_hi:[0,1]
	v_pk_add_f32 v[56:57], v[64:65], v[48:49]
	v_pk_add_f32 v[48:49], v[64:65], v[48:49] neg_lo:[0,1] neg_hi:[0,1]
	v_pk_add_f32 v[64:65], v[32:33], v[40:41] op_sel:[0,1] op_sel_hi:[1,0] neg_hi:[0,1]
	v_pk_add_f32 v[32:33], v[32:33], v[40:41] op_sel:[0,1] op_sel_hi:[1,0] neg_lo:[0,1]
	v_pk_add_f32 v[40:41], v[34:35], v[50:51]
	v_pk_add_f32 v[34:35], v[34:35], v[50:51] neg_lo:[0,1] neg_hi:[0,1]
	v_pk_add_f32 v[50:51], v[42:43], v[58:59]
	v_pk_add_f32 v[42:43], v[42:43], v[58:59] neg_lo:[0,1] neg_hi:[0,1]
	v_pk_add_f32 v[58:59], v[40:41], v[50:51]
	v_pk_add_f32 v[40:41], v[40:41], v[50:51] neg_lo:[0,1] neg_hi:[0,1]
	v_pk_add_f32 v[50:51], v[34:35], v[42:43] op_sel:[0,1] op_sel_hi:[1,0] neg_hi:[0,1]
	v_pk_add_f32 v[34:35], v[34:35], v[42:43] op_sel:[0,1] op_sel_hi:[1,0] neg_lo:[0,1]
	v_pk_add_f32 v[42:43], v[36:37], v[52:53]
	v_pk_add_f32 v[36:37], v[36:37], v[52:53] neg_lo:[0,1] neg_hi:[0,1]
	v_pk_add_f32 v[52:53], v[44:45], v[60:61]
	v_pk_add_f32 v[44:45], v[44:45], v[60:61] neg_lo:[0,1] neg_hi:[0,1]
	v_pk_add_f32 v[60:61], v[42:43], v[52:53]
	v_pk_add_f32 v[42:43], v[42:43], v[52:53] neg_lo:[0,1] neg_hi:[0,1]
	v_pk_add_f32 v[52:53], v[36:37], v[44:45] op_sel:[0,1] op_sel_hi:[1,0] neg_hi:[0,1]
	v_pk_add_f32 v[36:37], v[36:37], v[44:45] op_sel:[0,1] op_sel_hi:[1,0] neg_lo:[0,1]
	v_pk_add_f32 v[44:45], v[38:39], v[54:55]
	v_pk_add_f32 v[38:39], v[38:39], v[54:55] neg_lo:[0,1] neg_hi:[0,1]
	v_pk_add_f32 v[54:55], v[46:47], v[62:63]
	v_pk_add_f32 v[46:47], v[46:47], v[62:63] neg_lo:[0,1] neg_hi:[0,1]
	v_pk_add_f32 v[62:63], v[44:45], v[54:55]
	v_pk_add_f32 v[44:45], v[44:45], v[54:55] neg_lo:[0,1] neg_hi:[0,1]
	v_pk_add_f32 v[54:55], v[38:39], v[46:47] op_sel:[0,1] op_sel_hi:[1,0] neg_hi:[0,1]
	v_pk_add_f32 v[38:39], v[38:39], v[46:47] op_sel:[0,1] op_sel_hi:[1,0] neg_lo:[0,1]
	v_pk_mul_f32 v[46:47], v[50:51], s[6:7] op_sel:[0,0] op_sel_hi:[0,1]
	v_pk_fma_f32 v[46:47], v[50:51], s[6:7], v[46:47] op_sel:[1,1,0] op_sel_hi:[1,0,1] neg_lo:[0,1,0]
	v_pk_mul_f32 v[50:51], v[34:35], s[10:11] op_sel:[0,0] op_sel_hi:[0,1]
	v_pk_fma_f32 v[50:51], v[34:35], s[10:11], v[50:51] op_sel:[1,1,0] op_sel_hi:[1,0,1] neg_lo:[0,1,0]
	v_pk_add_f32 v[34:35], v[52:53], v[52:53] op_sel:[0,1] op_sel_hi:[1,0] neg_hi:[0,1]
	v_pk_add_f32 v[40:41], v[40:41], v[40:41] op_sel:[0,1] op_sel_hi:[1,0] neg_hi:[0,1]
	s_nop 0
	v_pk_mul_f32 v[52:53], v[54:55], s[10:11] op_sel:[0,0] op_sel_hi:[0,1]
	v_pk_fma_f32 v[52:53], v[54:55], s[10:11], v[52:53] op_sel:[1,1,0] op_sel_hi:[1,0,1] neg_lo:[0,1,0]
	v_pk_mul_f32 v[54:55], v[38:39], s[14:15] op_sel:[0,0] op_sel_hi:[0,1]
	v_pk_fma_f32 v[54:55], v[38:39], s[14:15], v[54:55] op_sel:[1,1,0] op_sel_hi:[1,0,1] neg_lo:[0,1,0]
	v_pk_add_f32 v[38:39], v[56:57], v[60:61]
	v_pk_mul_f32 v[34:35], v[34:35], s[8:9]
	v_pk_add_f32 v[56:57], v[56:57], v[60:61] neg_lo:[0,1] neg_hi:[0,1]
	v_pk_add_f32 v[60:61], v[58:59], v[62:63]
	v_pk_add_f32 v[58:59], v[58:59], v[62:63] neg_lo:[0,1] neg_hi:[0,1]
	v_pk_mul_f32 v[40:41], v[40:41], s[8:9]
	v_pk_add_f32 v[36:37], v[36:37], v[36:37] op_sel:[0,1] op_sel_hi:[1,0] neg_lo:[0,1]
	v_pk_add_f32 v[44:45], v[44:45], v[44:45] op_sel:[0,1] op_sel_hi:[1,0] neg_lo:[0,1]
	v_pk_add_f32 v[62:63], v[38:39], v[60:61]
	v_pk_add_f32 v[38:39], v[38:39], v[60:61] neg_lo:[0,1] neg_hi:[0,1]
	v_pk_add_f32 v[60:61], v[56:57], v[58:59] op_sel:[0,1] op_sel_hi:[1,0] neg_hi:[0,1]
	v_pk_add_f32 v[56:57], v[56:57], v[58:59] op_sel:[0,1] op_sel_hi:[1,0] neg_lo:[0,1]
	v_pk_add_f32 v[58:59], v[64:65], v[34:35]
	v_pk_add_f32 v[34:35], v[64:65], v[34:35] neg_lo:[0,1] neg_hi:[0,1]
	v_pk_add_f32 v[64:65], v[46:47], v[52:53]
	v_pk_add_f32 v[46:47], v[46:47], v[52:53] neg_lo:[0,1] neg_hi:[0,1]
	v_pk_mul_f32 v[36:37], v[36:37], s[12:13]
	v_pk_mul_f32 v[44:45], v[44:45], s[12:13]
	v_pk_add_f32 v[52:53], v[58:59], v[64:65]
	v_pk_add_f32 v[58:59], v[58:59], v[64:65] neg_lo:[0,1] neg_hi:[0,1]
	v_pk_add_f32 v[64:65], v[34:35], v[46:47] op_sel:[0,1] op_sel_hi:[1,0] neg_hi:[0,1]
	v_pk_add_f32 v[34:35], v[34:35], v[46:47] op_sel:[0,1] op_sel_hi:[1,0] neg_lo:[0,1]
	v_pk_add_f32 v[46:47], v[48:49], v[42:43] op_sel:[0,1] op_sel_hi:[1,0] neg_hi:[0,1]
	v_pk_add_f32 v[42:43], v[48:49], v[42:43] op_sel:[0,1] op_sel_hi:[1,0] neg_lo:[0,1]
	v_pk_add_f32 v[48:49], v[40:41], v[44:45]
	v_pk_add_f32 v[40:41], v[40:41], v[44:45] neg_lo:[0,1] neg_hi:[0,1]
	v_pk_add_f32 v[44:45], v[48:49], v[46:47]
	v_pk_add_f32 v[46:47], v[46:47], v[48:49] neg_lo:[0,1] neg_hi:[0,1]
	v_pk_add_f32 v[48:49], v[42:43], v[40:41] op_sel:[0,1] op_sel_hi:[1,0] neg_hi:[0,1]
	v_pk_add_f32 v[40:41], v[42:43], v[40:41] op_sel:[0,1] op_sel_hi:[1,0] neg_lo:[0,1]
	v_pk_add_f32 v[42:43], v[32:33], v[36:37]
	v_pk_add_f32 v[32:33], v[32:33], v[36:37] neg_lo:[0,1] neg_hi:[0,1]
	v_pk_add_f32 v[36:37], v[50:51], v[54:55]
	v_pk_add_f32 v[50:51], v[50:51], v[54:55] neg_lo:[0,1] neg_hi:[0,1]
	v_pk_add_f32 v[54:55], v[42:43], v[36:37]
	v_pk_add_f32 v[36:37], v[42:43], v[36:37] neg_lo:[0,1] neg_hi:[0,1]
	v_pk_add_f32 v[42:43], v[32:33], v[50:51] op_sel:[0,1] op_sel_hi:[1,0] neg_hi:[0,1]
	v_pk_add_f32 v[32:33], v[32:33], v[50:51] op_sel:[0,1] op_sel_hi:[1,0] neg_lo:[0,1]
	s_waitcnt vmcnt(14)
	v_pk_mul_f32 v[50:51], v[52:53], v[30:31] op_sel:[0,0] op_sel_hi:[0,1]
	v_pk_fma_f32 v[50:51], v[52:53], v[30:31], v[50:51] op_sel:[1,1,0] op_sel_hi:[1,0,1] neg_lo:[0,1,0]
	ds_write_b64 v1, v[50:51] offset:2184
	s_waitcnt vmcnt(13)
	v_pk_mul_f32 v[50:51], v[44:45], v[28:29] op_sel:[0,0] op_sel_hi:[0,1]
	v_pk_fma_f32 v[50:51], v[44:45], v[28:29], v[50:51] op_sel:[1,1,0] op_sel_hi:[1,0,1] neg_lo:[0,1,0]
	s_waitcnt vmcnt(12)
	v_pk_mul_f32 v[44:45], v[54:55], v[26:27] op_sel:[0,0] op_sel_hi:[0,1]
	v_pk_fma_f32 v[44:45], v[54:55], v[26:27], v[44:45] op_sel:[1,1,0] op_sel_hi:[1,0,1] neg_lo:[0,1,0]
	ds_write_b64 v1, v[44:45] offset:6552
	s_waitcnt vmcnt(11)
	v_pk_mul_f32 v[44:45], v[60:61], v[24:25] op_sel:[0,0] op_sel_hi:[0,1]
	v_pk_fma_f32 v[44:45], v[60:61], v[24:25], v[44:45] op_sel:[1,1,0] op_sel_hi:[1,0,1] neg_lo:[0,1,0]
	ds_write_b64 v1, v[44:45] offset:8736
	s_waitcnt vmcnt(10)
	v_pk_mul_f32 v[44:45], v[64:65], v[20:21] op_sel:[0,0] op_sel_hi:[0,1]
	v_pk_fma_f32 v[44:45], v[64:65], v[20:21], v[44:45] op_sel:[1,1,0] op_sel_hi:[1,0,1] neg_lo:[0,1,0]
	ds_write_b64 v1, v[44:45] offset:10920
	s_waitcnt vmcnt(9)
	v_pk_mul_f32 v[44:45], v[48:49], v[16:17] op_sel:[0,0] op_sel_hi:[0,1]
	v_pk_fma_f32 v[44:45], v[48:49], v[16:17], v[44:45] op_sel:[1,1,0] op_sel_hi:[1,0,1] neg_lo:[0,1,0]
	ds_write_b64 v1, v[44:45] offset:13104
	s_waitcnt vmcnt(8)
	v_pk_mul_f32 v[44:45], v[42:43], v[10:11] op_sel:[0,0] op_sel_hi:[0,1]
	v_pk_fma_f32 v[44:45], v[42:43], v[10:11], v[44:45] op_sel:[1,1,0] op_sel_hi:[1,0,1] neg_lo:[0,1,0]
	s_waitcnt vmcnt(7)
	v_pk_mul_f32 v[42:43], v[38:39], v[22:23] op_sel:[0,0] op_sel_hi:[0,1]
	v_pk_fma_f32 v[42:43], v[38:39], v[22:23], v[42:43] op_sel:[1,1,0] op_sel_hi:[1,0,1] neg_lo:[0,1,0]
	s_waitcnt vmcnt(6)
	v_pk_mul_f32 v[38:39], v[58:59], v[18:19] op_sel:[0,0] op_sel_hi:[0,1]
	v_pk_fma_f32 v[38:39], v[58:59], v[18:19], v[38:39] op_sel:[1,1,0] op_sel_hi:[1,0,1] neg_lo:[0,1,0]
	ds_write_b64 v1, v[38:39] offset:19656
	s_waitcnt vmcnt(5)
	v_pk_mul_f32 v[38:39], v[46:47], v[12:13] op_sel:[0,0] op_sel_hi:[0,1]
	v_pk_fma_f32 v[38:39], v[46:47], v[12:13], v[38:39] op_sel:[1,1,0] op_sel_hi:[1,0,1] neg_lo:[0,1,0]
	ds_write_b64 v1, v[38:39] offset:21840
	s_waitcnt vmcnt(4)
	v_pk_mul_f32 v[38:39], v[36:37], v[14:15] op_sel:[0,0] op_sel_hi:[0,1]
	v_pk_fma_f32 v[38:39], v[36:37], v[14:15], v[38:39] op_sel:[1,1,0] op_sel_hi:[1,0,1] neg_lo:[0,1,0]
	s_waitcnt vmcnt(3)
	v_pk_mul_f32 v[36:37], v[56:57], v[6:7] op_sel:[0,0] op_sel_hi:[0,1]
	v_pk_fma_f32 v[36:37], v[56:57], v[6:7], v[36:37] op_sel:[1,1,0] op_sel_hi:[1,0,1] neg_lo:[0,1,0]
	ds_write_b64 v1, v[36:37] offset:26208
	s_waitcnt vmcnt(2)
	v_pk_mul_f32 v[36:37], v[34:35], v[8:9] op_sel:[0,0] op_sel_hi:[0,1]
	v_pk_fma_f32 v[36:37], v[34:35], v[8:9], v[36:37] op_sel:[1,1,0] op_sel_hi:[1,0,1] neg_lo:[0,1,0]
	s_waitcnt vmcnt(1)
	v_pk_mul_f32 v[34:35], v[40:41], v[4:5] op_sel:[0,0] op_sel_hi:[0,1]
	v_pk_fma_f32 v[34:35], v[40:41], v[4:5], v[34:35] op_sel:[1,1,0] op_sel_hi:[1,0,1] neg_lo:[0,1,0]
	ds_write_b64 v1, v[34:35] offset:30576
	s_waitcnt vmcnt(0)
	v_pk_mul_f32 v[34:35], v[32:33], v[2:3] op_sel:[0,0] op_sel_hi:[0,1]
	v_pk_fma_f32 v[34:35], v[32:33], v[2:3], v[34:35] op_sel:[1,1,0] op_sel_hi:[1,0,1] neg_lo:[0,1,0]
	ds_write_b64 v1, v[62:63]
	ds_write_b64 v1, v[50:51] offset:4368
	ds_write_b64 v1, v[44:45] offset:15288
	ds_write_b64 v1, v[42:43] offset:17472
	ds_write_b64 v1, v[38:39] offset:24024
	ds_write_b64 v1, v[36:37] offset:28392
	ds_write_b64 v1, v[34:35] offset:32760
	ds_write_b64 v1, v[86:87] offset:34816
	s_waitcnt lgkmcnt(0)
	s_barrier
	ds_read2_b64 v[32:35], v96 offset1:16
	ds_read2_b64 v[36:39], v96 offset0:32 offset1:48
	ds_read2_b64 v[40:43], v96 offset0:64 offset1:80
	ds_read2_b64 v[44:47], v96 offset0:128 offset1:144
	ds_read2_b64 v[48:51], v96 offset0:96 offset1:112
	ds_read2_b64 v[52:55], v96 offset0:192 offset1:208
	ds_read2_b64 v[56:59], v96 offset0:160 offset1:176
	ds_read2_b64 v[60:63], v96 offset0:224 offset1:240
	s_waitcnt lgkmcnt(4)
	v_pk_add_f32 v[64:65], v[32:33], v[44:45]
	v_pk_add_f32 v[32:33], v[32:33], v[44:45] neg_lo:[0,1] neg_hi:[0,1]
	s_waitcnt lgkmcnt(2)
	v_pk_add_f32 v[44:45], v[40:41], v[52:53]
	v_pk_add_f32 v[40:41], v[40:41], v[52:53] neg_lo:[0,1] neg_hi:[0,1]
	v_pk_add_f32 v[52:53], v[64:65], v[44:45]
	v_pk_add_f32 v[44:45], v[64:65], v[44:45] neg_lo:[0,1] neg_hi:[0,1]
	v_pk_add_f32 v[64:65], v[32:33], v[40:41] op_sel:[0,1] op_sel_hi:[1,0] neg_hi:[0,1]
	v_pk_add_f32 v[32:33], v[32:33], v[40:41] op_sel:[0,1] op_sel_hi:[1,0] neg_lo:[0,1]
	v_pk_add_f32 v[40:41], v[34:35], v[46:47]
	v_pk_add_f32 v[34:35], v[34:35], v[46:47] neg_lo:[0,1] neg_hi:[0,1]
	v_pk_add_f32 v[46:47], v[42:43], v[54:55]
	v_pk_add_f32 v[42:43], v[42:43], v[54:55] neg_lo:[0,1] neg_hi:[0,1]
	v_pk_add_f32 v[54:55], v[40:41], v[46:47]
	v_pk_add_f32 v[40:41], v[40:41], v[46:47] neg_lo:[0,1] neg_hi:[0,1]
	v_pk_add_f32 v[46:47], v[34:35], v[42:43] op_sel:[0,1] op_sel_hi:[1,0] neg_hi:[0,1]
	v_pk_add_f32 v[34:35], v[34:35], v[42:43] op_sel:[0,1] op_sel_hi:[1,0] neg_lo:[0,1]
	s_waitcnt lgkmcnt(1)
	v_pk_add_f32 v[42:43], v[36:37], v[56:57]
	v_pk_add_f32 v[36:37], v[36:37], v[56:57] neg_lo:[0,1] neg_hi:[0,1]
	s_waitcnt lgkmcnt(0)
	v_pk_add_f32 v[56:57], v[48:49], v[60:61]
	v_pk_add_f32 v[48:49], v[48:49], v[60:61] neg_lo:[0,1] neg_hi:[0,1]
	v_pk_add_f32 v[60:61], v[42:43], v[56:57]
	v_pk_add_f32 v[42:43], v[42:43], v[56:57] neg_lo:[0,1] neg_hi:[0,1]
	v_pk_add_f32 v[56:57], v[36:37], v[48:49] op_sel:[0,1] op_sel_hi:[1,0] neg_hi:[0,1]
	v_pk_add_f32 v[36:37], v[36:37], v[48:49] op_sel:[0,1] op_sel_hi:[1,0] neg_lo:[0,1]
	v_pk_add_f32 v[48:49], v[38:39], v[58:59]
	v_pk_add_f32 v[38:39], v[38:39], v[58:59] neg_lo:[0,1] neg_hi:[0,1]
	v_pk_add_f32 v[58:59], v[50:51], v[62:63]
	v_pk_add_f32 v[50:51], v[50:51], v[62:63] neg_lo:[0,1] neg_hi:[0,1]
	v_pk_add_f32 v[62:63], v[48:49], v[58:59]
	v_pk_add_f32 v[48:49], v[48:49], v[58:59] neg_lo:[0,1] neg_hi:[0,1]
	v_pk_add_f32 v[58:59], v[38:39], v[50:51] op_sel:[0,1] op_sel_hi:[1,0] neg_hi:[0,1]
	v_pk_add_f32 v[38:39], v[38:39], v[50:51] op_sel:[0,1] op_sel_hi:[1,0] neg_lo:[0,1]
	v_pk_mul_f32 v[50:51], v[46:47], s[6:7] op_sel:[0,0] op_sel_hi:[0,1]
	v_pk_fma_f32 v[50:51], v[46:47], s[6:7], v[50:51] op_sel:[1,1,0] op_sel_hi:[1,0,1] neg_lo:[0,1,0]
	v_pk_mul_f32 v[46:47], v[34:35], s[10:11] op_sel:[0,0] op_sel_hi:[0,1]
	v_pk_fma_f32 v[46:47], v[34:35], s[10:11], v[46:47] op_sel:[1,1,0] op_sel_hi:[1,0,1] neg_lo:[0,1,0]
	v_pk_add_f32 v[34:35], v[56:57], v[56:57] op_sel:[0,1] op_sel_hi:[1,0] neg_hi:[0,1]
	v_pk_add_f32 v[40:41], v[40:41], v[40:41] op_sel:[0,1] op_sel_hi:[1,0] neg_hi:[0,1]
	s_nop 0
	v_pk_mul_f32 v[56:57], v[58:59], s[10:11] op_sel:[0,0] op_sel_hi:[0,1]
	v_pk_fma_f32 v[56:57], v[58:59], s[10:11], v[56:57] op_sel:[1,1,0] op_sel_hi:[1,0,1] neg_lo:[0,1,0]
	v_pk_mul_f32 v[58:59], v[38:39], s[14:15] op_sel:[0,0] op_sel_hi:[0,1]
	v_pk_fma_f32 v[58:59], v[38:39], s[14:15], v[58:59] op_sel:[1,1,0] op_sel_hi:[1,0,1] neg_lo:[0,1,0]
	v_pk_add_f32 v[38:39], v[52:53], v[60:61]
	v_pk_mul_f32 v[34:35], v[34:35], s[8:9]
	v_pk_add_f32 v[52:53], v[52:53], v[60:61] neg_lo:[0,1] neg_hi:[0,1]
	v_pk_add_f32 v[60:61], v[54:55], v[62:63]
	v_pk_add_f32 v[54:55], v[54:55], v[62:63] neg_lo:[0,1] neg_hi:[0,1]
	v_pk_add_f32 v[36:37], v[36:37], v[36:37] op_sel:[0,1] op_sel_hi:[1,0] neg_lo:[0,1]
	v_pk_add_f32 v[48:49], v[48:49], v[48:49] op_sel:[0,1] op_sel_hi:[1,0] neg_lo:[0,1]
	v_pk_add_f32 v[62:63], v[38:39], v[60:61]
	v_pk_add_f32 v[60:61], v[38:39], v[60:61] neg_lo:[0,1] neg_hi:[0,1]
	v_pk_add_f32 v[66:67], v[52:53], v[54:55] op_sel:[0,1] op_sel_hi:[1,0] neg_hi:[0,1]
	v_pk_add_f32 v[52:53], v[52:53], v[54:55] op_sel:[0,1] op_sel_hi:[1,0] neg_lo:[0,1]
	v_pk_add_f32 v[38:39], v[64:65], v[34:35]
	v_pk_add_f32 v[34:35], v[64:65], v[34:35] neg_lo:[0,1] neg_hi:[0,1]
	v_pk_add_f32 v[54:55], v[50:51], v[56:57]
	v_pk_add_f32 v[50:51], v[50:51], v[56:57] neg_lo:[0,1] neg_hi:[0,1]
	v_pk_mul_f32 v[40:41], v[40:41], s[8:9]
	v_pk_mul_f32 v[36:37], v[36:37], s[12:13]
	v_pk_mul_f32 v[48:49], v[48:49], s[12:13]
	v_pk_add_f32 v[56:57], v[38:39], v[54:55]
	v_pk_add_f32 v[54:55], v[38:39], v[54:55] neg_lo:[0,1] neg_hi:[0,1]
	v_pk_add_f32 v[64:65], v[34:35], v[50:51] op_sel:[0,1] op_sel_hi:[1,0] neg_hi:[0,1]
	v_pk_add_f32 v[50:51], v[34:35], v[50:51] op_sel:[0,1] op_sel_hi:[1,0] neg_lo:[0,1]
	v_pk_add_f32 v[34:35], v[44:45], v[42:43] op_sel:[0,1] op_sel_hi:[1,0] neg_hi:[0,1]
	v_pk_add_f32 v[38:39], v[44:45], v[42:43] op_sel:[0,1] op_sel_hi:[1,0] neg_lo:[0,1]
	v_pk_add_f32 v[42:43], v[40:41], v[48:49]
	v_pk_add_f32 v[40:41], v[40:41], v[48:49] neg_lo:[0,1] neg_hi:[0,1]
	v_pk_add_f32 v[44:45], v[42:43], v[34:35]
	v_pk_add_f32 v[42:43], v[34:35], v[42:43] neg_lo:[0,1] neg_hi:[0,1]
	v_pk_add_f32 v[34:35], v[32:33], v[36:37]
	v_pk_add_f32 v[36:37], v[32:33], v[36:37] neg_lo:[0,1] neg_hi:[0,1]
	v_pk_add_f32 v[32:33], v[46:47], v[58:59]
	v_pk_add_f32 v[48:49], v[38:39], v[40:41] op_sel:[0,1] op_sel_hi:[1,0] neg_hi:[0,1]
	v_pk_add_f32 v[40:41], v[38:39], v[40:41] op_sel:[0,1] op_sel_hi:[1,0] neg_lo:[0,1]
	v_pk_add_f32 v[38:39], v[46:47], v[58:59] neg_lo:[0,1] neg_hi:[0,1]
	v_pk_add_f32 v[46:47], v[34:35], v[32:33]
	v_pk_add_f32 v[58:59], v[34:35], v[32:33] neg_lo:[0,1] neg_hi:[0,1]
	v_pk_add_f32 v[68:69], v[36:37], v[38:39] op_sel:[0,1] op_sel_hi:[1,0] neg_hi:[0,1]
	v_pk_add_f32 v[86:87], v[36:37], v[38:39] op_sel:[0,1] op_sel_hi:[1,0] neg_lo:[0,1]
	s_nop 0
	v_ashrrev_i32_e32 v32, 4, v88
	v_lshlrev_b32_e32 v90, 3, v32
	v_add_u32_e32 v91, 0x8800, v90
	v_and_b32_e32 v36, 15, v88
	ds_read2_b64 v[32:35], v91 offset0:16 offset1:32
	v_mad_u32_u24 v92, v36, s5, v90
	ds_read2_b64 v[36:39], v91 offset0:48 offset1:64
	s_waitcnt lgkmcnt(1)
	v_pk_mul_f32 v[88:89], v[56:57], v[32:33] op_sel:[0,0] op_sel_hi:[0,1]
	v_pk_fma_f32 v[88:89], v[56:57], v[32:33], v[88:89] op_sel:[1,1,0] op_sel_hi:[1,0,1] neg_lo:[0,1,0]
	v_pk_mul_f32 v[56:57], v[44:45], v[34:35] op_sel:[0,0] op_sel_hi:[0,1]
	v_pk_fma_f32 v[56:57], v[44:45], v[34:35], v[56:57] op_sel:[1,1,0] op_sel_hi:[1,0,1] neg_lo:[0,1,0]
	s_waitcnt lgkmcnt(0)
	v_pk_mul_f32 v[44:45], v[46:47], v[36:37] op_sel:[0,0] op_sel_hi:[0,1]
	v_pk_fma_f32 v[44:45], v[46:47], v[36:37], v[44:45] op_sel:[1,1,0] op_sel_hi:[1,0,1] neg_lo:[0,1,0]
	ds_write2_b64 v92, v[56:57], v[44:45] offset0:32 offset1:48
	v_pk_mul_f32 v[44:45], v[66:67], v[38:39] op_sel:[0,0] op_sel_hi:[0,1]
	v_pk_fma_f32 v[44:45], v[66:67], v[38:39], v[44:45] op_sel:[1,1,0] op_sel_hi:[1,0,1] neg_lo:[0,1,0]
	ds_read2_b64 v[32:35], v91 offset0:80 offset1:96
	s_waitcnt lgkmcnt(0)
	v_pk_mul_f32 v[46:47], v[64:65], v[32:33] op_sel:[0,0] op_sel_hi:[0,1]
	v_pk_fma_f32 v[46:47], v[64:65], v[32:33], v[46:47] op_sel:[1,1,0] op_sel_hi:[1,0,1] neg_lo:[0,1,0]
	ds_write2_b64 v92, v[44:45], v[46:47] offset0:64 offset1:80
	v_pk_mul_f32 v[44:45], v[48:49], v[34:35] op_sel:[0,0] op_sel_hi:[0,1]
	v_pk_fma_f32 v[44:45], v[48:49], v[34:35], v[44:45] op_sel:[1,1,0] op_sel_hi:[1,0,1] neg_lo:[0,1,0]
	ds_read2_b64 v[36:39], v91 offset0:112 offset1:128
	ds_read2_b64 v[32:35], v91 offset0:144 offset1:160
	s_waitcnt lgkmcnt(1)
	v_pk_mul_f32 v[46:47], v[68:69], v[36:37] op_sel:[0,0] op_sel_hi:[0,1]
	v_pk_fma_f32 v[46:47], v[68:69], v[36:37], v[46:47] op_sel:[1,1,0] op_sel_hi:[1,0,1] neg_lo:[0,1,0]
	ds_write2_b64 v92, v[44:45], v[46:47] offset0:96 offset1:112
	v_pk_mul_f32 v[44:45], v[60:61], v[38:39] op_sel:[0,0] op_sel_hi:[0,1]
	v_pk_fma_f32 v[44:45], v[60:61], v[38:39], v[44:45] op_sel:[1,1,0] op_sel_hi:[1,0,1] neg_lo:[0,1,0]
	ds_read2_b64 v[36:39], v91 offset0:176 offset1:192
	s_waitcnt lgkmcnt(2)
	v_pk_mul_f32 v[46:47], v[54:55], v[32:33] op_sel:[0,0] op_sel_hi:[0,1]
	v_pk_fma_f32 v[46:47], v[54:55], v[32:33], v[46:47] op_sel:[1,1,0] op_sel_hi:[1,0,1] neg_lo:[0,1,0]
	ds_write2_b64 v92, v[44:45], v[46:47] offset0:128 offset1:144
	v_pk_mul_f32 v[44:45], v[42:43], v[34:35] op_sel:[0,0] op_sel_hi:[0,1]
	v_pk_fma_f32 v[44:45], v[42:43], v[34:35], v[44:45] op_sel:[1,1,0] op_sel_hi:[1,0,1] neg_lo:[0,1,0]
	ds_read2_b64 v[32:35], v91 offset0:208 offset1:224
	s_waitcnt lgkmcnt(2)
	v_pk_mul_f32 v[42:43], v[58:59], v[36:37] op_sel:[0,0] op_sel_hi:[0,1]
	v_pk_fma_f32 v[42:43], v[58:59], v[36:37], v[42:43] op_sel:[1,1,0] op_sel_hi:[1,0,1] neg_lo:[0,1,0]
	ds_write2_b64 v92, v[44:45], v[42:43] offset0:160 offset1:176
	v_pk_mul_f32 v[42:43], v[52:53], v[38:39] op_sel:[0,0] op_sel_hi:[0,1]
	v_pk_fma_f32 v[42:43], v[52:53], v[38:39], v[42:43] op_sel:[1,1,0] op_sel_hi:[1,0,1] neg_lo:[0,1,0]
	s_waitcnt lgkmcnt(1)
	v_pk_mul_f32 v[38:39], v[50:51], v[32:33] op_sel:[0,0] op_sel_hi:[0,1]
	v_pk_fma_f32 v[38:39], v[50:51], v[32:33], v[38:39] op_sel:[1,1,0] op_sel_hi:[1,0,1] neg_lo:[0,1,0]
	v_pk_mul_f32 v[32:33], v[40:41], v[34:35] op_sel:[0,0] op_sel_hi:[0,1]
	v_pk_fma_f32 v[32:33], v[40:41], v[34:35], v[32:33] op_sel:[1,1,0] op_sel_hi:[1,0,1] neg_lo:[0,1,0]
	ds_read_b64 v[36:37], v90 offset:36736
	s_waitcnt lgkmcnt(0)
	v_pk_mul_f32 v[34:35], v[86:87], v[36:37] op_sel:[0,0] op_sel_hi:[0,1]
	v_pk_fma_f32 v[34:35], v[86:87], v[36:37], v[34:35] op_sel:[1,1,0] op_sel_hi:[1,0,1] neg_lo:[0,1,0]
	ds_write2_b64 v92, v[32:33], v[34:35] offset0:224 offset1:240
	v_mov_b32_e32 v32, v0
	ds_write2_b64 v92, v[62:63], v[88:89] offset1:16
	ds_write2_b64 v92, v[42:43], v[38:39] offset0:192 offset1:208
	s_waitcnt lgkmcnt(0)
	s_barrier
	s_nop 0
	v_and_b32_e32 v33, 15, v32
	v_and_b32_e32 v32, 0x1ffffff0, v32
	v_lshlrev_b32_e32 v32, 3, v32
	v_mad_u32_u24 v60, v33, s5, v32
	ds_read2_b64 v[32:35], v60 offset1:1
	ds_read2_b64 v[36:39], v60 offset0:2 offset1:3
	ds_read2_b64 v[40:43], v60 offset0:8 offset1:9
	ds_read2_b64 v[44:47], v60 offset0:4 offset1:5
	ds_read2_b64 v[48:51], v60 offset0:6 offset1:7
	ds_read2_b64 v[52:55], v60 offset0:12 offset1:13
	ds_read2_b64 v[56:59], v60 offset0:10 offset1:11
	ds_read2_b64 v[60:63], v60 offset0:14 offset1:15
	s_waitcnt lgkmcnt(5)
	v_pk_add_f32 v[64:65], v[32:33], v[40:41]
	v_pk_add_f32 v[32:33], v[32:33], v[40:41] neg_lo:[0,1] neg_hi:[0,1]
	s_waitcnt lgkmcnt(2)
	v_pk_add_f32 v[40:41], v[44:45], v[52:53]
	v_pk_add_f32 v[44:45], v[44:45], v[52:53] neg_lo:[0,1] neg_hi:[0,1]
	v_pk_add_f32 v[52:53], v[64:65], v[40:41]
	v_pk_add_f32 v[40:41], v[64:65], v[40:41] neg_lo:[0,1] neg_hi:[0,1]
	v_pk_add_f32 v[64:65], v[32:33], v[44:45] op_sel:[0,1] op_sel_hi:[1,0] neg_hi:[0,1]
	v_pk_add_f32 v[66:67], v[32:33], v[44:45] op_sel:[0,1] op_sel_hi:[1,0] neg_lo:[0,1]
	v_pk_add_f32 v[32:33], v[34:35], v[42:43]
	v_pk_add_f32 v[34:35], v[34:35], v[42:43] neg_lo:[0,1] neg_hi:[0,1]
	v_pk_add_f32 v[42:43], v[46:47], v[54:55]
	v_pk_add_f32 v[44:45], v[46:47], v[54:55] neg_lo:[0,1] neg_hi:[0,1]
	v_pk_add_f32 v[46:47], v[32:33], v[42:43]
	v_pk_add_f32 v[32:33], v[32:33], v[42:43] neg_lo:[0,1] neg_hi:[0,1]
	v_pk_add_f32 v[42:43], v[34:35], v[44:45] op_sel:[0,1] op_sel_hi:[1,0] neg_hi:[0,1]
	v_pk_add_f32 v[34:35], v[34:35], v[44:45] op_sel:[0,1] op_sel_hi:[1,0] neg_lo:[0,1]
	s_waitcnt lgkmcnt(1)
	v_pk_add_f32 v[44:45], v[36:37], v[56:57]
	s_waitcnt lgkmcnt(0)
	v_pk_add_f32 v[54:55], v[48:49], v[60:61]
	v_pk_add_f32 v[32:33], v[32:33], v[32:33] op_sel:[0,1] op_sel_hi:[1,0] neg_hi:[0,1]
	v_pk_add_f32 v[36:37], v[36:37], v[56:57] neg_lo:[0,1] neg_hi:[0,1]
	v_pk_add_f32 v[48:49], v[48:49], v[60:61] neg_lo:[0,1] neg_hi:[0,1]
	v_pk_add_f32 v[56:57], v[44:45], v[54:55]
	v_pk_add_f32 v[54:55], v[44:45], v[54:55] neg_lo:[0,1] neg_hi:[0,1]
	v_pk_add_f32 v[44:45], v[36:37], v[48:49] op_sel:[0,1] op_sel_hi:[1,0] neg_hi:[0,1]
	v_pk_mul_f32 v[68:69], v[32:33], s[8:9]
	v_pk_add_f32 v[36:37], v[36:37], v[48:49] op_sel:[0,1] op_sel_hi:[1,0] neg_lo:[0,1]
	v_pk_add_f32 v[48:49], v[38:39], v[58:59]
	v_pk_add_f32 v[32:33], v[44:45], v[44:45] op_sel:[0,1] op_sel_hi:[1,0] neg_hi:[0,1]
	v_pk_add_f32 v[38:39], v[38:39], v[58:59] neg_lo:[0,1] neg_hi:[0,1]
	v_pk_add_f32 v[58:59], v[50:51], v[62:63]
	v_pk_mul_f32 v[86:87], v[34:35], s[10:11] op_sel:[0,0] op_sel_hi:[0,1]
	v_pk_fma_f32 v[86:87], v[34:35], s[10:11], v[86:87] op_sel:[1,1,0] op_sel_hi:[1,0,1] neg_lo:[0,1,0]
	v_pk_mul_f32 v[34:35], v[32:33], s[8:9]
	v_pk_add_f32 v[32:33], v[36:37], v[36:37] op_sel:[0,1] op_sel_hi:[1,0] neg_lo:[0,1]
	v_pk_add_f32 v[50:51], v[50:51], v[62:63] neg_lo:[0,1] neg_hi:[0,1]
	v_pk_add_f32 v[60:61], v[48:49], v[58:59]
	v_pk_add_f32 v[48:49], v[48:49], v[58:59] neg_lo:[0,1] neg_hi:[0,1]
	v_pk_add_f32 v[58:59], v[38:39], v[50:51] op_sel:[0,1] op_sel_hi:[1,0] neg_hi:[0,1]
	v_pk_add_f32 v[38:39], v[38:39], v[50:51] op_sel:[0,1] op_sel_hi:[1,0] neg_lo:[0,1]
	v_pk_mul_f32 v[88:89], v[32:33], s[12:13]
	v_pk_add_f32 v[36:37], v[46:47], v[60:61]
	v_pk_add_f32 v[32:33], v[48:49], v[48:49] op_sel:[0,1] op_sel_hi:[1,0] neg_lo:[0,1]
	v_pk_mul_f32 v[44:45], v[58:59], s[10:11] op_sel:[0,0] op_sel_hi:[0,1]
	v_pk_fma_f32 v[44:45], v[58:59], s[10:11], v[44:45] op_sel:[1,1,0] op_sel_hi:[1,0,1] neg_lo:[0,1,0]
	v_pk_mul_f32 v[58:59], v[38:39], s[14:15] op_sel:[0,0] op_sel_hi:[0,1]
	v_pk_fma_f32 v[58:59], v[38:39], s[14:15], v[58:59] op_sel:[1,1,0] op_sel_hi:[1,0,1] neg_lo:[0,1,0]
	v_pk_add_f32 v[38:39], v[52:53], v[56:57] neg_lo:[0,1] neg_hi:[0,1]
	v_pk_mul_f32 v[48:49], v[32:33], s[12:13]
	v_pk_add_f32 v[32:33], v[52:53], v[56:57]
	v_pk_add_f32 v[46:47], v[46:47], v[60:61] neg_lo:[0,1] neg_hi:[0,1]
	v_pk_mul_f32 v[62:63], v[42:43], s[6:7] op_sel:[0,0] op_sel_hi:[0,1]
	v_pk_fma_f32 v[62:63], v[42:43], s[6:7], v[62:63] op_sel:[1,1,0] op_sel_hi:[1,0,1] neg_lo:[0,1,0]
	v_pk_add_f32 v[50:51], v[32:33], v[36:37]
	v_pk_add_f32 v[36:37], v[32:33], v[36:37] neg_lo:[0,1] neg_hi:[0,1]
	v_pk_add_f32 v[42:43], v[38:39], v[46:47] op_sel:[0,1] op_sel_hi:[1,0] neg_hi:[0,1]
	v_pk_add_f32 v[32:33], v[38:39], v[46:47] op_sel:[0,1] op_sel_hi:[1,0] neg_lo:[0,1]
	v_pk_add_f32 v[38:39], v[64:65], v[34:35]
	v_pk_add_f32 v[34:35], v[64:65], v[34:35] neg_lo:[0,1] neg_hi:[0,1]
	v_pk_add_f32 v[46:47], v[62:63], v[44:45]
	v_pk_add_f32 v[56:57], v[62:63], v[44:45] neg_lo:[0,1] neg_hi:[0,1]
	v_pk_add_f32 v[52:53], v[38:39], v[46:47]
	v_pk_add_f32 v[38:39], v[38:39], v[46:47] neg_lo:[0,1] neg_hi:[0,1]
	v_pk_add_f32 v[44:45], v[34:35], v[56:57] op_sel:[0,1] op_sel_hi:[1,0] neg_hi:[0,1]
	v_pk_add_f32 v[34:35], v[34:35], v[56:57] op_sel:[0,1] op_sel_hi:[1,0] neg_lo:[0,1]
	v_pk_add_f32 v[46:47], v[40:41], v[54:55] op_sel:[0,1] op_sel_hi:[1,0] neg_hi:[0,1]
	v_pk_add_f32 v[56:57], v[40:41], v[54:55] op_sel:[0,1] op_sel_hi:[1,0] neg_lo:[0,1]
	v_pk_add_f32 v[40:41], v[68:69], v[48:49]
	v_pk_add_f32 v[60:61], v[68:69], v[48:49] neg_lo:[0,1] neg_hi:[0,1]
	v_pk_add_f32 v[54:55], v[40:41], v[46:47]
	v_pk_add_f32 v[40:41], v[46:47], v[40:41] neg_lo:[0,1] neg_hi:[0,1]
	v_pk_add_f32 v[46:47], v[66:67], v[88:89]
	v_pk_add_f32 v[62:63], v[86:87], v[58:59]
	v_pk_add_f32 v[58:59], v[86:87], v[58:59] neg_lo:[0,1] neg_hi:[0,1]
	v_pk_add_f32 v[48:49], v[56:57], v[60:61] op_sel:[0,1] op_sel_hi:[1,0] neg_hi:[0,1]
	v_pk_add_f32 v[64:65], v[56:57], v[60:61] op_sel:[0,1] op_sel_hi:[1,0] neg_lo:[0,1]
	v_pk_add_f32 v[60:61], v[66:67], v[88:89] neg_lo:[0,1] neg_hi:[0,1]
	v_pk_add_f32 v[56:57], v[46:47], v[62:63]
	v_pk_add_f32 v[68:69], v[46:47], v[62:63] neg_lo:[0,1] neg_hi:[0,1]
	v_pk_add_f32 v[46:47], v[60:61], v[58:59] op_sel:[0,1] op_sel_hi:[1,0] neg_hi:[0,1]
	v_pk_add_f32 v[66:67], v[60:61], v[58:59] op_sel:[0,1] op_sel_hi:[1,0] neg_lo:[0,1]
	v_mov_b32_e32 v58, v0
	s_nop 0
	v_and_b32_e32 v59, -16, v58
	v_and_b32_e32 v60, 15, v58
	v_lshlrev_b32_e32 v61, 3, v59
	v_mad_u32_u24 v61, v60, s5, v61
	v_cmp_ne_u32_e32 vcc, 0, v60
	ds_write2_b64 v61, v[50:51], v[52:53] offset1:1
	ds_write2_b64 v61, v[54:55], v[56:57] offset0:2 offset1:3
	ds_write2_b64 v61, v[42:43], v[44:45] offset0:4 offset1:5
	ds_write2_b64 v61, v[48:49], v[46:47] offset0:6 offset1:7
	ds_write2_b64 v61, v[36:37], v[38:39] offset0:8 offset1:9
	ds_write2_b64 v61, v[40:41], v[68:69] offset0:10 offset1:11
	ds_write2_b64 v61, v[32:33], v[34:35] offset0:12 offset1:13
	ds_write2_b64 v61, v[64:65], v[66:67] offset0:14 offset1:15
	s_waitcnt lgkmcnt(0)
	s_barrier
	s_and_saveexec_b64 s[6:7], vcc
	s_xor_b64 s[6:7], exec, s[6:7]
	v_sub_u32_e32 v60, 16, v60
	v_mul_u32_u24_e32 v60, 0x111, v60
	v_sub_u32_e32 v59, v60, v59
	v_add_u32_e32 v61, 0xf0, v59
	s_andn2_saveexec_b64 s[6:7], s[6:7]
	v_sub_u32_e32 v59, 0x100, v58
	v_cmp_lt_u32_e32 vcc, 15, v58
	s_nop 1
	v_cndmask_b32_e32 v61, 1, v59, vcc
	s_or_b64 exec, exec, s[6:7]
	v_mov_b32_e32 v59, 0
	v_lshlrev_b32_e32 v92, 3, v61
	ds_read_b64 v[90:91], v59
	ds_read2_b64 v[60:63], v92 offset0:14 offset1:15
	ds_read2_b64 v[86:89], v92 offset0:12 offset1:13
	v_cmp_eq_u32_e32 vcc, 0, v58
	v_cvt_f32_fp8_sdwa v93, v74 src0_sel:BYTE_3
	v_cvt_f32_fp8_sdwa v94, v72 src0_sel:BYTE_1
	s_waitcnt lgkmcnt(1)
	v_cndmask_b32_e32 v59, v63, v91, vcc
	v_cndmask_b32_e32 v58, v62, v90, vcc
	v_pk_add_f32 v[90:91], v[50:51], v[58:59] neg_hi:[0,1]
	v_pk_add_f32 v[50:51], v[50:51], v[58:59] neg_lo:[0,1]
	v_cvt_f32_fp8_sdwa v95, v72 src0_sel:BYTE_3
	v_pk_mul_f32 v[62:63], v[90:91], v[50:51] op_sel:[0,0] op_sel_hi:[0,1]
	v_pk_fma_f32 v[62:63], v[90:91], v[50:51], v[62:63] op_sel:[1,1,0] op_sel_hi:[1,0,1] neg_hi:[0,1,0]
	v_pk_add_f32 v[50:51], v[52:53], v[60:61] neg_hi:[0,1]
	v_pk_add_f32 v[52:53], v[52:53], v[60:61] neg_lo:[0,1]
	v_cvt_f32_fp8_sdwa v72, v71 src0_sel:BYTE_1
	v_pk_mul_f32 v[60:61], v[50:51], v[52:53] op_sel:[0,0] op_sel_hi:[0,1]
	v_pk_fma_f32 v[60:61], v[50:51], v[52:53], v[60:61] op_sel:[1,1,0] op_sel_hi:[1,0,1] neg_hi:[0,1,0]
	s_waitcnt lgkmcnt(0)
	v_pk_add_f32 v[50:51], v[54:55], v[88:89] neg_hi:[0,1]
	v_pk_add_f32 v[52:53], v[54:55], v[88:89] neg_lo:[0,1]
	v_pk_add_f32 v[54:55], v[56:57], v[86:87] neg_hi:[0,1]
	v_pk_add_f32 v[86:87], v[56:57], v[86:87] neg_lo:[0,1]
	v_cvt_f32_fp8_sdwa v98, v70 src0_sel:BYTE_1
	v_pk_mul_f32 v[58:59], v[50:51], v[52:53] op_sel:[0,0] op_sel_hi:[0,1]
	v_pk_fma_f32 v[58:59], v[50:51], v[52:53], v[58:59] op_sel:[1,1,0] op_sel_hi:[1,0,1] neg_hi:[0,1,0]
	ds_read2_b64 v[50:53], v92 offset0:10 offset1:11
	v_pk_mul_f32 v[56:57], v[54:55], v[86:87] op_sel:[0,0] op_sel_hi:[0,1]
	v_pk_fma_f32 v[56:57], v[54:55], v[86:87], v[56:57] op_sel:[1,1,0] op_sel_hi:[1,0,1] neg_hi:[0,1,0]
	ds_read2_b64 v[86:89], v92 offset0:8 offset1:9
	s_waitcnt lgkmcnt(1)
	v_pk_add_f32 v[90:91], v[42:43], v[52:53] neg_hi:[0,1]
	v_pk_add_f32 v[42:43], v[42:43], v[52:53] neg_lo:[0,1]
	v_cvt_f32_fp8_sdwa v99, v70 src0_sel:BYTE_3
	v_pk_mul_f32 v[54:55], v[90:91], v[42:43] op_sel:[0,0] op_sel_hi:[0,1]
	v_pk_fma_f32 v[54:55], v[90:91], v[42:43], v[54:55] op_sel:[1,1,0] op_sel_hi:[1,0,1] neg_hi:[0,1,0]
	v_pk_add_f32 v[42:43], v[44:45], v[50:51] neg_hi:[0,1]
	v_pk_add_f32 v[44:45], v[44:45], v[50:51] neg_lo:[0,1]
	s_mov_b32 s6, 0x3f6c835e
	v_pk_mul_f32 v[52:53], v[42:43], v[44:45] op_sel:[0,0] op_sel_hi:[0,1]
	v_pk_fma_f32 v[52:53], v[42:43], v[44:45], v[52:53] op_sel:[1,1,0] op_sel_hi:[1,0,1] neg_hi:[0,1,0]
	s_waitcnt lgkmcnt(0)
	v_pk_add_f32 v[42:43], v[48:49], v[88:89] neg_hi:[0,1]
	v_pk_add_f32 v[44:45], v[48:49], v[88:89] neg_lo:[0,1]
	v_pk_add_f32 v[88:89], v[46:47], v[86:87] neg_hi:[0,1]
	v_pk_add_f32 v[46:47], v[46:47], v[86:87] neg_lo:[0,1]
	s_mov_b32 s7, 0xbec3ef15
	v_pk_mul_f32 v[50:51], v[42:43], v[44:45] op_sel:[0,0] op_sel_hi:[0,1]
	v_pk_fma_f32 v[50:51], v[42:43], v[44:45], v[50:51] op_sel:[1,1,0] op_sel_hi:[1,0,1] neg_hi:[0,1,0]
	ds_read2_b64 v[42:45], v92 offset0:6 offset1:7
	v_pk_mul_f32 v[48:49], v[88:89], v[46:47] op_sel:[0,0] op_sel_hi:[0,1]
	v_pk_fma_f32 v[48:49], v[88:89], v[46:47], v[48:49] op_sel:[1,1,0] op_sel_hi:[1,0,1] neg_hi:[0,1,0]
	ds_read2_b64 v[86:89], v92 offset0:4 offset1:5
	s_waitcnt lgkmcnt(1)
	v_pk_add_f32 v[90:91], v[36:37], v[44:45] neg_hi:[0,1]
	v_pk_add_f32 v[36:37], v[36:37], v[44:45] neg_lo:[0,1]
	s_mov_b32 s9, s8
	v_pk_mul_f32 v[46:47], v[90:91], v[36:37] op_sel:[0,0] op_sel_hi:[0,1]
	v_pk_fma_f32 v[46:47], v[90:91], v[36:37], v[46:47] op_sel:[1,1,0] op_sel_hi:[1,0,1] neg_hi:[0,1,0]
	v_pk_add_f32 v[36:37], v[38:39], v[42:43] neg_hi:[0,1]
	v_pk_add_f32 v[38:39], v[38:39], v[42:43] neg_lo:[0,1]
	v_cvt_f32_fp8_sdwa v90, v76 src0_sel:BYTE_1
	v_pk_mul_f32 v[44:45], v[36:37], v[38:39] op_sel:[0,0] op_sel_hi:[0,1]
	v_pk_fma_f32 v[44:45], v[36:37], v[38:39], v[44:45] op_sel:[1,1,0] op_sel_hi:[1,0,1] neg_hi:[0,1,0]
	s_waitcnt lgkmcnt(0)
	v_pk_add_f32 v[36:37], v[40:41], v[88:89] neg_hi:[0,1]
	v_pk_add_f32 v[38:39], v[40:41], v[88:89] neg_lo:[0,1]
	v_pk_add_f32 v[88:89], v[68:69], v[86:87] neg_hi:[0,1]
	v_pk_add_f32 v[68:69], v[68:69], v[86:87] neg_lo:[0,1]
	v_cvt_f32_fp8_sdwa v91, v76 src0_sel:BYTE_3
	v_pk_mul_f32 v[42:43], v[36:37], v[38:39] op_sel:[0,0] op_sel_hi:[0,1]
	v_pk_fma_f32 v[42:43], v[36:37], v[38:39], v[42:43] op_sel:[1,1,0] op_sel_hi:[1,0,1] neg_hi:[0,1,0]
	ds_read2_b64 v[36:39], v92 offset0:2 offset1:3
	v_pk_mul_f32 v[40:41], v[88:89], v[68:69] op_sel:[0,0] op_sel_hi:[0,1]
	v_pk_fma_f32 v[40:41], v[88:89], v[68:69], v[40:41] op_sel:[1,1,0] op_sel_hi:[1,0,1] neg_hi:[0,1,0]
	ds_read2_b64 v[86:89], v92 offset1:1
	s_waitcnt lgkmcnt(1)
	v_pk_add_f32 v[68:69], v[32:33], v[38:39] neg_hi:[0,1]
	v_pk_add_f32 v[32:33], v[32:33], v[38:39] neg_lo:[0,1]
	v_cvt_f32_fp8_sdwa v76, v75 src0_sel:BYTE_1
	v_pk_mul_f32 v[38:39], v[68:69], v[32:33] op_sel:[0,0] op_sel_hi:[0,1]
	v_pk_fma_f32 v[38:39], v[68:69], v[32:33], v[38:39] op_sel:[1,1,0] op_sel_hi:[1,0,1] neg_hi:[0,1,0]
	v_pk_add_f32 v[32:33], v[34:35], v[36:37] neg_hi:[0,1]
	v_pk_add_f32 v[34:35], v[34:35], v[36:37] neg_lo:[0,1]
	v_cvt_f32_fp8_sdwa v68, v83 src0_sel:BYTE_1
	v_pk_mul_f32 v[36:37], v[32:33], v[34:35] op_sel:[0,0] op_sel_hi:[0,1]
	v_pk_fma_f32 v[36:37], v[32:33], v[34:35], v[36:37] op_sel:[1,1,0] op_sel_hi:[1,0,1] neg_hi:[0,1,0]
	s_waitcnt lgkmcnt(0)
	v_pk_add_f32 v[32:33], v[64:65], v[88:89] neg_hi:[0,1]
	v_pk_add_f32 v[64:65], v[64:65], v[88:89] neg_lo:[0,1]
	v_cvt_f32_fp8_sdwa v69, v83 src0_sel:BYTE_3
	v_pk_mul_f32 v[34:35], v[32:33], v[64:65] op_sel:[0,0] op_sel_hi:[0,1]
	v_pk_fma_f32 v[34:35], v[32:33], v[64:65], v[34:35] op_sel:[1,1,0] op_sel_hi:[1,0,1] neg_hi:[0,1,0]
	v_pk_add_f32 v[64:65], v[66:67], v[86:87] neg_hi:[0,1]
	v_pk_add_f32 v[66:67], v[66:67], v[86:87] neg_lo:[0,1]
	v_cvt_f32_fp8_sdwa v83, v81 src0_sel:BYTE_3
	v_pk_mul_f32 v[32:33], v[64:65], v[66:67] op_sel:[0,0] op_sel_hi:[0,1]
	v_pk_fma_f32 v[32:33], v[64:65], v[66:67], v[32:33] op_sel:[1,1,0] op_sel_hi:[1,0,1] neg_hi:[0,1,0]
	v_cvt_f32_fp8_sdwa v64, v85 src0_sel:BYTE_1
	v_cvt_f32_fp8_sdwa v65, v85 src0_sel:BYTE_3
	v_cvt_f32_fp8_sdwa v66, v84 src0_sel:BYTE_1
	v_cvt_f32_fp8_sdwa v67, v84 src0_sel:BYTE_3
	v_cvt_f32_fp8_sdwa v84, v82 src0_sel:BYTE_1
	v_cvt_f32_fp8_sdwa v85, v82 src0_sel:BYTE_3
	v_cvt_f32_fp8_sdwa v82, v81 src0_sel:BYTE_1
	v_cvt_f32_fp8_sdwa v86, v80 src0_sel:BYTE_1
	v_cvt_f32_fp8_sdwa v87, v80 src0_sel:BYTE_3
	v_cvt_f32_fp8_sdwa v80, v79 src0_sel:BYTE_1
	v_cvt_f32_fp8_sdwa v81, v79 src0_sel:BYTE_3
	v_cvt_f32_fp8_sdwa v88, v78 src0_sel:BYTE_1
	v_cvt_f32_fp8_sdwa v89, v78 src0_sel:BYTE_3
	v_cvt_f32_fp8_sdwa v78, v77 src0_sel:BYTE_1
	v_cvt_f32_fp8_sdwa v79, v77 src0_sel:BYTE_3
	v_cvt_f32_fp8_sdwa v77, v75 src0_sel:BYTE_3
	v_cvt_f32_fp8_sdwa v92, v74 src0_sel:BYTE_1
	v_cvt_f32_fp8_sdwa v74, v73 src0_sel:BYTE_1
	v_cvt_f32_fp8_sdwa v75, v73 src0_sel:BYTE_3
	v_cvt_f32_fp8_sdwa v73, v71 src0_sel:BYTE_3
	v_pk_add_f32 v[70:71], v[64:65], v[78:79]
	v_pk_add_f32 v[64:65], v[64:65], v[78:79] neg_lo:[0,1] neg_hi:[0,1]
	v_pk_add_f32 v[78:79], v[82:83], v[74:75]
	v_pk_add_f32 v[74:75], v[82:83], v[74:75] neg_lo:[0,1] neg_hi:[0,1]
	v_pk_add_f32 v[82:83], v[70:71], v[78:79]
	v_pk_add_f32 v[70:71], v[70:71], v[78:79] neg_lo:[0,1] neg_hi:[0,1]
	v_pk_add_f32 v[78:79], v[64:65], v[74:75] op_sel:[0,1] op_sel_hi:[1,0] neg_hi:[0,1]
	v_pk_add_f32 v[64:65], v[64:65], v[74:75] op_sel:[0,1] op_sel_hi:[1,0] neg_lo:[0,1]
	v_pk_add_f32 v[74:75], v[66:67], v[90:91]
	v_pk_add_f32 v[66:67], v[66:67], v[90:91] neg_lo:[0,1] neg_hi:[0,1]
	v_pk_add_f32 v[90:91], v[86:87], v[94:95]
	v_pk_add_f32 v[86:87], v[86:87], v[94:95] neg_lo:[0,1] neg_hi:[0,1]
	v_pk_add_f32 v[94:95], v[74:75], v[90:91]
	v_pk_add_f32 v[74:75], v[74:75], v[90:91] neg_lo:[0,1] neg_hi:[0,1]
	v_pk_add_f32 v[90:91], v[66:67], v[86:87] op_sel:[0,1] op_sel_hi:[1,0] neg_hi:[0,1]
	v_pk_add_f32 v[66:67], v[66:67], v[86:87] op_sel:[0,1] op_sel_hi:[1,0] neg_lo:[0,1]
	v_pk_add_f32 v[86:87], v[68:69], v[76:77]
	v_pk_add_f32 v[68:69], v[68:69], v[76:77] neg_lo:[0,1] neg_hi:[0,1]
	v_pk_add_f32 v[76:77], v[80:81], v[72:73]
	v_pk_add_f32 v[72:73], v[80:81], v[72:73] neg_lo:[0,1] neg_hi:[0,1]
	v_pk_add_f32 v[80:81], v[86:87], v[76:77]
	v_pk_add_f32 v[76:77], v[86:87], v[76:77] neg_lo:[0,1] neg_hi:[0,1]
	v_pk_add_f32 v[86:87], v[68:69], v[72:73] op_sel:[0,1] op_sel_hi:[1,0] neg_hi:[0,1]
	v_pk_add_f32 v[68:69], v[68:69], v[72:73] op_sel:[0,1] op_sel_hi:[1,0] neg_lo:[0,1]
	v_pk_add_f32 v[72:73], v[84:85], v[92:93]
	v_pk_add_f32 v[84:85], v[84:85], v[92:93] neg_lo:[0,1] neg_hi:[0,1]
	v_pk_add_f32 v[92:93], v[88:89], v[98:99]
	v_pk_add_f32 v[88:89], v[88:89], v[98:99] neg_lo:[0,1] neg_hi:[0,1]
	v_pk_add_f32 v[98:99], v[72:73], v[92:93]
	v_pk_add_f32 v[72:73], v[72:73], v[92:93] neg_lo:[0,1] neg_hi:[0,1]
	v_pk_add_f32 v[92:93], v[84:85], v[88:89] op_sel:[0,1] op_sel_hi:[1,0] neg_hi:[0,1]
	v_pk_add_f32 v[84:85], v[84:85], v[88:89] op_sel:[0,1] op_sel_hi:[1,0] neg_lo:[0,1]
	v_pk_mul_f32 v[88:89], v[90:91], s[6:7] op_sel:[0,0] op_sel_hi:[0,1]
	v_pk_fma_f32 v[88:89], v[90:91], s[6:7], v[88:89] op_sel:[1,1,0] op_sel_hi:[1,0,1] neg_lo:[0,1,0]
	v_pk_mul_f32 v[90:91], v[66:67], s[10:11] op_sel:[0,0] op_sel_hi:[0,1]
	v_pk_fma_f32 v[90:91], v[66:67], s[10:11], v[90:91] op_sel:[1,1,0] op_sel_hi:[1,0,1] neg_lo:[0,1,0]
	v_pk_add_f32 v[66:67], v[86:87], v[86:87] op_sel:[0,1] op_sel_hi:[1,0] neg_hi:[0,1]
	s_nop 0
	v_pk_add_f32 v[72:73], v[72:73], v[72:73] op_sel:[0,1] op_sel_hi:[1,0] neg_lo:[0,1]
	v_pk_mul_f32 v[86:87], v[92:93], s[10:11] op_sel:[0,0] op_sel_hi:[0,1]
	v_pk_fma_f32 v[86:87], v[92:93], s[10:11], v[86:87] op_sel:[1,1,0] op_sel_hi:[1,0,1] neg_lo:[0,1,0]
	s_mov_b32 s14, s11
	v_pk_mul_f32 v[66:67], v[66:67], s[8:9]
	s_mov_b32 s15, s10
	v_pk_mul_f32 v[92:93], v[84:85], s[14:15] op_sel:[0,0] op_sel_hi:[0,1]
	v_pk_fma_f32 v[92:93], v[84:85], s[14:15], v[92:93] op_sel:[1,1,0] op_sel_hi:[1,0,1] neg_lo:[0,1,0]
	v_pk_add_f32 v[84:85], v[82:83], v[80:81]
	v_pk_add_f32 v[80:81], v[82:83], v[80:81] neg_lo:[0,1] neg_hi:[0,1]
	v_pk_add_f32 v[82:83], v[94:95], v[98:99]
	v_pk_add_f32 v[94:95], v[94:95], v[98:99] neg_lo:[0,1] neg_hi:[0,1]
	v_pk_add_f32 v[74:75], v[74:75], v[74:75] op_sel:[0,1] op_sel_hi:[1,0] neg_hi:[0,1]
	v_pk_add_f32 v[68:69], v[68:69], v[68:69] op_sel:[0,1] op_sel_hi:[1,0] neg_lo:[0,1]
	s_mov_b32 s13, s12
	v_pk_mul_f32 v[72:73], v[72:73], s[12:13]
	v_pk_add_f32 v[98:99], v[84:85], v[82:83]
	v_pk_add_f32 v[82:83], v[84:85], v[82:83] neg_lo:[0,1] neg_hi:[0,1]
	v_pk_add_f32 v[84:85], v[80:81], v[94:95] op_sel:[0,1] op_sel_hi:[1,0] neg_hi:[0,1]
	v_pk_add_f32 v[80:81], v[80:81], v[94:95] op_sel:[0,1] op_sel_hi:[1,0] neg_lo:[0,1]
	v_pk_add_f32 v[94:95], v[78:79], v[66:67]
	v_pk_add_f32 v[66:67], v[78:79], v[66:67] neg_lo:[0,1] neg_hi:[0,1]
	v_pk_add_f32 v[78:79], v[88:89], v[86:87]
	v_pk_add_f32 v[86:87], v[88:89], v[86:87] neg_lo:[0,1] neg_hi:[0,1]
	v_pk_mul_f32 v[74:75], v[74:75], s[8:9]
	v_pk_mul_f32 v[68:69], v[68:69], s[12:13]
	v_pk_add_f32 v[88:89], v[94:95], v[78:79]
	v_pk_add_f32 v[78:79], v[94:95], v[78:79] neg_lo:[0,1] neg_hi:[0,1]
	v_pk_add_f32 v[94:95], v[66:67], v[86:87] op_sel:[0,1] op_sel_hi:[1,0] neg_hi:[0,1]
	v_pk_add_f32 v[66:67], v[66:67], v[86:87] op_sel:[0,1] op_sel_hi:[1,0] neg_lo:[0,1]
	v_pk_add_f32 v[86:87], v[70:71], v[76:77] op_sel:[0,1] op_sel_hi:[1,0] neg_hi:[0,1]
	v_pk_add_f32 v[70:71], v[70:71], v[76:77] op_sel:[0,1] op_sel_hi:[1,0] neg_lo:[0,1]
	v_pk_add_f32 v[76:77], v[74:75], v[72:73]
	v_pk_add_f32 v[72:73], v[74:75], v[72:73] neg_lo:[0,1] neg_hi:[0,1]
	v_pk_add_f32 v[74:75], v[76:77], v[86:87]
	v_pk_add_f32 v[76:77], v[86:87], v[76:77] neg_lo:[0,1] neg_hi:[0,1]
	v_pk_add_f32 v[86:87], v[70:71], v[72:73] op_sel:[0,1] op_sel_hi:[1,0] neg_hi:[0,1]
	v_pk_add_f32 v[70:71], v[70:71], v[72:73] op_sel:[0,1] op_sel_hi:[1,0] neg_lo:[0,1]
	v_pk_add_f32 v[72:73], v[64:65], v[68:69]
	v_pk_add_f32 v[64:65], v[64:65], v[68:69] neg_lo:[0,1] neg_hi:[0,1]
	v_pk_add_f32 v[68:69], v[90:91], v[92:93]
	v_pk_add_f32 v[90:91], v[90:91], v[92:93] neg_lo:[0,1] neg_hi:[0,1]
	v_pk_add_f32 v[92:93], v[72:73], v[68:69]
	v_pk_add_f32 v[68:69], v[72:73], v[68:69] neg_lo:[0,1] neg_hi:[0,1]
	v_pk_add_f32 v[72:73], v[64:65], v[90:91] op_sel:[0,1] op_sel_hi:[1,0] neg_hi:[0,1]
	v_pk_add_f32 v[64:65], v[64:65], v[90:91] op_sel:[0,1] op_sel_hi:[1,0] neg_lo:[0,1]
	v_pk_mul_f32 v[90:91], v[88:89], v[30:31] op_sel:[0,0] op_sel_hi:[0,1]
	v_pk_fma_f32 v[90:91], v[88:89], v[30:31], v[90:91] op_sel:[1,1,0] op_sel_hi:[1,0,1] neg_lo:[0,1,0]
	v_pk_mul_f32 v[88:89], v[74:75], v[28:29] op_sel:[0,0] op_sel_hi:[0,1]
	v_pk_fma_f32 v[88:89], v[74:75], v[28:29], v[88:89] op_sel:[1,1,0] op_sel_hi:[1,0,1] neg_lo:[0,1,0]
	v_pk_mul_f32 v[74:75], v[92:93], v[26:27] op_sel:[0,0] op_sel_hi:[0,1]
	v_pk_fma_f32 v[74:75], v[92:93], v[26:27], v[74:75] op_sel:[1,1,0] op_sel_hi:[1,0,1] neg_lo:[0,1,0]
	s_barrier
	ds_write_b64 v1, v[74:75] offset:6552
	v_pk_mul_f32 v[74:75], v[84:85], v[24:25] op_sel:[0,0] op_sel_hi:[0,1]
	v_pk_fma_f32 v[74:75], v[84:85], v[24:25], v[74:75] op_sel:[1,1,0] op_sel_hi:[1,0,1] neg_lo:[0,1,0]
	ds_write_b64 v1, v[74:75] offset:8736
	v_pk_mul_f32 v[74:75], v[94:95], v[20:21] op_sel:[0,0] op_sel_hi:[0,1]
	v_pk_fma_f32 v[74:75], v[94:95], v[20:21], v[74:75] op_sel:[1,1,0] op_sel_hi:[1,0,1] neg_lo:[0,1,0]
	ds_write_b64 v1, v[74:75] offset:10920
	v_pk_mul_f32 v[74:75], v[86:87], v[16:17] op_sel:[0,0] op_sel_hi:[0,1]
	v_pk_fma_f32 v[74:75], v[86:87], v[16:17], v[74:75] op_sel:[1,1,0] op_sel_hi:[1,0,1] neg_lo:[0,1,0]
	ds_write_b64 v1, v[74:75] offset:13104
	v_pk_mul_f32 v[74:75], v[72:73], v[10:11] op_sel:[0,0] op_sel_hi:[0,1]
	v_pk_fma_f32 v[74:75], v[72:73], v[10:11], v[74:75] op_sel:[1,1,0] op_sel_hi:[1,0,1] neg_lo:[0,1,0]
	v_pk_mul_f32 v[72:73], v[82:83], v[22:23] op_sel:[0,0] op_sel_hi:[0,1]
	v_pk_fma_f32 v[72:73], v[82:83], v[22:23], v[72:73] op_sel:[1,1,0] op_sel_hi:[1,0,1] neg_lo:[0,1,0]
	ds_write_b64 v1, v[72:73] offset:17472
	v_pk_mul_f32 v[72:73], v[78:79], v[18:19] op_sel:[0,0] op_sel_hi:[0,1]
	v_pk_fma_f32 v[72:73], v[78:79], v[18:19], v[72:73] op_sel:[1,1,0] op_sel_hi:[1,0,1] neg_lo:[0,1,0]
	ds_write_b64 v1, v[72:73] offset:19656
	v_pk_mul_f32 v[72:73], v[76:77], v[12:13] op_sel:[0,0] op_sel_hi:[0,1]
	v_pk_fma_f32 v[72:73], v[76:77], v[12:13], v[72:73] op_sel:[1,1,0] op_sel_hi:[1,0,1] neg_lo:[0,1,0]
	ds_write_b64 v1, v[72:73] offset:21840
	v_pk_mul_f32 v[72:73], v[68:69], v[14:15] op_sel:[0,0] op_sel_hi:[0,1]
	v_pk_fma_f32 v[72:73], v[68:69], v[14:15], v[72:73] op_sel:[1,1,0] op_sel_hi:[1,0,1] neg_lo:[0,1,0]
	v_pk_mul_f32 v[68:69], v[80:81], v[6:7] op_sel:[0,0] op_sel_hi:[0,1]
	v_pk_fma_f32 v[68:69], v[80:81], v[6:7], v[68:69] op_sel:[1,1,0] op_sel_hi:[1,0,1] neg_lo:[0,1,0]
	ds_write_b64 v1, v[68:69] offset:26208
	v_pk_mul_f32 v[68:69], v[66:67], v[8:9] op_sel:[0,0] op_sel_hi:[0,1]
	v_pk_fma_f32 v[68:69], v[66:67], v[8:9], v[68:69] op_sel:[1,1,0] op_sel_hi:[1,0,1] neg_lo:[0,1,0]
	v_pk_mul_f32 v[66:67], v[70:71], v[4:5] op_sel:[0,0] op_sel_hi:[0,1]
	v_pk_fma_f32 v[66:67], v[70:71], v[4:5], v[66:67] op_sel:[1,1,0] op_sel_hi:[1,0,1] neg_lo:[0,1,0]
	ds_write_b64 v1, v[66:67] offset:30576
	v_pk_mul_f32 v[66:67], v[64:65], v[2:3] op_sel:[0,0] op_sel_hi:[0,1]
	v_pk_fma_f32 v[66:67], v[64:65], v[2:3], v[66:67] op_sel:[1,1,0] op_sel_hi:[1,0,1] neg_lo:[0,1,0]
	ds_write_b64 v1, v[98:99]
	ds_write_b64 v1, v[90:91] offset:2184
	ds_write_b64 v1, v[88:89] offset:4368
	ds_write_b64 v1, v[74:75] offset:15288
	ds_write_b64 v1, v[72:73] offset:24024
	ds_write_b64 v1, v[68:69] offset:28392
	ds_write_b64 v1, v[66:67] offset:32760
	s_waitcnt lgkmcnt(0)
	s_barrier
	ds_read2_b64 v[64:67], v96 offset1:16
	ds_read2_b64 v[68:71], v96 offset0:32 offset1:48
	ds_read2_b64 v[72:75], v96 offset0:64 offset1:80
	ds_read2_b64 v[76:79], v96 offset0:128 offset1:144
	ds_read2_b64 v[80:83], v96 offset0:96 offset1:112
	ds_read2_b64 v[84:87], v96 offset0:192 offset1:208
	ds_read2_b64 v[88:91], v96 offset0:160 offset1:176
	ds_read2_b64 v[92:95], v96 offset0:224 offset1:240
	s_waitcnt lgkmcnt(4)
	v_pk_add_f32 v[98:99], v[64:65], v[76:77]
	v_pk_add_f32 v[64:65], v[64:65], v[76:77] neg_lo:[0,1] neg_hi:[0,1]
	s_waitcnt lgkmcnt(2)
	v_pk_add_f32 v[76:77], v[72:73], v[84:85]
	v_pk_add_f32 v[72:73], v[72:73], v[84:85] neg_lo:[0,1] neg_hi:[0,1]
	v_pk_add_f32 v[84:85], v[98:99], v[76:77]
	v_pk_add_f32 v[76:77], v[98:99], v[76:77] neg_lo:[0,1] neg_hi:[0,1]
	v_pk_add_f32 v[98:99], v[64:65], v[72:73] op_sel:[0,1] op_sel_hi:[1,0] neg_hi:[0,1]
	v_pk_add_f32 v[64:65], v[64:65], v[72:73] op_sel:[0,1] op_sel_hi:[1,0] neg_lo:[0,1]
	v_pk_add_f32 v[72:73], v[66:67], v[78:79]
	v_pk_add_f32 v[66:67], v[66:67], v[78:79] neg_lo:[0,1] neg_hi:[0,1]
	v_pk_add_f32 v[78:79], v[74:75], v[86:87]
	v_pk_add_f32 v[74:75], v[74:75], v[86:87] neg_lo:[0,1] neg_hi:[0,1]
	v_pk_add_f32 v[86:87], v[72:73], v[78:79]
	v_pk_add_f32 v[72:73], v[72:73], v[78:79] neg_lo:[0,1] neg_hi:[0,1]
	v_pk_add_f32 v[78:79], v[66:67], v[74:75] op_sel:[0,1] op_sel_hi:[1,0] neg_hi:[0,1]
	v_pk_add_f32 v[66:67], v[66:67], v[74:75] op_sel:[0,1] op_sel_hi:[1,0] neg_lo:[0,1]
	s_waitcnt lgkmcnt(1)
	v_pk_add_f32 v[74:75], v[68:69], v[88:89]
	v_pk_add_f32 v[68:69], v[68:69], v[88:89] neg_lo:[0,1] neg_hi:[0,1]
	s_waitcnt lgkmcnt(0)
	v_pk_add_f32 v[88:89], v[80:81], v[92:93]
	v_pk_add_f32 v[80:81], v[80:81], v[92:93] neg_lo:[0,1] neg_hi:[0,1]
	v_pk_add_f32 v[92:93], v[74:75], v[88:89]
	v_pk_add_f32 v[74:75], v[74:75], v[88:89] neg_lo:[0,1] neg_hi:[0,1]
	v_pk_add_f32 v[88:89], v[68:69], v[80:81] op_sel:[0,1] op_sel_hi:[1,0] neg_hi:[0,1]
	v_pk_add_f32 v[68:69], v[68:69], v[80:81] op_sel:[0,1] op_sel_hi:[1,0] neg_lo:[0,1]
	v_pk_add_f32 v[80:81], v[70:71], v[90:91]
	v_pk_add_f32 v[70:71], v[70:71], v[90:91] neg_lo:[0,1] neg_hi:[0,1]
	v_pk_add_f32 v[90:91], v[82:83], v[94:95]
	v_pk_add_f32 v[82:83], v[82:83], v[94:95] neg_lo:[0,1] neg_hi:[0,1]
	v_pk_add_f32 v[94:95], v[80:81], v[90:91]
	v_pk_add_f32 v[80:81], v[80:81], v[90:91] neg_lo:[0,1] neg_hi:[0,1]
	v_pk_add_f32 v[90:91], v[70:71], v[82:83] op_sel:[0,1] op_sel_hi:[1,0] neg_hi:[0,1]
	v_pk_add_f32 v[70:71], v[70:71], v[82:83] op_sel:[0,1] op_sel_hi:[1,0] neg_lo:[0,1]
	v_pk_mul_f32 v[82:83], v[78:79], s[6:7] op_sel:[0,0] op_sel_hi:[0,1]
	v_pk_fma_f32 v[82:83], v[78:79], s[6:7], v[82:83] op_sel:[1,1,0] op_sel_hi:[1,0,1] neg_lo:[0,1,0]
	v_pk_mul_f32 v[78:79], v[66:67], s[10:11] op_sel:[0,0] op_sel_hi:[0,1]
	v_pk_fma_f32 v[78:79], v[66:67], s[10:11], v[78:79] op_sel:[1,1,0] op_sel_hi:[1,0,1] neg_lo:[0,1,0]
	v_pk_add_f32 v[66:67], v[88:89], v[88:89] op_sel:[0,1] op_sel_hi:[1,0] neg_hi:[0,1]
	v_pk_add_f32 v[72:73], v[72:73], v[72:73] op_sel:[0,1] op_sel_hi:[1,0] neg_hi:[0,1]
	s_nop 0
	v_pk_mul_f32 v[88:89], v[90:91], s[10:11] op_sel:[0,0] op_sel_hi:[0,1]
	v_pk_fma_f32 v[88:89], v[90:91], s[10:11], v[88:89] op_sel:[1,1,0] op_sel_hi:[1,0,1] neg_lo:[0,1,0]
	v_pk_mul_f32 v[90:91], v[70:71], s[14:15] op_sel:[0,0] op_sel_hi:[0,1]
	v_pk_fma_f32 v[90:91], v[70:71], s[14:15], v[90:91] op_sel:[1,1,0] op_sel_hi:[1,0,1] neg_lo:[0,1,0]
	v_pk_add_f32 v[70:71], v[84:85], v[92:93]
	v_pk_mul_f32 v[66:67], v[66:67], s[8:9]
	v_pk_add_f32 v[84:85], v[84:85], v[92:93] neg_lo:[0,1] neg_hi:[0,1]
	v_pk_add_f32 v[92:93], v[86:87], v[94:95]
	v_pk_add_f32 v[86:87], v[86:87], v[94:95] neg_lo:[0,1] neg_hi:[0,1]
	v_pk_add_f32 v[68:69], v[68:69], v[68:69] op_sel:[0,1] op_sel_hi:[1,0] neg_lo:[0,1]
	v_pk_add_f32 v[80:81], v[80:81], v[80:81] op_sel:[0,1] op_sel_hi:[1,0] neg_lo:[0,1]
	v_pk_add_f32 v[94:95], v[70:71], v[92:93]
	v_pk_add_f32 v[92:93], v[70:71], v[92:93] neg_lo:[0,1] neg_hi:[0,1]
	v_pk_add_f32 v[100:101], v[84:85], v[86:87] op_sel:[0,1] op_sel_hi:[1,0] neg_hi:[0,1]
	v_pk_add_f32 v[84:85], v[84:85], v[86:87] op_sel:[0,1] op_sel_hi:[1,0] neg_lo:[0,1]
	v_pk_add_f32 v[70:71], v[98:99], v[66:67]
	v_pk_add_f32 v[66:67], v[98:99], v[66:67] neg_lo:[0,1] neg_hi:[0,1]
	v_pk_add_f32 v[86:87], v[82:83], v[88:89]
	v_pk_add_f32 v[82:83], v[82:83], v[88:89] neg_lo:[0,1] neg_hi:[0,1]
	v_pk_mul_f32 v[72:73], v[72:73], s[8:9]
	v_pk_mul_f32 v[68:69], v[68:69], s[12:13]
	v_pk_mul_f32 v[80:81], v[80:81], s[12:13]
	v_pk_add_f32 v[88:89], v[70:71], v[86:87]
	v_pk_add_f32 v[86:87], v[70:71], v[86:87] neg_lo:[0,1] neg_hi:[0,1]
	v_pk_add_f32 v[98:99], v[66:67], v[82:83] op_sel:[0,1] op_sel_hi:[1,0] neg_hi:[0,1]
	v_pk_add_f32 v[82:83], v[66:67], v[82:83] op_sel:[0,1] op_sel_hi:[1,0] neg_lo:[0,1]
	v_pk_add_f32 v[66:67], v[76:77], v[74:75] op_sel:[0,1] op_sel_hi:[1,0] neg_hi:[0,1]
	v_pk_add_f32 v[70:71], v[76:77], v[74:75] op_sel:[0,1] op_sel_hi:[1,0] neg_lo:[0,1]
	v_pk_add_f32 v[74:75], v[72:73], v[80:81]
	v_pk_add_f32 v[72:73], v[72:73], v[80:81] neg_lo:[0,1] neg_hi:[0,1]
	v_pk_add_f32 v[76:77], v[74:75], v[66:67]
	v_pk_add_f32 v[74:75], v[66:67], v[74:75] neg_lo:[0,1] neg_hi:[0,1]
	v_pk_add_f32 v[66:67], v[64:65], v[68:69]
	v_pk_add_f32 v[64:65], v[64:65], v[68:69] neg_lo:[0,1] neg_hi:[0,1]
	v_pk_add_f32 v[68:69], v[78:79], v[90:91]
	v_pk_add_f32 v[80:81], v[70:71], v[72:73] op_sel:[0,1] op_sel_hi:[1,0] neg_hi:[0,1]
	v_pk_add_f32 v[72:73], v[70:71], v[72:73] op_sel:[0,1] op_sel_hi:[1,0] neg_lo:[0,1]
	v_pk_add_f32 v[70:71], v[78:79], v[90:91] neg_lo:[0,1] neg_hi:[0,1]
	v_pk_add_f32 v[78:79], v[66:67], v[68:69]
	v_pk_add_f32 v[90:91], v[66:67], v[68:69] neg_lo:[0,1] neg_hi:[0,1]
	v_mov_b32_e32 v68, v0
	v_pk_add_f32 v[102:103], v[64:65], v[70:71] op_sel:[0,1] op_sel_hi:[1,0] neg_hi:[0,1]
	v_pk_add_f32 v[104:105], v[64:65], v[70:71] op_sel:[0,1] op_sel_hi:[1,0] neg_lo:[0,1]
	s_nop 0
	v_ashrrev_i32_e32 v64, 4, v68
	v_lshlrev_b32_e32 v97, 3, v64
	v_add_u32_e32 v108, 0x8800, v97
	v_and_b32_e32 v68, 15, v68
	ds_read2_b64 v[64:67], v108 offset0:16 offset1:32
	v_mad_u32_u24 v109, v68, s5, v97
	ds_read2_b64 v[68:71], v108 offset0:48 offset1:64
	s_waitcnt lgkmcnt(1)
	v_pk_mul_f32 v[106:107], v[88:89], v[64:65] op_sel:[0,0] op_sel_hi:[0,1]
	v_pk_fma_f32 v[106:107], v[88:89], v[64:65], v[106:107] op_sel:[1,1,0] op_sel_hi:[1,0,1] neg_lo:[0,1,0]
	v_pk_mul_f32 v[88:89], v[76:77], v[66:67] op_sel:[0,0] op_sel_hi:[0,1]
	v_pk_fma_f32 v[88:89], v[76:77], v[66:67], v[88:89] op_sel:[1,1,0] op_sel_hi:[1,0,1] neg_lo:[0,1,0]
	s_waitcnt lgkmcnt(0)
	v_pk_mul_f32 v[76:77], v[78:79], v[68:69] op_sel:[0,0] op_sel_hi:[0,1]
	v_pk_fma_f32 v[76:77], v[78:79], v[68:69], v[76:77] op_sel:[1,1,0] op_sel_hi:[1,0,1] neg_lo:[0,1,0]
	ds_write2_b64 v109, v[88:89], v[76:77] offset0:32 offset1:48
	v_pk_mul_f32 v[76:77], v[100:101], v[70:71] op_sel:[0,0] op_sel_hi:[0,1]
	v_pk_fma_f32 v[76:77], v[100:101], v[70:71], v[76:77] op_sel:[1,1,0] op_sel_hi:[1,0,1] neg_lo:[0,1,0]
	ds_read2_b64 v[64:67], v108 offset0:80 offset1:96
	s_waitcnt lgkmcnt(0)
	v_pk_mul_f32 v[78:79], v[98:99], v[64:65] op_sel:[0,0] op_sel_hi:[0,1]
	v_pk_fma_f32 v[78:79], v[98:99], v[64:65], v[78:79] op_sel:[1,1,0] op_sel_hi:[1,0,1] neg_lo:[0,1,0]
	ds_write2_b64 v109, v[76:77], v[78:79] offset0:64 offset1:80
	v_pk_mul_f32 v[76:77], v[80:81], v[66:67] op_sel:[0,0] op_sel_hi:[0,1]
	v_pk_fma_f32 v[76:77], v[80:81], v[66:67], v[76:77] op_sel:[1,1,0] op_sel_hi:[1,0,1] neg_lo:[0,1,0]
	ds_read2_b64 v[68:71], v108 offset0:112 offset1:128
	ds_read2_b64 v[64:67], v108 offset0:144 offset1:160
	s_waitcnt lgkmcnt(1)
	v_pk_mul_f32 v[78:79], v[102:103], v[68:69] op_sel:[0,0] op_sel_hi:[0,1]
	v_pk_fma_f32 v[78:79], v[102:103], v[68:69], v[78:79] op_sel:[1,1,0] op_sel_hi:[1,0,1] neg_lo:[0,1,0]
	ds_write2_b64 v109, v[76:77], v[78:79] offset0:96 offset1:112
	v_pk_mul_f32 v[76:77], v[92:93], v[70:71] op_sel:[0,0] op_sel_hi:[0,1]
	v_pk_fma_f32 v[76:77], v[92:93], v[70:71], v[76:77] op_sel:[1,1,0] op_sel_hi:[1,0,1] neg_lo:[0,1,0]
	ds_read2_b64 v[68:71], v108 offset0:176 offset1:192
	s_waitcnt lgkmcnt(2)
	v_pk_mul_f32 v[78:79], v[86:87], v[64:65] op_sel:[0,0] op_sel_hi:[0,1]
	v_pk_fma_f32 v[78:79], v[86:87], v[64:65], v[78:79] op_sel:[1,1,0] op_sel_hi:[1,0,1] neg_lo:[0,1,0]
	ds_write2_b64 v109, v[76:77], v[78:79] offset0:128 offset1:144
	v_pk_mul_f32 v[76:77], v[74:75], v[66:67] op_sel:[0,0] op_sel_hi:[0,1]
	v_pk_fma_f32 v[76:77], v[74:75], v[66:67], v[76:77] op_sel:[1,1,0] op_sel_hi:[1,0,1] neg_lo:[0,1,0]
	ds_read2_b64 v[64:67], v108 offset0:208 offset1:224
	s_waitcnt lgkmcnt(2)
	v_pk_mul_f32 v[74:75], v[90:91], v[68:69] op_sel:[0,0] op_sel_hi:[0,1]
	v_pk_fma_f32 v[74:75], v[90:91], v[68:69], v[74:75] op_sel:[1,1,0] op_sel_hi:[1,0,1] neg_lo:[0,1,0]
	ds_write2_b64 v109, v[76:77], v[74:75] offset0:160 offset1:176
	v_pk_mul_f32 v[74:75], v[84:85], v[70:71] op_sel:[0,0] op_sel_hi:[0,1]
	v_pk_fma_f32 v[74:75], v[84:85], v[70:71], v[74:75] op_sel:[1,1,0] op_sel_hi:[1,0,1] neg_lo:[0,1,0]
	s_waitcnt lgkmcnt(1)
	v_pk_mul_f32 v[70:71], v[82:83], v[64:65] op_sel:[0,0] op_sel_hi:[0,1]
	v_pk_fma_f32 v[70:71], v[82:83], v[64:65], v[70:71] op_sel:[1,1,0] op_sel_hi:[1,0,1] neg_lo:[0,1,0]
	v_pk_mul_f32 v[64:65], v[72:73], v[66:67] op_sel:[0,0] op_sel_hi:[0,1]
	v_pk_fma_f32 v[64:65], v[72:73], v[66:67], v[64:65] op_sel:[1,1,0] op_sel_hi:[1,0,1] neg_lo:[0,1,0]
	ds_read_b64 v[68:69], v97 offset:36736
	s_waitcnt lgkmcnt(0)
	v_pk_mul_f32 v[66:67], v[104:105], v[68:69] op_sel:[0,0] op_sel_hi:[0,1]
	v_pk_fma_f32 v[66:67], v[104:105], v[68:69], v[66:67] op_sel:[1,1,0] op_sel_hi:[1,0,1] neg_lo:[0,1,0]
	ds_write2_b64 v109, v[64:65], v[66:67] offset0:224 offset1:240
	v_mov_b32_e32 v64, v0
	ds_write2_b64 v109, v[94:95], v[106:107] offset1:16
	ds_write2_b64 v109, v[74:75], v[70:71] offset0:192 offset1:208
	s_waitcnt lgkmcnt(0)
	s_barrier
	s_nop 0
	v_and_b32_e32 v65, 15, v64
	v_and_b32_e32 v64, 0x1ffffff0, v64
	v_lshlrev_b32_e32 v64, 3, v64
	v_mad_u32_u24 v92, v65, s5, v64
	ds_read2_b64 v[64:67], v92 offset1:1
	ds_read2_b64 v[68:71], v92 offset0:2 offset1:3
	ds_read2_b64 v[72:75], v92 offset0:8 offset1:9
	ds_read2_b64 v[76:79], v92 offset0:4 offset1:5
	ds_read2_b64 v[80:83], v92 offset0:6 offset1:7
	ds_read2_b64 v[84:87], v92 offset0:12 offset1:13
	ds_read2_b64 v[88:91], v92 offset0:10 offset1:11
	ds_read2_b64 v[92:95], v92 offset0:14 offset1:15
	s_waitcnt lgkmcnt(5)
	v_pk_add_f32 v[98:99], v[64:65], v[72:73]
	v_pk_add_f32 v[64:65], v[64:65], v[72:73] neg_lo:[0,1] neg_hi:[0,1]
	s_waitcnt lgkmcnt(2)
	v_pk_add_f32 v[72:73], v[76:77], v[84:85]
	v_pk_add_f32 v[76:77], v[76:77], v[84:85] neg_lo:[0,1] neg_hi:[0,1]
	v_pk_add_f32 v[84:85], v[98:99], v[72:73]
	v_pk_add_f32 v[98:99], v[98:99], v[72:73] neg_lo:[0,1] neg_hi:[0,1]
	v_pk_add_f32 v[100:101], v[64:65], v[76:77] op_sel:[0,1] op_sel_hi:[1,0] neg_hi:[0,1]
	v_pk_add_f32 v[102:103], v[64:65], v[76:77] op_sel:[0,1] op_sel_hi:[1,0] neg_lo:[0,1]
	v_pk_add_f32 v[64:65], v[66:67], v[74:75]
	v_pk_add_f32 v[72:73], v[78:79], v[86:87]
	v_pk_add_f32 v[66:67], v[66:67], v[74:75] neg_lo:[0,1] neg_hi:[0,1]
	v_pk_add_f32 v[74:75], v[78:79], v[86:87] neg_lo:[0,1] neg_hi:[0,1]
	v_pk_add_f32 v[76:77], v[64:65], v[72:73]
	v_pk_add_f32 v[64:65], v[64:65], v[72:73] neg_lo:[0,1] neg_hi:[0,1]
	v_pk_add_f32 v[72:73], v[66:67], v[74:75] op_sel:[0,1] op_sel_hi:[1,0] neg_hi:[0,1]
	v_pk_add_f32 v[66:67], v[66:67], v[74:75] op_sel:[0,1] op_sel_hi:[1,0] neg_lo:[0,1]
	s_waitcnt lgkmcnt(1)
	v_pk_add_f32 v[74:75], v[68:69], v[88:89]
	s_waitcnt lgkmcnt(0)
	v_pk_add_f32 v[78:79], v[80:81], v[92:93]
	v_pk_add_f32 v[64:65], v[64:65], v[64:65] op_sel:[0,1] op_sel_hi:[1,0] neg_hi:[0,1]
	v_pk_add_f32 v[68:69], v[68:69], v[88:89] neg_lo:[0,1] neg_hi:[0,1]
	v_pk_add_f32 v[80:81], v[80:81], v[92:93] neg_lo:[0,1] neg_hi:[0,1]
	v_pk_add_f32 v[86:87], v[74:75], v[78:79]
	v_pk_add_f32 v[78:79], v[74:75], v[78:79] neg_lo:[0,1] neg_hi:[0,1]
	v_pk_add_f32 v[74:75], v[68:69], v[80:81] op_sel:[0,1] op_sel_hi:[1,0] neg_hi:[0,1]
	v_pk_mul_f32 v[92:93], v[64:65], s[8:9]
	v_pk_add_f32 v[68:69], v[68:69], v[80:81] op_sel:[0,1] op_sel_hi:[1,0] neg_lo:[0,1]
	v_pk_add_f32 v[80:81], v[70:71], v[90:91]
	v_pk_add_f32 v[64:65], v[74:75], v[74:75] op_sel:[0,1] op_sel_hi:[1,0] neg_hi:[0,1]
	v_pk_add_f32 v[70:71], v[70:71], v[90:91] neg_lo:[0,1] neg_hi:[0,1]
	v_pk_add_f32 v[88:89], v[82:83], v[94:95]
	v_pk_add_f32 v[82:83], v[82:83], v[94:95] neg_lo:[0,1] neg_hi:[0,1]
	v_pk_mul_f32 v[94:95], v[66:67], s[10:11] op_sel:[0,0] op_sel_hi:[0,1]
	v_pk_fma_f32 v[94:95], v[66:67], s[10:11], v[94:95] op_sel:[1,1,0] op_sel_hi:[1,0,1] neg_lo:[0,1,0]
	v_pk_mul_f32 v[66:67], v[64:65], s[8:9]
	v_pk_add_f32 v[64:65], v[68:69], v[68:69] op_sel:[0,1] op_sel_hi:[1,0] neg_lo:[0,1]
	v_pk_add_f32 v[90:91], v[80:81], v[88:89]
	v_pk_add_f32 v[80:81], v[80:81], v[88:89] neg_lo:[0,1] neg_hi:[0,1]
	v_pk_add_f32 v[88:89], v[70:71], v[82:83] op_sel:[0,1] op_sel_hi:[1,0] neg_hi:[0,1]
	v_pk_add_f32 v[70:71], v[70:71], v[82:83] op_sel:[0,1] op_sel_hi:[1,0] neg_lo:[0,1]
	v_pk_mul_f32 v[104:105], v[64:65], s[12:13]
	v_pk_mul_f32 v[82:83], v[72:73], s[6:7] op_sel:[0,0] op_sel_hi:[0,1]
	v_pk_fma_f32 v[82:83], v[72:73], s[6:7], v[82:83] op_sel:[1,1,0] op_sel_hi:[1,0,1] neg_lo:[0,1,0]
	v_pk_add_f32 v[72:73], v[76:77], v[90:91]
	v_pk_add_f32 v[64:65], v[80:81], v[80:81] op_sel:[0,1] op_sel_hi:[1,0] neg_lo:[0,1]
	v_pk_mul_f32 v[68:69], v[88:89], s[10:11] op_sel:[0,0] op_sel_hi:[0,1]
	v_pk_fma_f32 v[68:69], v[88:89], s[10:11], v[68:69] op_sel:[1,1,0] op_sel_hi:[1,0,1] neg_lo:[0,1,0]
	v_pk_mul_f32 v[108:109], v[70:71], s[14:15] op_sel:[0,0] op_sel_hi:[0,1]
	v_pk_fma_f32 v[108:109], v[70:71], s[14:15], v[108:109] op_sel:[1,1,0] op_sel_hi:[1,0,1] neg_lo:[0,1,0]
	v_pk_add_f32 v[70:71], v[84:85], v[86:87] neg_lo:[0,1] neg_hi:[0,1]
	v_pk_mul_f32 v[106:107], v[64:65], s[12:13]
	v_pk_add_f32 v[64:65], v[84:85], v[86:87]
	v_pk_add_f32 v[74:75], v[76:77], v[90:91] neg_lo:[0,1] neg_hi:[0,1]
	v_pk_add_f32 v[88:89], v[64:65], v[72:73]
	v_pk_add_f32 v[72:73], v[64:65], v[72:73] neg_lo:[0,1] neg_hi:[0,1]
	v_pk_add_f32 v[80:81], v[70:71], v[74:75] op_sel:[0,1] op_sel_hi:[1,0] neg_hi:[0,1]
	v_pk_add_f32 v[64:65], v[70:71], v[74:75] op_sel:[0,1] op_sel_hi:[1,0] neg_lo:[0,1]
	v_pk_add_f32 v[70:71], v[100:101], v[66:67]
	v_pk_add_f32 v[66:67], v[100:101], v[66:67] neg_lo:[0,1] neg_hi:[0,1]
	v_pk_add_f32 v[74:75], v[82:83], v[68:69]
	v_pk_add_f32 v[68:69], v[82:83], v[68:69] neg_lo:[0,1] neg_hi:[0,1]
	v_pk_add_f32 v[90:91], v[70:71], v[74:75]
	v_pk_add_f32 v[74:75], v[70:71], v[74:75] neg_lo:[0,1] neg_hi:[0,1]
	v_pk_add_f32 v[82:83], v[66:67], v[68:69] op_sel:[0,1] op_sel_hi:[1,0] neg_hi:[0,1]
	v_pk_add_f32 v[66:67], v[66:67], v[68:69] op_sel:[0,1] op_sel_hi:[1,0] neg_lo:[0,1]
	v_pk_add_f32 v[68:69], v[98:99], v[78:79] op_sel:[0,1] op_sel_hi:[1,0] neg_hi:[0,1]
	v_pk_add_f32 v[70:71], v[98:99], v[78:79] op_sel:[0,1] op_sel_hi:[1,0] neg_lo:[0,1]
	v_pk_add_f32 v[76:77], v[92:93], v[106:107]
	v_pk_add_f32 v[78:79], v[92:93], v[106:107] neg_lo:[0,1] neg_hi:[0,1]
	v_pk_add_f32 v[92:93], v[76:77], v[68:69]
	v_pk_add_f32 v[76:77], v[68:69], v[76:77] neg_lo:[0,1] neg_hi:[0,1]
	v_pk_add_f32 v[86:87], v[70:71], v[78:79] op_sel:[0,1] op_sel_hi:[1,0] neg_hi:[0,1]
	v_pk_add_f32 v[68:69], v[70:71], v[78:79] op_sel:[0,1] op_sel_hi:[1,0] neg_lo:[0,1]
	v_pk_add_f32 v[70:71], v[102:103], v[104:105]
	v_pk_add_f32 v[98:99], v[102:103], v[104:105] neg_lo:[0,1] neg_hi:[0,1]
	v_pk_add_f32 v[78:79], v[94:95], v[108:109]
	v_pk_add_f32 v[100:101], v[94:95], v[108:109] neg_lo:[0,1] neg_hi:[0,1]
	v_pk_add_f32 v[94:95], v[70:71], v[78:79]
	v_pk_add_f32 v[78:79], v[70:71], v[78:79] neg_lo:[0,1] neg_hi:[0,1]
	v_pk_add_f32 v[84:85], v[98:99], v[100:101] op_sel:[0,1] op_sel_hi:[1,0] neg_hi:[0,1]
	v_pk_add_f32 v[70:71], v[98:99], v[100:101] op_sel:[0,1] op_sel_hi:[1,0] neg_lo:[0,1]
	v_mov_b32_e32 v98, v0
	s_nop 0
	v_and_b32_e32 v97, -16, v98
	v_and_b32_e32 v99, 15, v98
	v_lshlrev_b32_e32 v100, 3, v97
	v_mad_u32_u24 v100, v99, s5, v100
	v_cmp_ne_u32_e32 vcc, 0, v99
	ds_write2_b64 v100, v[88:89], v[90:91] offset1:1
	ds_write2_b64 v100, v[92:93], v[94:95] offset0:2 offset1:3
	ds_write2_b64 v100, v[80:81], v[82:83] offset0:4 offset1:5
	ds_write2_b64 v100, v[86:87], v[84:85] offset0:6 offset1:7
	ds_write2_b64 v100, v[72:73], v[74:75] offset0:8 offset1:9
	ds_write2_b64 v100, v[76:77], v[78:79] offset0:10 offset1:11
	ds_write2_b64 v100, v[64:65], v[66:67] offset0:12 offset1:13
	ds_write2_b64 v100, v[68:69], v[70:71] offset0:14 offset1:15
	s_waitcnt lgkmcnt(0)
	s_barrier
	s_and_saveexec_b64 s[6:7], vcc
	s_xor_b64 s[6:7], exec, s[6:7]
	v_sub_u32_e32 v99, 16, v99
	v_mul_u32_u24_e32 v99, 0x111, v99
	v_sub_u32_e32 v97, v99, v97
	v_add_u32_e32 v100, 0xf0, v97
	s_andn2_saveexec_b64 s[6:7], s[6:7]
	v_sub_u32_e32 v97, 0x100, v98
	v_cmp_lt_u32_e32 vcc, 15, v98
	s_nop 1
	v_cndmask_b32_e32 v100, 1, v97, vcc
	s_or_b64 exec, exec, s[6:7]
	v_mov_b32_e32 v97, 0
	v_lshlrev_b32_e32 v110, 3, v100
	ds_read_b64 v[108:109], v97
	ds_read2_b64 v[100:103], v110 offset0:14 offset1:15
	v_cmp_eq_u32_e32 vcc, 0, v98
	ds_read2_b64 v[104:107], v110 offset0:12 offset1:13
	s_mov_b32 s6, 0x3f6c835e
	s_mov_b32 s7, 0xbec3ef15
	s_waitcnt lgkmcnt(1)
	v_cndmask_b32_e32 v99, v103, v109, vcc
	v_cndmask_b32_e32 v98, v102, v108, vcc
	v_pk_add_f32 v[102:103], v[88:89], v[98:99] neg_hi:[0,1]
	v_pk_add_f32 v[88:89], v[88:89], v[98:99] neg_lo:[0,1]
	s_mov_b32 s9, s8
	v_pk_mul_f32 v[98:99], v[102:103], v[88:89] op_sel:[0,0] op_sel_hi:[0,1]
	v_pk_fma_f32 v[98:99], v[102:103], v[88:89], v[98:99] op_sel:[1,1,0] op_sel_hi:[1,0,1] neg_hi:[0,1,0]
	v_pk_add_f32 v[88:89], v[90:91], v[100:101] neg_hi:[0,1]
	v_pk_add_f32 v[90:91], v[90:91], v[100:101] neg_lo:[0,1]
	s_mov_b32 s14, s11
	v_pk_add_f32 v[62:63], v[62:63], v[98:99] op_sel:[1,0] op_sel_hi:[0,1] neg_lo:[0,1] neg_hi:[1,1]
	v_pk_mul_f32 v[98:99], v[88:89], v[90:91] op_sel:[0,0] op_sel_hi:[0,1]
	v_pk_fma_f32 v[98:99], v[88:89], v[90:91], v[98:99] op_sel:[1,1,0] op_sel_hi:[1,0,1] neg_hi:[0,1,0]
	s_waitcnt lgkmcnt(0)
	v_pk_add_f32 v[88:89], v[92:93], v[106:107] neg_hi:[0,1]
	v_pk_add_f32 v[90:91], v[92:93], v[106:107] neg_lo:[0,1]
	s_mov_b32 s15, s10
	v_pk_mul_f32 v[92:93], v[88:89], v[90:91] op_sel:[0,0] op_sel_hi:[0,1]
	v_pk_fma_f32 v[92:93], v[88:89], v[90:91], v[92:93] op_sel:[1,1,0] op_sel_hi:[1,0,1] neg_hi:[0,1,0]
	v_pk_add_f32 v[60:61], v[60:61], v[98:99] op_sel:[1,0] op_sel_hi:[0,1] neg_lo:[0,1] neg_hi:[1,1]
	ds_read2_b64 v[88:91], v110 offset0:10 offset1:11
	v_pk_add_f32 v[58:59], v[58:59], v[92:93] op_sel:[1,0] op_sel_hi:[0,1] neg_lo:[0,1] neg_hi:[1,1]
	v_pk_add_f32 v[92:93], v[94:95], v[104:105] neg_hi:[0,1]
	v_pk_add_f32 v[94:95], v[94:95], v[104:105] neg_lo:[0,1]
	s_mov_b32 s13, s12
	v_pk_mul_f32 v[98:99], v[92:93], v[94:95] op_sel:[0,0] op_sel_hi:[0,1]
	v_pk_fma_f32 v[98:99], v[92:93], v[94:95], v[98:99] op_sel:[1,1,0] op_sel_hi:[1,0,1] neg_hi:[0,1,0]
	ds_read2_b64 v[92:95], v110 offset0:8 offset1:9
	v_pk_add_f32 v[56:57], v[56:57], v[98:99] op_sel:[1,0] op_sel_hi:[0,1] neg_lo:[0,1] neg_hi:[1,1]
	s_waitcnt lgkmcnt(1)
	v_pk_add_f32 v[98:99], v[80:81], v[90:91] neg_hi:[0,1]
	v_pk_add_f32 v[80:81], v[80:81], v[90:91] neg_lo:[0,1]
	s_add_u32 s2, s2, 0x2000000
	v_pk_mul_f32 v[90:91], v[98:99], v[80:81] op_sel:[0,0] op_sel_hi:[0,1]
	v_pk_fma_f32 v[90:91], v[98:99], v[80:81], v[90:91] op_sel:[1,1,0] op_sel_hi:[1,0,1] neg_hi:[0,1,0]
	v_pk_add_f32 v[80:81], v[82:83], v[88:89] neg_hi:[0,1]
	v_pk_add_f32 v[82:83], v[82:83], v[88:89] neg_lo:[0,1]
	s_addc_u32 s3, s3, 0
	v_pk_mul_f32 v[88:89], v[80:81], v[82:83] op_sel:[0,0] op_sel_hi:[0,1]
	v_pk_fma_f32 v[88:89], v[80:81], v[82:83], v[88:89] op_sel:[1,1,0] op_sel_hi:[1,0,1] neg_hi:[0,1,0]
	s_waitcnt lgkmcnt(0)
	v_pk_add_f32 v[80:81], v[86:87], v[94:95] neg_lo:[0,1]
	v_pk_add_f32 v[54:55], v[54:55], v[90:91] op_sel:[1,0] op_sel_hi:[0,1] neg_lo:[0,1] neg_hi:[1,1]
	s_load_dwordx2 s[0:1], s[0:1], 0x8
	v_pk_add_f32 v[88:89], v[52:53], v[88:89] op_sel:[1,0] op_sel_hi:[0,1] neg_lo:[0,1] neg_hi:[1,1]
	v_pk_add_f32 v[52:53], v[86:87], v[94:95] neg_hi:[0,1]
	s_nop 0
	v_pk_mul_f32 v[82:83], v[52:53], v[80:81] op_sel:[0,0] op_sel_hi:[0,1]
	v_pk_fma_f32 v[82:83], v[52:53], v[80:81], v[82:83] op_sel:[1,1,0] op_sel_hi:[1,0,1] neg_hi:[0,1,0]
	v_pk_add_f32 v[80:81], v[84:85], v[92:93] neg_hi:[0,1]
	s_nop 0
	v_pk_add_f32 v[86:87], v[50:51], v[82:83] op_sel:[1,0] op_sel_hi:[0,1] neg_lo:[0,1] neg_hi:[1,1]
	ds_read2_b64 v[50:53], v110 offset0:6 offset1:7
	v_pk_add_f32 v[82:83], v[84:85], v[92:93] neg_lo:[0,1]
	s_nop 0
	v_pk_mul_f32 v[84:85], v[80:81], v[82:83] op_sel:[0,0] op_sel_hi:[0,1]
	v_pk_fma_f32 v[84:85], v[80:81], v[82:83], v[84:85] op_sel:[1,1,0] op_sel_hi:[1,0,1] neg_hi:[0,1,0]
	ds_read2_b64 v[80:83], v110 offset0:4 offset1:5
	v_pk_add_f32 v[84:85], v[48:49], v[84:85] op_sel:[1,0] op_sel_hi:[0,1] neg_lo:[0,1] neg_hi:[1,1]
	s_waitcnt lgkmcnt(0)
	v_pk_add_f32 v[48:49], v[72:73], v[52:53] neg_hi:[0,1]
	v_pk_add_f32 v[52:53], v[72:73], v[52:53] neg_lo:[0,1]
	s_nop 0
	v_pk_mul_f32 v[72:73], v[48:49], v[52:53] op_sel:[0,0] op_sel_hi:[0,1]
	v_pk_fma_f32 v[72:73], v[48:49], v[52:53], v[72:73] op_sel:[1,1,0] op_sel_hi:[1,0,1] neg_hi:[0,1,0]
	v_pk_add_f32 v[48:49], v[74:75], v[50:51] neg_lo:[0,1]
	s_nop 0
	v_pk_add_f32 v[52:53], v[46:47], v[72:73] op_sel:[1,0] op_sel_hi:[0,1] neg_lo:[0,1] neg_hi:[1,1]
	v_pk_add_f32 v[46:47], v[74:75], v[50:51] neg_hi:[0,1]
	s_nop 0
	v_pk_mul_f32 v[50:51], v[46:47], v[48:49] op_sel:[0,0] op_sel_hi:[0,1]
	v_pk_fma_f32 v[50:51], v[46:47], v[48:49], v[50:51] op_sel:[1,1,0] op_sel_hi:[1,0,1] neg_hi:[0,1,0]
	v_pk_add_f32 v[46:47], v[76:77], v[82:83] neg_lo:[0,1]
	s_nop 0
	v_pk_add_f32 v[50:51], v[44:45], v[50:51] op_sel:[1,0] op_sel_hi:[0,1] neg_lo:[0,1] neg_hi:[1,1]
	v_pk_add_f32 v[44:45], v[76:77], v[82:83] neg_hi:[0,1]
	s_nop 0
	v_pk_mul_f32 v[48:49], v[44:45], v[46:47] op_sel:[0,0] op_sel_hi:[0,1]
	v_pk_fma_f32 v[48:49], v[44:45], v[46:47], v[48:49] op_sel:[1,1,0] op_sel_hi:[1,0,1] neg_hi:[0,1,0]
	v_pk_add_f32 v[46:47], v[78:79], v[80:81] neg_hi:[0,1]
	s_nop 0
	v_pk_add_f32 v[72:73], v[42:43], v[48:49] op_sel:[1,0] op_sel_hi:[0,1] neg_lo:[0,1] neg_hi:[1,1]
	ds_read2_b64 v[42:45], v110 offset0:2 offset1:3
	v_pk_add_f32 v[48:49], v[78:79], v[80:81] neg_lo:[0,1]
	s_nop 0
	v_pk_mul_f32 v[74:75], v[46:47], v[48:49] op_sel:[0,0] op_sel_hi:[0,1]
	v_pk_fma_f32 v[74:75], v[46:47], v[48:49], v[74:75] op_sel:[1,1,0] op_sel_hi:[1,0,1] neg_hi:[0,1,0]
	ds_read2_b64 v[46:49], v110 offset1:1
	v_pk_add_f32 v[40:41], v[40:41], v[74:75] op_sel:[1,0] op_sel_hi:[0,1] neg_lo:[0,1] neg_hi:[1,1]
	s_waitcnt lgkmcnt(1)
	v_pk_add_f32 v[74:75], v[64:65], v[44:45] neg_hi:[0,1]
	v_pk_add_f32 v[44:45], v[64:65], v[44:45] neg_lo:[0,1]
	s_waitcnt lgkmcnt(0)
	v_pk_mul_f32 v[64:65], v[74:75], v[44:45] op_sel:[0,0] op_sel_hi:[0,1]
	v_pk_fma_f32 v[64:65], v[74:75], v[44:45], v[64:65] op_sel:[1,1,0] op_sel_hi:[1,0,1] neg_hi:[0,1,0]
	v_pk_add_f32 v[44:45], v[66:67], v[42:43] neg_hi:[0,1]
	v_pk_add_f32 v[42:43], v[66:67], v[42:43] neg_lo:[0,1]
	s_barrier
	v_pk_add_f32 v[38:39], v[38:39], v[64:65] op_sel:[1,0] op_sel_hi:[0,1] neg_lo:[0,1] neg_hi:[1,1]
	v_pk_mul_f32 v[64:65], v[44:45], v[42:43] op_sel:[0,0] op_sel_hi:[0,1]
	v_pk_fma_f32 v[64:65], v[44:45], v[42:43], v[64:65] op_sel:[1,1,0] op_sel_hi:[1,0,1] neg_hi:[0,1,0]
	v_pk_add_f32 v[42:43], v[68:69], v[48:49] neg_hi:[0,1]
	v_pk_add_f32 v[44:45], v[68:69], v[48:49] neg_lo:[0,1]
	s_nop 0
	v_pk_mul_f32 v[48:49], v[42:43], v[44:45] op_sel:[0,0] op_sel_hi:[0,1]
	v_pk_fma_f32 v[48:49], v[42:43], v[44:45], v[48:49] op_sel:[1,1,0] op_sel_hi:[1,0,1] neg_hi:[0,1,0]
	v_pk_add_f32 v[42:43], v[70:71], v[46:47] neg_hi:[0,1]
	v_pk_add_f32 v[44:45], v[70:71], v[46:47] neg_lo:[0,1]
	v_pk_add_f32 v[36:37], v[36:37], v[64:65] op_sel:[1,0] op_sel_hi:[0,1] neg_lo:[0,1] neg_hi:[1,1]
	s_nop 0
	v_pk_mul_f32 v[46:47], v[42:43], v[44:45] op_sel:[0,0] op_sel_hi:[0,1]
	v_pk_fma_f32 v[46:47], v[42:43], v[44:45], v[46:47] op_sel:[1,1,0] op_sel_hi:[1,0,1] neg_hi:[0,1,0]
	v_pk_add_f32 v[42:43], v[62:63], v[52:53]
	v_pk_add_f32 v[32:33], v[32:33], v[46:47] op_sel:[1,0] op_sel_hi:[0,1] neg_lo:[0,1] neg_hi:[1,1]
	v_pk_add_f32 v[44:45], v[62:63], v[52:53] neg_lo:[0,1] neg_hi:[0,1]
	v_pk_add_f32 v[46:47], v[54:55], v[38:39]
	v_pk_add_f32 v[38:39], v[54:55], v[38:39] neg_lo:[0,1] neg_hi:[0,1]
	v_pk_add_f32 v[34:35], v[34:35], v[48:49] op_sel:[1,0] op_sel_hi:[0,1] neg_lo:[0,1] neg_hi:[1,1]
	v_pk_add_f32 v[48:49], v[42:43], v[46:47]
	v_pk_add_f32 v[42:43], v[42:43], v[46:47] neg_lo:[0,1] neg_hi:[0,1]
	v_pk_add_f32 v[46:47], v[44:45], v[38:39] op_sel:[0,1] op_sel_hi:[1,0] neg_hi:[0,1]
	v_pk_add_f32 v[38:39], v[44:45], v[38:39] op_sel:[0,1] op_sel_hi:[1,0] neg_lo:[0,1]
	v_pk_add_f32 v[44:45], v[60:61], v[50:51]
	v_pk_add_f32 v[50:51], v[60:61], v[50:51] neg_lo:[0,1] neg_hi:[0,1]
	v_pk_add_f32 v[52:53], v[88:89], v[36:37]
	v_pk_add_f32 v[36:37], v[88:89], v[36:37] neg_lo:[0,1] neg_hi:[0,1]
	v_pk_add_f32 v[54:55], v[44:45], v[52:53]
	v_pk_add_f32 v[44:45], v[44:45], v[52:53] neg_lo:[0,1] neg_hi:[0,1]
	v_pk_add_f32 v[52:53], v[50:51], v[36:37] op_sel:[0,1] op_sel_hi:[1,0] neg_hi:[0,1]
	v_pk_add_f32 v[36:37], v[50:51], v[36:37] op_sel:[0,1] op_sel_hi:[1,0] neg_lo:[0,1]
	v_pk_add_f32 v[50:51], v[58:59], v[72:73]
	v_pk_add_f32 v[58:59], v[58:59], v[72:73] neg_lo:[0,1] neg_hi:[0,1]
	v_pk_add_f32 v[60:61], v[86:87], v[34:35]
	v_pk_add_f32 v[34:35], v[86:87], v[34:35] neg_lo:[0,1] neg_hi:[0,1]
	v_pk_add_f32 v[62:63], v[50:51], v[60:61]
	v_pk_add_f32 v[50:51], v[50:51], v[60:61] neg_lo:[0,1] neg_hi:[0,1]
	v_pk_add_f32 v[60:61], v[58:59], v[34:35] op_sel:[0,1] op_sel_hi:[1,0] neg_hi:[0,1]
	v_pk_add_f32 v[34:35], v[58:59], v[34:35] op_sel:[0,1] op_sel_hi:[1,0] neg_lo:[0,1]
	v_pk_add_f32 v[58:59], v[56:57], v[40:41]
	v_pk_add_f32 v[40:41], v[56:57], v[40:41] neg_lo:[0,1] neg_hi:[0,1]
	v_pk_add_f32 v[56:57], v[84:85], v[32:33]
	v_pk_add_f32 v[32:33], v[84:85], v[32:33] neg_lo:[0,1] neg_hi:[0,1]
	v_pk_add_f32 v[64:65], v[58:59], v[56:57]
	v_pk_add_f32 v[56:57], v[58:59], v[56:57] neg_lo:[0,1] neg_hi:[0,1]
	v_pk_add_f32 v[58:59], v[40:41], v[32:33] op_sel:[0,1] op_sel_hi:[1,0] neg_hi:[0,1]
	v_pk_add_f32 v[32:33], v[40:41], v[32:33] op_sel:[0,1] op_sel_hi:[1,0] neg_lo:[0,1]
	v_pk_mul_f32 v[40:41], v[52:53], s[6:7] op_sel:[0,0] op_sel_hi:[0,1]
	v_pk_fma_f32 v[40:41], v[52:53], s[6:7], v[40:41] op_sel:[1,1,0] op_sel_hi:[1,0,1] neg_lo:[0,1,0]
	v_pk_mul_f32 v[52:53], v[36:37], s[10:11] op_sel:[0,0] op_sel_hi:[0,1]
	v_pk_fma_f32 v[52:53], v[36:37], s[10:11], v[52:53] op_sel:[1,1,0] op_sel_hi:[1,0,1] neg_lo:[0,1,0]
	v_pk_add_f32 v[36:37], v[60:61], v[60:61] op_sel:[0,1] op_sel_hi:[1,0] neg_hi:[0,1]
	v_pk_add_f32 v[44:45], v[44:45], v[44:45] op_sel:[0,1] op_sel_hi:[1,0] neg_hi:[0,1]
	s_nop 0
	v_pk_mul_f32 v[60:61], v[58:59], s[10:11] op_sel:[0,0] op_sel_hi:[0,1]
	v_pk_fma_f32 v[60:61], v[58:59], s[10:11], v[60:61] op_sel:[1,1,0] op_sel_hi:[1,0,1] neg_lo:[0,1,0]
	v_pk_mul_f32 v[58:59], v[32:33], s[14:15] op_sel:[0,0] op_sel_hi:[0,1]
	v_pk_fma_f32 v[58:59], v[32:33], s[14:15], v[58:59] op_sel:[1,1,0] op_sel_hi:[1,0,1] neg_lo:[0,1,0]
	v_pk_add_f32 v[32:33], v[48:49], v[62:63]
	v_pk_mul_f32 v[36:37], v[36:37], s[8:9]
	v_pk_add_f32 v[48:49], v[48:49], v[62:63] neg_lo:[0,1] neg_hi:[0,1]
	v_pk_add_f32 v[62:63], v[54:55], v[64:65]
	v_pk_add_f32 v[54:55], v[54:55], v[64:65] neg_lo:[0,1] neg_hi:[0,1]
	v_pk_mul_f32 v[44:45], v[44:45], s[8:9]
	v_pk_add_f32 v[34:35], v[34:35], v[34:35] op_sel:[0,1] op_sel_hi:[1,0] neg_lo:[0,1]
	v_pk_add_f32 v[56:57], v[56:57], v[56:57] op_sel:[0,1] op_sel_hi:[1,0] neg_lo:[0,1]
	v_pk_add_f32 v[64:65], v[32:33], v[62:63]
	v_pk_add_f32 v[32:33], v[32:33], v[62:63] neg_lo:[0,1] neg_hi:[0,1]
	v_pk_add_f32 v[62:63], v[48:49], v[54:55] op_sel:[0,1] op_sel_hi:[1,0] neg_hi:[0,1]
	v_pk_add_f32 v[48:49], v[48:49], v[54:55] op_sel:[0,1] op_sel_hi:[1,0] neg_lo:[0,1]
	v_pk_add_f32 v[54:55], v[46:47], v[36:37]
	v_pk_add_f32 v[36:37], v[46:47], v[36:37] neg_lo:[0,1] neg_hi:[0,1]
	v_pk_add_f32 v[46:47], v[40:41], v[60:61]
	v_pk_add_f32 v[40:41], v[40:41], v[60:61] neg_lo:[0,1] neg_hi:[0,1]
	v_pk_mul_f32 v[34:35], v[34:35], s[12:13]
	v_pk_mul_f32 v[56:57], v[56:57], s[12:13]
	v_pk_add_f32 v[60:61], v[54:55], v[46:47]
	v_pk_add_f32 v[46:47], v[54:55], v[46:47] neg_lo:[0,1] neg_hi:[0,1]
	v_pk_add_f32 v[54:55], v[36:37], v[40:41] op_sel:[0,1] op_sel_hi:[1,0] neg_hi:[0,1]
	v_pk_add_f32 v[36:37], v[36:37], v[40:41] op_sel:[0,1] op_sel_hi:[1,0] neg_lo:[0,1]
	v_pk_add_f32 v[40:41], v[42:43], v[50:51] op_sel:[0,1] op_sel_hi:[1,0] neg_hi:[0,1]
	v_pk_add_f32 v[42:43], v[42:43], v[50:51] op_sel:[0,1] op_sel_hi:[1,0] neg_lo:[0,1]
	v_pk_add_f32 v[50:51], v[44:45], v[56:57]
	v_pk_add_f32 v[44:45], v[44:45], v[56:57] neg_lo:[0,1] neg_hi:[0,1]
	v_pk_add_f32 v[56:57], v[50:51], v[40:41]
	v_pk_add_f32 v[40:41], v[40:41], v[50:51] neg_lo:[0,1] neg_hi:[0,1]
	v_pk_add_f32 v[50:51], v[42:43], v[44:45] op_sel:[0,1] op_sel_hi:[1,0] neg_hi:[0,1]
	v_pk_add_f32 v[42:43], v[42:43], v[44:45] op_sel:[0,1] op_sel_hi:[1,0] neg_lo:[0,1]
	v_pk_add_f32 v[44:45], v[38:39], v[34:35]
	v_pk_add_f32 v[34:35], v[38:39], v[34:35] neg_lo:[0,1] neg_hi:[0,1]
	v_pk_add_f32 v[38:39], v[52:53], v[58:59]
	v_pk_add_f32 v[52:53], v[52:53], v[58:59] neg_lo:[0,1] neg_hi:[0,1]
	v_pk_add_f32 v[58:59], v[44:45], v[38:39]
	v_pk_add_f32 v[38:39], v[44:45], v[38:39] neg_lo:[0,1] neg_hi:[0,1]
	v_pk_add_f32 v[44:45], v[34:35], v[52:53] op_sel:[0,1] op_sel_hi:[1,0] neg_hi:[0,1]
	v_pk_add_f32 v[34:35], v[34:35], v[52:53] op_sel:[0,1] op_sel_hi:[1,0] neg_lo:[0,1]
	v_pk_mul_f32 v[52:53], v[60:61], v[30:31] op_sel:[0,0] op_sel_hi:[0,1]
	v_pk_fma_f32 v[52:53], v[60:61], v[30:31], v[52:53] op_sel:[1,1,0] op_sel_hi:[1,0,1] neg_lo:[0,1,0]
	v_pk_mul_f32 v[30:31], v[56:57], v[28:29] op_sel:[0,0] op_sel_hi:[0,1]
	v_pk_fma_f32 v[30:31], v[56:57], v[28:29], v[30:31] op_sel:[1,1,0] op_sel_hi:[1,0,1] neg_lo:[0,1,0]
	v_pk_mul_f32 v[28:29], v[58:59], v[26:27] op_sel:[0,0] op_sel_hi:[0,1]
	v_pk_fma_f32 v[28:29], v[58:59], v[26:27], v[28:29] op_sel:[1,1,0] op_sel_hi:[1,0,1] neg_lo:[0,1,0]
	v_pk_mul_f32 v[26:27], v[62:63], v[24:25] op_sel:[0,0] op_sel_hi:[0,1]
	v_pk_fma_f32 v[26:27], v[62:63], v[24:25], v[26:27] op_sel:[1,1,0] op_sel_hi:[1,0,1] neg_lo:[0,1,0]
	v_pk_mul_f32 v[24:25], v[54:55], v[20:21] op_sel:[0,0] op_sel_hi:[0,1]
	v_pk_fma_f32 v[24:25], v[54:55], v[20:21], v[24:25] op_sel:[1,1,0] op_sel_hi:[1,0,1] neg_lo:[0,1,0]
	v_pk_mul_f32 v[20:21], v[50:51], v[16:17] op_sel:[0,0] op_sel_hi:[0,1]
	v_pk_fma_f32 v[20:21], v[50:51], v[16:17], v[20:21] op_sel:[1,1,0] op_sel_hi:[1,0,1] neg_lo:[0,1,0]
	s_nop 0
	v_pk_mul_f32 v[16:17], v[44:45], v[10:11] op_sel:[0,0] op_sel_hi:[0,1]
	v_pk_fma_f32 v[16:17], v[44:45], v[10:11], v[16:17] op_sel:[1,1,0] op_sel_hi:[1,0,1] neg_lo:[0,1,0]
	v_pk_mul_f32 v[10:11], v[32:33], v[22:23] op_sel:[0,0] op_sel_hi:[0,1]
	v_pk_fma_f32 v[10:11], v[32:33], v[22:23], v[10:11] op_sel:[1,1,0] op_sel_hi:[1,0,1] neg_lo:[0,1,0]
	ds_write_b64 v1, v[10:11] offset:17472
	v_pk_mul_f32 v[10:11], v[46:47], v[18:19] op_sel:[0,0] op_sel_hi:[0,1]
	v_pk_fma_f32 v[10:11], v[46:47], v[18:19], v[10:11] op_sel:[1,1,0] op_sel_hi:[1,0,1] neg_lo:[0,1,0]
	ds_write_b64 v1, v[10:11] offset:19656
	v_pk_mul_f32 v[10:11], v[40:41], v[12:13] op_sel:[0,0] op_sel_hi:[0,1]
	v_pk_fma_f32 v[10:11], v[40:41], v[12:13], v[10:11] op_sel:[1,1,0] op_sel_hi:[1,0,1] neg_lo:[0,1,0]
	ds_write_b64 v1, v[10:11] offset:21840
	v_pk_mul_f32 v[10:11], v[38:39], v[14:15] op_sel:[0,0] op_sel_hi:[0,1]
	v_pk_fma_f32 v[10:11], v[38:39], v[14:15], v[10:11] op_sel:[1,1,0] op_sel_hi:[1,0,1] neg_lo:[0,1,0]
	ds_write_b64 v1, v[10:11] offset:24024
	v_pk_mul_f32 v[10:11], v[48:49], v[6:7] op_sel:[0,0] op_sel_hi:[0,1]
	v_pk_fma_f32 v[10:11], v[48:49], v[6:7], v[10:11] op_sel:[1,1,0] op_sel_hi:[1,0,1] neg_lo:[0,1,0]
	v_pk_mul_f32 v[6:7], v[36:37], v[8:9] op_sel:[0,0] op_sel_hi:[0,1]
	v_pk_fma_f32 v[6:7], v[36:37], v[8:9], v[6:7] op_sel:[1,1,0] op_sel_hi:[1,0,1] neg_lo:[0,1,0]
	ds_write_b64 v1, v[6:7] offset:28392
	v_pk_mul_f32 v[6:7], v[42:43], v[4:5] op_sel:[0,0] op_sel_hi:[0,1]
	v_pk_fma_f32 v[6:7], v[42:43], v[4:5], v[6:7] op_sel:[1,1,0] op_sel_hi:[1,0,1] neg_lo:[0,1,0]
	v_pk_mul_f32 v[4:5], v[34:35], v[2:3] op_sel:[0,0] op_sel_hi:[0,1]
	v_pk_fma_f32 v[4:5], v[34:35], v[2:3], v[4:5] op_sel:[1,1,0] op_sel_hi:[1,0,1] neg_lo:[0,1,0]
	ds_write_b64 v1, v[64:65]
	ds_write_b64 v1, v[52:53] offset:2184
	ds_write_b64 v1, v[30:31] offset:4368
	ds_write_b64 v1, v[28:29] offset:6552
	ds_write_b64 v1, v[26:27] offset:8736
	ds_write_b64 v1, v[24:25] offset:10920
	ds_write_b64 v1, v[20:21] offset:13104
	ds_write_b64 v1, v[16:17] offset:15288
	ds_write_b64 v1, v[10:11] offset:26208
	ds_write_b64 v1, v[6:7] offset:30576
	ds_write_b64 v1, v[4:5] offset:32760
	s_waitcnt lgkmcnt(0)
	s_barrier
	ds_read2_b64 v[2:5], v96 offset1:16
	ds_read2_b64 v[6:9], v96 offset0:32 offset1:48
	ds_read2_b64 v[10:13], v96 offset0:64 offset1:80
	ds_read2_b64 v[14:17], v96 offset0:128 offset1:144
	ds_read2_b64 v[18:21], v96 offset0:96 offset1:112
	ds_read2_b64 v[22:25], v96 offset0:192 offset1:208
	ds_read2_b64 v[26:29], v96 offset0:160 offset1:176
	ds_read2_b64 v[30:33], v96 offset0:224 offset1:240
	s_waitcnt lgkmcnt(4)
	v_pk_add_f32 v[34:35], v[2:3], v[14:15]
	v_pk_add_f32 v[2:3], v[2:3], v[14:15] neg_lo:[0,1] neg_hi:[0,1]
	s_waitcnt lgkmcnt(2)
	v_pk_add_f32 v[14:15], v[10:11], v[22:23]
	v_pk_add_f32 v[10:11], v[10:11], v[22:23] neg_lo:[0,1] neg_hi:[0,1]
	v_pk_add_f32 v[22:23], v[34:35], v[14:15]
	v_pk_add_f32 v[14:15], v[34:35], v[14:15] neg_lo:[0,1] neg_hi:[0,1]
	v_pk_add_f32 v[34:35], v[2:3], v[10:11] op_sel:[0,1] op_sel_hi:[1,0] neg_hi:[0,1]
	v_pk_add_f32 v[2:3], v[2:3], v[10:11] op_sel:[0,1] op_sel_hi:[1,0] neg_lo:[0,1]
	v_pk_add_f32 v[10:11], v[4:5], v[16:17]
	v_pk_add_f32 v[4:5], v[4:5], v[16:17] neg_lo:[0,1] neg_hi:[0,1]
	v_pk_add_f32 v[16:17], v[12:13], v[24:25]
	v_pk_add_f32 v[12:13], v[12:13], v[24:25] neg_lo:[0,1] neg_hi:[0,1]
	v_pk_add_f32 v[24:25], v[10:11], v[16:17]
	v_pk_add_f32 v[10:11], v[10:11], v[16:17] neg_lo:[0,1] neg_hi:[0,1]
	v_pk_add_f32 v[16:17], v[4:5], v[12:13] op_sel:[0,1] op_sel_hi:[1,0] neg_hi:[0,1]
	v_pk_add_f32 v[4:5], v[4:5], v[12:13] op_sel:[0,1] op_sel_hi:[1,0] neg_lo:[0,1]
	s_waitcnt lgkmcnt(1)
	v_pk_add_f32 v[12:13], v[6:7], v[26:27]
	v_pk_add_f32 v[6:7], v[6:7], v[26:27] neg_lo:[0,1] neg_hi:[0,1]
	s_waitcnt lgkmcnt(0)
	v_pk_add_f32 v[26:27], v[18:19], v[30:31]
	v_pk_add_f32 v[18:19], v[18:19], v[30:31] neg_lo:[0,1] neg_hi:[0,1]
	v_pk_add_f32 v[30:31], v[12:13], v[26:27]
	v_pk_add_f32 v[12:13], v[12:13], v[26:27] neg_lo:[0,1] neg_hi:[0,1]
	v_pk_add_f32 v[26:27], v[6:7], v[18:19] op_sel:[0,1] op_sel_hi:[1,0] neg_hi:[0,1]
	v_pk_add_f32 v[6:7], v[6:7], v[18:19] op_sel:[0,1] op_sel_hi:[1,0] neg_lo:[0,1]
	v_pk_add_f32 v[18:19], v[8:9], v[28:29]
	v_pk_add_f32 v[8:9], v[8:9], v[28:29] neg_lo:[0,1] neg_hi:[0,1]
	v_pk_add_f32 v[28:29], v[20:21], v[32:33]
	v_pk_add_f32 v[20:21], v[20:21], v[32:33] neg_lo:[0,1] neg_hi:[0,1]
	v_pk_add_f32 v[32:33], v[18:19], v[28:29]
	v_pk_add_f32 v[18:19], v[18:19], v[28:29] neg_lo:[0,1] neg_hi:[0,1]
	v_pk_add_f32 v[28:29], v[8:9], v[20:21] op_sel:[0,1] op_sel_hi:[1,0] neg_hi:[0,1]
	v_pk_add_f32 v[8:9], v[8:9], v[20:21] op_sel:[0,1] op_sel_hi:[1,0] neg_lo:[0,1]
	v_pk_mul_f32 v[20:21], v[16:17], s[6:7] op_sel:[0,0] op_sel_hi:[0,1]
	v_pk_fma_f32 v[20:21], v[16:17], s[6:7], v[20:21] op_sel:[1,1,0] op_sel_hi:[1,0,1] neg_lo:[0,1,0]
	v_pk_mul_f32 v[16:17], v[4:5], s[10:11] op_sel:[0,0] op_sel_hi:[0,1]
	v_pk_fma_f32 v[16:17], v[4:5], s[10:11], v[16:17] op_sel:[1,1,0] op_sel_hi:[1,0,1] neg_lo:[0,1,0]
	v_pk_add_f32 v[4:5], v[26:27], v[26:27] op_sel:[0,1] op_sel_hi:[1,0] neg_hi:[0,1]
	v_pk_add_f32 v[10:11], v[10:11], v[10:11] op_sel:[0,1] op_sel_hi:[1,0] neg_hi:[0,1]
	s_nop 0
	v_pk_mul_f32 v[26:27], v[28:29], s[10:11] op_sel:[0,0] op_sel_hi:[0,1]
	v_pk_fma_f32 v[26:27], v[28:29], s[10:11], v[26:27] op_sel:[1,1,0] op_sel_hi:[1,0,1] neg_lo:[0,1,0]
	v_pk_mul_f32 v[28:29], v[8:9], s[14:15] op_sel:[0,0] op_sel_hi:[0,1]
	v_pk_fma_f32 v[28:29], v[8:9], s[14:15], v[28:29] op_sel:[1,1,0] op_sel_hi:[1,0,1] neg_lo:[0,1,0]
	v_pk_add_f32 v[8:9], v[22:23], v[30:31]
	v_pk_mul_f32 v[4:5], v[4:5], s[8:9]
	v_pk_add_f32 v[22:23], v[22:23], v[30:31] neg_lo:[0,1] neg_hi:[0,1]
	v_pk_add_f32 v[30:31], v[24:25], v[32:33]
	v_pk_add_f32 v[24:25], v[24:25], v[32:33] neg_lo:[0,1] neg_hi:[0,1]
	v_pk_add_f32 v[18:19], v[18:19], v[18:19] op_sel:[0,1] op_sel_hi:[1,0] neg_lo:[0,1]
	v_pk_add_f32 v[32:33], v[8:9], v[30:31]
	v_pk_add_f32 v[30:31], v[8:9], v[30:31] neg_lo:[0,1] neg_hi:[0,1]
	v_pk_add_f32 v[36:37], v[22:23], v[24:25] op_sel:[0,1] op_sel_hi:[1,0] neg_hi:[0,1]
	v_pk_add_f32 v[22:23], v[22:23], v[24:25] op_sel:[0,1] op_sel_hi:[1,0] neg_lo:[0,1]
	v_pk_add_f32 v[8:9], v[34:35], v[4:5]
	v_pk_add_f32 v[4:5], v[34:35], v[4:5] neg_lo:[0,1] neg_hi:[0,1]
	v_pk_add_f32 v[24:25], v[20:21], v[26:27]
	v_pk_add_f32 v[20:21], v[20:21], v[26:27] neg_lo:[0,1] neg_hi:[0,1]
	v_pk_mul_f32 v[10:11], v[10:11], s[8:9]
	v_pk_add_f32 v[6:7], v[6:7], v[6:7] op_sel:[0,1] op_sel_hi:[1,0] neg_lo:[0,1]
	v_pk_mul_f32 v[18:19], v[18:19], s[12:13]
	v_pk_add_f32 v[26:27], v[8:9], v[24:25]
	v_pk_add_f32 v[24:25], v[8:9], v[24:25] neg_lo:[0,1] neg_hi:[0,1]
	v_pk_add_f32 v[34:35], v[4:5], v[20:21] op_sel:[0,1] op_sel_hi:[1,0] neg_hi:[0,1]
	v_pk_add_f32 v[20:21], v[4:5], v[20:21] op_sel:[0,1] op_sel_hi:[1,0] neg_lo:[0,1]
	v_pk_add_f32 v[4:5], v[14:15], v[12:13] op_sel:[0,1] op_sel_hi:[1,0] neg_hi:[0,1]
	v_pk_add_f32 v[8:9], v[14:15], v[12:13] op_sel:[0,1] op_sel_hi:[1,0] neg_lo:[0,1]
	v_pk_add_f32 v[12:13], v[10:11], v[18:19]
	v_pk_mul_f32 v[6:7], v[6:7], s[12:13]
	v_pk_add_f32 v[10:11], v[10:11], v[18:19] neg_lo:[0,1] neg_hi:[0,1]
	v_pk_add_f32 v[14:15], v[12:13], v[4:5]
	v_pk_add_f32 v[12:13], v[4:5], v[12:13] neg_lo:[0,1] neg_hi:[0,1]
	v_pk_add_f32 v[4:5], v[2:3], v[6:7]
	v_pk_add_f32 v[2:3], v[2:3], v[6:7] neg_lo:[0,1] neg_hi:[0,1]
	v_mov_b32_e32 v1, v0
	v_pk_add_f32 v[18:19], v[8:9], v[10:11] op_sel:[0,1] op_sel_hi:[1,0] neg_hi:[0,1]
	v_pk_add_f32 v[10:11], v[8:9], v[10:11] op_sel:[0,1] op_sel_hi:[1,0] neg_lo:[0,1]
	v_pk_add_f32 v[8:9], v[16:17], v[28:29] neg_lo:[0,1] neg_hi:[0,1]
	v_pk_add_f32 v[6:7], v[16:17], v[28:29]
	v_pk_add_f32 v[38:39], v[2:3], v[8:9] op_sel:[0,1] op_sel_hi:[1,0] neg_hi:[0,1]
	v_pk_add_f32 v[40:41], v[2:3], v[8:9] op_sel:[0,1] op_sel_hi:[1,0] neg_lo:[0,1]
	v_ashrrev_i32_e32 v2, 4, v1
	v_lshlrev_b32_e32 v44, 3, v2
	v_add_u32_e32 v45, 0x8800, v44
	v_and_b32_e32 v1, 15, v1
	v_pk_add_f32 v[16:17], v[4:5], v[6:7]
	v_pk_add_f32 v[28:29], v[4:5], v[6:7] neg_lo:[0,1] neg_hi:[0,1]
	ds_read2_b64 v[2:5], v45 offset0:16 offset1:32
	v_mad_u32_u24 v1, v1, s5, v44
	ds_read2_b64 v[6:9], v45 offset0:48 offset1:64
	s_waitcnt lgkmcnt(1)
	v_pk_mul_f32 v[42:43], v[26:27], v[2:3] op_sel:[0,0] op_sel_hi:[0,1]
	v_pk_fma_f32 v[42:43], v[26:27], v[2:3], v[42:43] op_sel:[1,1,0] op_sel_hi:[1,0,1] neg_lo:[0,1,0]
	v_pk_mul_f32 v[26:27], v[14:15], v[4:5] op_sel:[0,0] op_sel_hi:[0,1]
	v_pk_fma_f32 v[26:27], v[14:15], v[4:5], v[26:27] op_sel:[1,1,0] op_sel_hi:[1,0,1] neg_lo:[0,1,0]
	s_waitcnt lgkmcnt(0)
	v_pk_mul_f32 v[14:15], v[16:17], v[6:7] op_sel:[0,0] op_sel_hi:[0,1]
	v_pk_fma_f32 v[14:15], v[16:17], v[6:7], v[14:15] op_sel:[1,1,0] op_sel_hi:[1,0,1] neg_lo:[0,1,0]
	ds_write2_b64 v1, v[26:27], v[14:15] offset0:32 offset1:48
	v_pk_mul_f32 v[14:15], v[36:37], v[8:9] op_sel:[0,0] op_sel_hi:[0,1]
	v_pk_fma_f32 v[14:15], v[36:37], v[8:9], v[14:15] op_sel:[1,1,0] op_sel_hi:[1,0,1] neg_lo:[0,1,0]
	ds_read2_b64 v[2:5], v45 offset0:80 offset1:96
	s_waitcnt lgkmcnt(0)
	v_pk_mul_f32 v[16:17], v[34:35], v[2:3] op_sel:[0,0] op_sel_hi:[0,1]
	v_pk_fma_f32 v[16:17], v[34:35], v[2:3], v[16:17] op_sel:[1,1,0] op_sel_hi:[1,0,1] neg_lo:[0,1,0]
	ds_write2_b64 v1, v[14:15], v[16:17] offset0:64 offset1:80
	v_pk_mul_f32 v[14:15], v[18:19], v[4:5] op_sel:[0,0] op_sel_hi:[0,1]
	v_pk_fma_f32 v[14:15], v[18:19], v[4:5], v[14:15] op_sel:[1,1,0] op_sel_hi:[1,0,1] neg_lo:[0,1,0]
	ds_read2_b64 v[6:9], v45 offset0:112 offset1:128
	ds_read2_b64 v[2:5], v45 offset0:144 offset1:160
	s_waitcnt lgkmcnt(1)
	v_pk_mul_f32 v[16:17], v[38:39], v[6:7] op_sel:[0,0] op_sel_hi:[0,1]
	v_pk_fma_f32 v[16:17], v[38:39], v[6:7], v[16:17] op_sel:[1,1,0] op_sel_hi:[1,0,1] neg_lo:[0,1,0]
	ds_write2_b64 v1, v[14:15], v[16:17] offset0:96 offset1:112
	v_pk_mul_f32 v[14:15], v[30:31], v[8:9] op_sel:[0,0] op_sel_hi:[0,1]
	v_pk_fma_f32 v[14:15], v[30:31], v[8:9], v[14:15] op_sel:[1,1,0] op_sel_hi:[1,0,1] neg_lo:[0,1,0]
	ds_read2_b64 v[6:9], v45 offset0:176 offset1:192
	s_waitcnt lgkmcnt(2)
	v_pk_mul_f32 v[16:17], v[24:25], v[2:3] op_sel:[0,0] op_sel_hi:[0,1]
	v_pk_fma_f32 v[16:17], v[24:25], v[2:3], v[16:17] op_sel:[1,1,0] op_sel_hi:[1,0,1] neg_lo:[0,1,0]
	ds_write2_b64 v1, v[14:15], v[16:17] offset0:128 offset1:144
	v_pk_mul_f32 v[14:15], v[12:13], v[4:5] op_sel:[0,0] op_sel_hi:[0,1]
	v_pk_fma_f32 v[14:15], v[12:13], v[4:5], v[14:15] op_sel:[1,1,0] op_sel_hi:[1,0,1] neg_lo:[0,1,0]
	ds_read2_b64 v[2:5], v45 offset0:208 offset1:224
	s_waitcnt lgkmcnt(2)
	v_pk_mul_f32 v[12:13], v[28:29], v[6:7] op_sel:[0,0] op_sel_hi:[0,1]
	v_pk_fma_f32 v[12:13], v[28:29], v[6:7], v[12:13] op_sel:[1,1,0] op_sel_hi:[1,0,1] neg_lo:[0,1,0]
	ds_write2_b64 v1, v[32:33], v[42:43] offset1:16
	ds_write2_b64 v1, v[14:15], v[12:13] offset0:160 offset1:176
	ds_read_b64 v[6:7], v44 offset:36736
	v_pk_mul_f32 v[12:13], v[22:23], v[8:9] op_sel:[0,0] op_sel_hi:[0,1]
	v_pk_fma_f32 v[12:13], v[22:23], v[8:9], v[12:13] op_sel:[1,1,0] op_sel_hi:[1,0,1] neg_lo:[0,1,0]
	s_waitcnt lgkmcnt(3)
	v_pk_mul_f32 v[8:9], v[20:21], v[2:3] op_sel:[0,0] op_sel_hi:[0,1]
	v_pk_fma_f32 v[8:9], v[20:21], v[2:3], v[8:9] op_sel:[1,1,0] op_sel_hi:[1,0,1] neg_lo:[0,1,0]
	ds_write2_b64 v1, v[12:13], v[8:9] offset0:192 offset1:208
	v_pk_mul_f32 v[2:3], v[10:11], v[4:5] op_sel:[0,0] op_sel_hi:[0,1]
	v_pk_fma_f32 v[2:3], v[10:11], v[4:5], v[2:3] op_sel:[1,1,0] op_sel_hi:[1,0,1] neg_lo:[0,1,0]
	s_waitcnt lgkmcnt(1)
	v_pk_mul_f32 v[4:5], v[40:41], v[6:7] op_sel:[0,0] op_sel_hi:[0,1]
	v_pk_fma_f32 v[4:5], v[40:41], v[6:7], v[4:5] op_sel:[1,1,0] op_sel_hi:[1,0,1] neg_lo:[0,1,0]
	ds_write2_b64 v1, v[2:3], v[4:5] offset0:224 offset1:240
	v_mov_b32_e32 v1, v0
	s_waitcnt lgkmcnt(0)
	s_barrier
	v_mov_b32_e32 v53, 0
	v_and_b32_e32 v2, 15, v1
	v_and_b32_e32 v1, 0x1ffffff0, v1
	v_lshlrev_b32_e32 v1, 3, v1
	v_mad_u32_u24 v1, v2, s5, v1
	ds_read2_b64 v[2:5], v1 offset1:1
	ds_read2_b64 v[6:9], v1 offset0:2 offset1:3
	ds_read2_b64 v[10:13], v1 offset0:8 offset1:9
	ds_read2_b64 v[18:21], v1 offset0:4 offset1:5
	ds_read2_b64 v[22:25], v1 offset0:6 offset1:7
	ds_read2_b64 v[26:29], v1 offset0:12 offset1:13
	ds_read2_b64 v[30:33], v1 offset0:10 offset1:11
	ds_read2_b64 v[34:37], v1 offset0:14 offset1:15
	s_waitcnt lgkmcnt(5)
	v_pk_add_f32 v[14:15], v[2:3], v[10:11]
	v_pk_add_f32 v[2:3], v[2:3], v[10:11] neg_lo:[0,1] neg_hi:[0,1]
	s_waitcnt lgkmcnt(2)
	v_pk_add_f32 v[10:11], v[18:19], v[26:27]
	v_pk_add_f32 v[18:19], v[18:19], v[26:27] neg_lo:[0,1] neg_hi:[0,1]
	v_pk_add_f32 v[26:27], v[14:15], v[10:11]
	v_pk_add_f32 v[16:17], v[14:15], v[10:11] neg_lo:[0,1] neg_hi:[0,1]
	v_pk_add_f32 v[14:15], v[2:3], v[18:19] op_sel:[0,1] op_sel_hi:[1,0] neg_hi:[0,1]
	v_pk_add_f32 v[18:19], v[2:3], v[18:19] op_sel:[0,1] op_sel_hi:[1,0] neg_lo:[0,1]
	v_pk_add_f32 v[2:3], v[4:5], v[12:13]
	v_pk_add_f32 v[10:11], v[20:21], v[28:29]
	v_pk_add_f32 v[4:5], v[4:5], v[12:13] neg_lo:[0,1] neg_hi:[0,1]
	v_pk_add_f32 v[12:13], v[20:21], v[28:29] neg_lo:[0,1] neg_hi:[0,1]
	v_pk_add_f32 v[28:29], v[2:3], v[10:11]
	v_pk_add_f32 v[2:3], v[2:3], v[10:11] neg_lo:[0,1] neg_hi:[0,1]
	v_pk_add_f32 v[10:11], v[4:5], v[12:13] op_sel:[0,1] op_sel_hi:[1,0] neg_hi:[0,1]
	v_pk_add_f32 v[4:5], v[4:5], v[12:13] op_sel:[0,1] op_sel_hi:[1,0] neg_lo:[0,1]
	s_waitcnt lgkmcnt(1)
	v_pk_add_f32 v[12:13], v[6:7], v[30:31]
	s_waitcnt lgkmcnt(0)
	v_pk_add_f32 v[20:21], v[22:23], v[34:35]
	v_pk_add_f32 v[2:3], v[2:3], v[2:3] op_sel:[0,1] op_sel_hi:[1,0] neg_hi:[0,1]
	v_pk_add_f32 v[6:7], v[6:7], v[30:31] neg_lo:[0,1] neg_hi:[0,1]
	v_pk_add_f32 v[22:23], v[22:23], v[34:35] neg_lo:[0,1] neg_hi:[0,1]
	v_pk_add_f32 v[30:31], v[12:13], v[20:21]
	v_pk_add_f32 v[20:21], v[12:13], v[20:21] neg_lo:[0,1] neg_hi:[0,1]
	v_pk_add_f32 v[12:13], v[6:7], v[22:23] op_sel:[0,1] op_sel_hi:[1,0] neg_hi:[0,1]
	v_pk_mul_f32 v[44:45], v[2:3], s[8:9]
	v_pk_add_f32 v[6:7], v[6:7], v[22:23] op_sel:[0,1] op_sel_hi:[1,0] neg_lo:[0,1]
	v_pk_add_f32 v[22:23], v[8:9], v[32:33]
	v_pk_add_f32 v[2:3], v[12:13], v[12:13] op_sel:[0,1] op_sel_hi:[1,0] neg_hi:[0,1]
	v_pk_add_f32 v[8:9], v[8:9], v[32:33] neg_lo:[0,1] neg_hi:[0,1]
	v_pk_add_f32 v[32:33], v[24:25], v[36:37]
	v_pk_mul_f32 v[12:13], v[2:3], s[8:9]
	v_pk_add_f32 v[2:3], v[6:7], v[6:7] op_sel:[0,1] op_sel_hi:[1,0] neg_lo:[0,1]
	v_pk_add_f32 v[24:25], v[24:25], v[36:37] neg_lo:[0,1] neg_hi:[0,1]
	v_pk_add_f32 v[34:35], v[22:23], v[32:33]
	v_pk_add_f32 v[32:33], v[22:23], v[32:33] neg_lo:[0,1] neg_hi:[0,1]
	v_pk_mul_f32 v[54:55], v[2:3], s[12:13]
	v_pk_add_f32 v[36:37], v[8:9], v[24:25] op_sel:[0,1] op_sel_hi:[1,0] neg_hi:[0,1]
	v_pk_add_f32 v[8:9], v[8:9], v[24:25] op_sel:[0,1] op_sel_hi:[1,0] neg_lo:[0,1]
	v_pk_mul_f32 v[22:23], v[4:5], s[10:11] op_sel:[0,0] op_sel_hi:[0,1]
	v_pk_fma_f32 v[22:23], v[4:5], s[10:11], v[22:23] op_sel:[1,1,0] op_sel_hi:[1,0,1] neg_lo:[0,1,0]
	v_pk_add_f32 v[4:5], v[28:29], v[34:35]
	v_pk_add_f32 v[2:3], v[32:33], v[32:33] op_sel:[0,1] op_sel_hi:[1,0] neg_lo:[0,1]
	v_pk_add_f32 v[28:29], v[28:29], v[34:35] neg_lo:[0,1] neg_hi:[0,1]
	v_pk_mul_f32 v[32:33], v[2:3], s[12:13]
	v_pk_add_f32 v[2:3], v[26:27], v[30:31]
	v_pk_add_f32 v[26:27], v[26:27], v[30:31] neg_lo:[0,1] neg_hi:[0,1]
	v_pk_mul_f32 v[24:25], v[10:11], s[6:7] op_sel:[0,0] op_sel_hi:[0,1]
	v_pk_fma_f32 v[24:25], v[10:11], s[6:7], v[24:25] op_sel:[1,1,0] op_sel_hi:[1,0,1] neg_lo:[0,1,0]
	v_pk_mul_f32 v[6:7], v[36:37], s[10:11] op_sel:[0,0] op_sel_hi:[0,1]
	v_pk_fma_f32 v[6:7], v[36:37], s[10:11], v[6:7] op_sel:[1,1,0] op_sel_hi:[1,0,1] neg_lo:[0,1,0]
	v_pk_mul_f32 v[56:57], v[8:9], s[14:15] op_sel:[0,0] op_sel_hi:[0,1]
	v_pk_fma_f32 v[56:57], v[8:9], s[14:15], v[56:57] op_sel:[1,1,0] op_sel_hi:[1,0,1] neg_lo:[0,1,0]
	v_pk_add_f32 v[10:11], v[2:3], v[4:5]
	v_lshlrev_b32_e32 v34, 2, v0
	v_pk_add_f32 v[4:5], v[2:3], v[4:5] neg_lo:[0,1] neg_hi:[0,1]
	v_pk_add_f32 v[8:9], v[26:27], v[28:29] op_sel:[0,1] op_sel_hi:[1,0] neg_hi:[0,1]
	v_pk_add_f32 v[2:3], v[26:27], v[28:29] op_sel:[0,1] op_sel_hi:[1,0] neg_lo:[0,1]
	v_pk_add_f32 v[26:27], v[14:15], v[12:13]
	v_pk_add_f32 v[28:29], v[24:25], v[6:7]
	v_add_u32_e32 v1, 0x400, v34
	v_pk_add_f32 v[14:15], v[14:15], v[12:13] neg_lo:[0,1] neg_hi:[0,1]
	v_pk_add_f32 v[30:31], v[24:25], v[6:7] neg_lo:[0,1] neg_hi:[0,1]
	v_pk_add_f32 v[12:13], v[26:27], v[28:29]
	v_pk_add_f32 v[6:7], v[26:27], v[28:29] neg_lo:[0,1] neg_hi:[0,1]
	v_add_u32_e32 v24, 0x800, v34
	v_add_u32_e32 v25, 0xc00, v34
	v_add_u32_e32 v26, 0x1000, v34
	v_add_u32_e32 v27, 0x1400, v34
	v_add_u32_e32 v28, 0x1800, v34
	v_add_u32_e32 v29, 0x1c00, v34
	v_add_u32_e32 v35, 0x2000, v34
	global_load_ushort v1, v1, s[2:3]
	s_nop 0
	global_load_ushort v36, v24, s[2:3]
	global_load_ushort v37, v25, s[2:3]
	global_load_ushort v38, v26, s[2:3]
	global_load_ushort v39, v27, s[2:3]
	global_load_ushort v40, v28, s[2:3]
	global_load_ushort v41, v29, s[2:3]
	global_load_ushort v42, v35, s[2:3]
	v_add_u32_e32 v24, 0x2400, v34
	v_add_u32_e32 v25, 0x2800, v34
	v_add_u32_e32 v26, 0x2c00, v34
	v_add_u32_e32 v27, 0x3000, v34
	v_add_u32_e32 v28, 0x3400, v34
	v_add_u32_e32 v35, 0x3800, v34
	global_load_ushort v52, v34, s[2:3]
	global_load_ushort v43, v35, s[2:3]
	v_add_u32_e32 v29, 0x3c00, v34
	global_load_ushort v47, v24, s[2:3]
	global_load_ushort v48, v25, s[2:3]
	global_load_ushort v49, v26, s[2:3]
	global_load_ushort v50, v27, s[2:3]
	global_load_ushort v51, v28, s[2:3]
	global_load_ushort v46, v29, s[2:3]
	v_pk_add_f32 v[26:27], v[16:17], v[20:21] op_sel:[0,1] op_sel_hi:[1,0] neg_hi:[0,1]
	v_pk_add_f32 v[16:17], v[16:17], v[20:21] op_sel:[0,1] op_sel_hi:[1,0] neg_lo:[0,1]
	v_pk_add_f32 v[20:21], v[44:45], v[32:33]
	v_pk_add_f32 v[28:29], v[44:45], v[32:33] neg_lo:[0,1] neg_hi:[0,1]
	v_pk_add_f32 v[24:25], v[14:15], v[30:31] op_sel:[0,1] op_sel_hi:[1,0] neg_hi:[0,1]
	v_pk_add_f32 v[14:15], v[14:15], v[30:31] op_sel:[0,1] op_sel_hi:[1,0] neg_lo:[0,1]
	v_pk_add_f32 v[30:31], v[20:21], v[26:27]
	v_pk_add_f32 v[20:21], v[26:27], v[20:21] neg_lo:[0,1] neg_hi:[0,1]
	v_pk_add_f32 v[26:27], v[16:17], v[28:29] op_sel:[0,1] op_sel_hi:[1,0] neg_hi:[0,1]
	v_pk_add_f32 v[16:17], v[16:17], v[28:29] op_sel:[0,1] op_sel_hi:[1,0] neg_lo:[0,1]
	v_pk_add_f32 v[28:29], v[18:19], v[54:55]
	v_pk_add_f32 v[44:45], v[22:23], v[56:57]
	s_mov_b32 s2, 0xff61b1e6
	v_pk_add_f32 v[18:19], v[18:19], v[54:55] neg_lo:[0,1] neg_hi:[0,1]
	v_pk_add_f32 v[54:55], v[22:23], v[56:57] neg_lo:[0,1] neg_hi:[0,1]
	v_pk_add_f32 v[32:33], v[28:29], v[44:45]
	v_pk_add_f32 v[22:23], v[28:29], v[44:45] neg_lo:[0,1] neg_hi:[0,1]
	v_max3_f32 v44, v10, s2, v12
	v_max3_f32 v44, v44, v30, v32
	v_max3_f32 v44, v44, v8, v24
	v_pk_add_f32 v[28:29], v[18:19], v[54:55] op_sel:[0,1] op_sel_hi:[1,0] neg_hi:[0,1]
	v_pk_add_f32 v[18:19], v[18:19], v[54:55] op_sel:[0,1] op_sel_hi:[1,0] neg_lo:[0,1]
	v_max3_f32 v45, -v11, s2, -v13
	v_max3_f32 v44, v44, v26, v28
	v_max3_f32 v44, v44, v4, v6
	v_max3_f32 v44, v44, v20, v22
	v_max3_f32 v44, v44, v2, v14
	v_max3_f32 v44, v44, v16, v18
	v_max3_f32 v45, v45, -v31, -v33
	v_max3_f32 v45, v45, -v9, -v25
	v_mov_b32_dpp v53, v44 quad_perm:[1,0,3,2] row_mask:0xf bank_mask:0xf
	v_max_f32_e32 v53, v53, v53
	v_max_f32_e32 v44, v44, v53
	v_mov_b32_e32 v53, 0
	v_max3_f32 v45, v45, -v27, -v29
	v_max3_f32 v45, v45, -v5, -v7
	v_mov_b32_dpp v53, v44 quad_perm:[2,3,0,1] row_mask:0xf bank_mask:0xf
	v_max_f32_e32 v53, v53, v53
	v_max_f32_e32 v44, v44, v53
	v_mov_b32_e32 v53, 0
	v_max3_f32 v45, v45, -v21, -v23
	v_max3_f32 v45, v45, -v3, -v15
	v_mov_b32_dpp v53, v44 row_half_mirror row_mask:0xf bank_mask:0xf
	v_max_f32_e32 v53, v53, v53
	v_max_f32_e32 v44, v44, v53
	v_mov_b32_e32 v53, 0
	v_max3_f32 v45, v45, -v17, -v19
	s_nop 0
	v_mov_b32_dpp v53, v44 row_mirror row_mask:0xf bank_mask:0xf
	v_max_f32_e32 v53, v53, v53
	v_max_f32_e32 v44, v44, v53
	s_nop 0
	v_readlane_b32 s5, v44, 0
	v_readlane_b32 s6, v44, 16
	v_readlane_b32 s7, v44, 32
	v_readlane_b32 s8, v44, 48
	v_mov_b32_e32 v44, 0
	s_nop 1
	v_mov_b32_dpp v44, v45 quad_perm:[1,0,3,2] row_mask:0xf bank_mask:0xf
	v_max_f32_e32 v44, v44, v44
	v_max_f32_e32 v44, v45, v44
	v_mov_b32_e32 v45, 0
	s_nop 1
	v_mov_b32_dpp v45, v44 quad_perm:[2,3,0,1] row_mask:0xf bank_mask:0xf
	v_max_f32_e32 v45, v45, v45
	v_max_f32_e32 v44, v44, v45
	v_mov_b32_e32 v45, 0
	s_nop 1
	v_mov_b32_dpp v45, v44 row_half_mirror row_mask:0xf bank_mask:0xf
	v_max_f32_e32 v45, v45, v45
	v_max_f32_e32 v44, v44, v45
	v_mov_b32_e32 v45, 0
	s_nop 1
	v_mov_b32_dpp v45, v44 row_mirror row_mask:0xf bank_mask:0xf
	v_max_f32_e32 v45, v45, v45
	v_max_f32_e32 v44, v44, v45
	v_and_b32_e32 v45, 63, v0
	v_readlane_b32 s9, v44, 0
	v_readlane_b32 s10, v44, 16
	v_readlane_b32 s11, v44, 32
	v_readlane_b32 s12, v44, 48
	v_ashrrev_i32_e32 v44, 6, v0
	v_cmp_eq_u32_e32 vcc, 0, v45
	v_lshlrev_b32_e32 v61, 3, v44
	s_and_saveexec_b64 s[2:3], vcc
	s_cbranch_execz .LBB1_10
	v_max_f32_e64 v44, s12, s12
	v_max_f32_e64 v45, s11, s11
	v_max_f32_e32 v44, v45, v44
	v_mov_b32_e32 v45, s10
	v_max3_f32 v45, s9, v45, v44
	v_max_f32_e64 v44, s8, s8
	v_max_f32_e64 v53, s7, s7
	v_max_f32_e32 v44, v53, v44
	v_mov_b32_e32 v53, s6
	v_max3_f32 v44, s5, v53, v44
	ds_write_b64 v61, v[44:45] offset:36864

.LBB1_12:
	s_or_b64 exec, exec, s[8:9]
	s_waitcnt vmcnt(7)
	v_and_b32_e32 v23, 0xffff, v52
	v_and_b32_e32 v52, 0xffff, v1
	v_mov_b32_e32 v1, 0
	v_and_b32_e32 v61, 0xffff, v36
	v_and_b32_e32 v62, 0xffff, v37
	v_and_b32_e32 v63, 0xffff, v38
	v_and_b32_e32 v64, 0xffff, v39
	v_and_b32_e32 v65, 0xffff, v40
	v_and_b32_e32 v66, 0xffff, v41
	v_and_b32_e32 v67, 0xffff, v42
	s_waitcnt vmcnt(6)
	v_and_b32_e32 v14, 0xffff, v43
	s_waitcnt lgkmcnt(0)
	s_barrier
	ds_read_b128 v[36:39], v1 offset:36896
	ds_read_b128 v[40:43], v1 offset:36912
	s_mov_b32 s5, 0
	s_lshl_b64 s[2:3], s[4:5], 16
	s_add_u32 s0, s0, s2
	s_waitcnt lgkmcnt(1)
	v_add_f32_e32 v16, v36, v38
	s_waitcnt lgkmcnt(0)
	v_add_f32_e32 v18, v40, v42
	s_addc_u32 s1, s1, s3
	s_lshl_b32 s2, s16, 1
	v_add_f32_e32 v16, v16, v18
	s_mov_b32 s4, 0x45800000
	s_add_u32 s0, s0, s2
	v_div_scale_f32 v18, s[2:3], v16, v16, s4
	v_rcp_f32_e32 v36, v18
	v_add_f32_e32 v37, v37, v39
	v_add_f32_e32 v38, v41, v43
	v_add_f32_e32 v37, v37, v38
	v_fma_f32 v38, -v18, v36, 1.0
	v_fmac_f32_e32 v36, v38, v36
	v_div_scale_f32 v38, vcc, s4, v16, s4
	v_mul_f32_e32 v39, v38, v36
	v_fma_f32 v40, -v18, v39, v38
	v_fmac_f32_e32 v39, v40, v36
	v_fma_f32 v18, -v18, v39, v38
	v_div_scale_f32 v38, s[2:3], v37, v37, s4
	v_rcp_f32_e32 v40, v38
	v_div_fmas_f32 v18, v18, v36, v39
	v_div_fixup_f32 v16, v18, v16, s4
	s_addc_u32 s1, s1, 0
	v_fma_f32 v18, -v38, v40, 1.0
	v_fmac_f32_e32 v40, v18, v40
	v_div_scale_f32 v18, vcc, s4, v37, s4
	v_mul_f32_e32 v36, v18, v40
	v_fma_f32 v39, -v38, v36, v18
	v_fmac_f32_e32 v36, v39, v40
	v_fma_f32 v18, -v38, v36, v18
	v_div_fmas_f32 v18, v18, v40, v36
	v_cvt_f32_fp8_e32 v36, v23
	v_cvt_f32_fp8_sdwa v23, v23 src0_sel:BYTE_1
	v_div_fixup_f32 v18, v18, v37, s4
	v_mul_f32_e32 v37, v16, v59
	v_mul_f32_e32 v36, v37, v36
	v_mul_f32_e32 v37, v18, v60
	v_mul_f32_e32 v23, v37, v23
	v_mov_b32_e32 v38, 0
	v_cvt_pk_fp8_f32 v38, v36, v23
	v_cvt_f32_fp8_e32 v23, v52
	v_cvt_f32_fp8_sdwa v36, v52 src0_sel:BYTE_1
	v_mul_f32_e32 v37, v16, v57
	v_cvt_pk_fp8_f32 v38, 0, 0 op_sel:[0,0,1]
	v_mul_f32_e32 v23, v37, v23
	v_mul_f32_e32 v37, v18, v58
	v_lshlrev_b32_e32 v0, 3, v0
	v_mul_f32_e32 v36, v37, v36
	v_mov_b32_e32 v39, v1
	v_cvt_pk_fp8_f32 v39, v23, v36
	v_lshl_add_u64 v[36:37], v[0:1], 1, s[0:1]
	v_cvt_f32_fp8_e32 v23, v61
	global_store_short v[36:37], v38, off
	v_cvt_f32_fp8_sdwa v38, v61 src0_sel:BYTE_1
	v_mul_f32_e32 v40, v16, v55
	v_mul_f32_e32 v23, v40, v23
	v_mul_f32_e32 v40, v18, v56
	v_cvt_pk_fp8_f32 v39, 0, 0 op_sel:[0,0,1]
	v_mul_f32_e32 v38, v40, v38
	v_mov_b32_e32 v40, v1
	v_cvt_pk_fp8_f32 v40, v23, v38
	v_cvt_f32_fp8_e32 v23, v62
	v_add_u32_e32 v36, 0x800, v0
	v_mov_b32_e32 v37, v1
	v_cvt_f32_fp8_sdwa v38, v62 src0_sel:BYTE_1
	v_lshl_add_u64 v[36:37], v[36:37], 1, s[0:1]
	global_store_short v[36:37], v39, off
	v_mul_f32_e32 v39, v16, v53
	v_mul_f32_e32 v23, v39, v23
	v_mul_f32_e32 v39, v18, v54
	v_cvt_pk_fp8_f32 v40, 0, 0 op_sel:[0,0,1]
	v_mul_f32_e32 v38, v39, v38
	v_mov_b32_e32 v39, v1
	v_cvt_pk_fp8_f32 v39, v23, v38
	v_cvt_f32_fp8_e32 v23, v63
	v_add_u32_e32 v36, 0x1000, v0
	v_mov_b32_e32 v37, v1
	v_cvt_f32_fp8_sdwa v38, v63 src0_sel:BYTE_1
	v_lshl_add_u64 v[36:37], v[36:37], 1, s[0:1]
	global_store_short v[36:37], v40, off
	v_mul_f32_e32 v40, v16, v44
	v_mul_f32_e32 v23, v40, v23
	v_mul_f32_e32 v40, v18, v45
	v_mul_f32_e32 v38, v40, v38
	v_mov_b32_e32 v40, v1
	v_cvt_pk_fp8_f32 v40, v23, v38
	v_cvt_f32_fp8_e32 v23, v64
	v_cvt_f32_fp8_sdwa v38, v64 src0_sel:BYTE_1
	v_cvt_pk_fp8_f32 v39, 0, 0 op_sel:[0,0,1]
	v_mul_f32_e32 v32, v16, v32
	v_add_u32_e32 v36, 0x1800, v0
	v_mov_b32_e32 v37, v1
	v_mul_f32_e32 v23, v32, v23
	v_mul_f32_e32 v32, v18, v33
	v_lshl_add_u64 v[36:37], v[36:37], 1, s[0:1]
	v_mul_f32_e32 v32, v32, v38
	v_mov_b32_e32 v38, v1
	global_store_short v[36:37], v39, off
	v_add_u32_e32 v36, 0x2000, v0
	v_mov_b32_e32 v37, v1
	v_cvt_pk_fp8_f32 v38, v23, v32
	v_cvt_f32_fp8_e32 v23, v65
	v_lshl_add_u64 v[32:33], v[36:37], 1, s[0:1]
	v_cvt_f32_fp8_sdwa v36, v65 src0_sel:BYTE_1
	v_cvt_pk_fp8_f32 v40, 0, 0 op_sel:[0,0,1]
	v_mul_f32_e32 v30, v16, v30
	v_mul_f32_e32 v23, v30, v23
	v_mul_f32_e32 v30, v18, v31
	v_mul_f32_e32 v30, v30, v36
	v_mov_b32_e32 v36, v1
	global_store_short v[32:33], v40, off
	v_add_u32_e32 v32, 0x2800, v0
	v_mov_b32_e32 v33, v1
	v_cvt_pk_fp8_f32 v36, v23, v30
	v_cvt_f32_fp8_e32 v23, v66
	v_lshl_add_u64 v[30:31], v[32:33], 1, s[0:1]
	v_cvt_f32_fp8_sdwa v32, v66 src0_sel:BYTE_1
	v_cvt_pk_fp8_f32 v38, 0, 0 op_sel:[0,0,1]
	v_mul_f32_e32 v28, v16, v28
	v_mul_f32_e32 v23, v28, v23
	v_mul_f32_e32 v28, v18, v29
	v_mul_f32_e32 v28, v28, v32
	v_mov_b32_e32 v32, v1
	global_store_short v[30:31], v38, off
	v_add_u32_e32 v30, 0x3000, v0
	v_mov_b32_e32 v31, v1
	v_cvt_pk_fp8_f32 v32, v23, v28
	v_cvt_f32_fp8_e32 v23, v67
	v_lshl_add_u64 v[28:29], v[30:31], 1, s[0:1]
	v_cvt_f32_fp8_sdwa v30, v67 src0_sel:BYTE_1
	v_mul_f32_e32 v26, v16, v26
	v_mul_f32_e32 v23, v26, v23
	v_mul_f32_e32 v26, v18, v27
	s_waitcnt vmcnt(11)
	v_and_b32_e32 v22, 0xffff, v47
	v_mul_f32_e32 v26, v26, v30
	v_mov_b32_e32 v30, v1
	v_cvt_pk_fp8_f32 v30, v23, v26
	v_cvt_f32_fp8_e32 v23, v22
	s_waitcnt vmcnt(10)
	v_and_b32_e32 v21, 0xffff, v48
	v_mul_f32_e32 v24, v16, v24
	v_cvt_f32_fp8_sdwa v22, v22 src0_sel:BYTE_1
	v_mul_f32_e32 v23, v24, v23
	v_mul_f32_e32 v24, v18, v25
	v_cvt_f32_fp8_e32 v25, v21
	v_cvt_f32_fp8_sdwa v21, v21 src0_sel:BYTE_1
	v_mul_f32_e32 v13, v16, v13
	v_mul_f32_e32 v20, v18, v20
	s_waitcnt vmcnt(9)
	v_and_b32_e32 v19, 0xffff, v49
	v_cvt_pk_fp8_f32 v36, 0, 0 op_sel:[0,0,1]
	v_mul_f32_e32 v13, v13, v25
	v_mul_f32_e32 v20, v20, v21
	v_mov_b32_e32 v25, v1
	v_mul_f32_e32 v22, v24, v22
	v_mov_b32_e32 v24, v1
	v_cvt_pk_fp8_f32 v25, v13, v20
	v_cvt_f32_fp8_e32 v13, v19
	v_cvt_f32_fp8_sdwa v19, v19 src0_sel:BYTE_1
	v_cvt_pk_fp8_f32 v32, 0, 0 op_sel:[0,0,1]
	v_cvt_pk_fp8_f32 v24, v23, v22
	global_store_short v[28:29], v36, off
	v_add_u32_e32 v28, v35, v34
	v_mov_b32_e32 v29, v1
	v_cvt_pk_fp8_f32 v30, 0, 0 op_sel:[0,0,1]
	v_mul_f32_e32 v10, v16, v10
	v_mul_f32_e32 v11, v18, v11
	v_lshl_add_u64 v[26:27], v[28:29], 1, s[0:1]
	v_mul_f32_e32 v10, v10, v13
	v_mul_f32_e32 v11, v11, v19
	v_mov_b32_e32 v13, v1
	global_store_short v[26:27], v32, off
	v_add_u32_e32 v26, 0x4000, v0
	v_mov_b32_e32 v27, v1
	v_cvt_pk_fp8_f32 v24, 0, 0 op_sel:[0,0,1]
	v_cvt_pk_fp8_f32 v13, v10, v11
	v_lshl_add_u64 v[22:23], v[26:27], 1, s[0:1]
	s_waitcnt vmcnt(10)
	v_and_b32_e32 v17, 0xffff, v50
	global_store_short v[22:23], v30, off
	v_add_u32_e32 v22, 0x4800, v0
	v_mov_b32_e32 v23, v1
	v_cvt_pk_fp8_f32 v25, 0, 0 op_sel:[0,0,1]
	v_lshl_add_u64 v[20:21], v[22:23], 1, s[0:1]
	v_cvt_f32_fp8_e32 v19, v17
	v_cvt_f32_fp8_sdwa v17, v17 src0_sel:BYTE_1
	global_store_short v[20:21], v24, off
	v_add_u32_e32 v20, 0x5000, v0
	v_mov_b32_e32 v21, v1
	v_cvt_pk_fp8_f32 v13, 0, 0 op_sel:[0,0,1]
	v_lshl_add_u64 v[10:11], v[20:21], 1, s[0:1]
	global_store_short v[10:11], v25, off
	v_add_u32_e32 v10, 0x5800, v0
	v_mov_b32_e32 v11, v1
	v_mul_f32_e32 v8, v16, v8
	v_mul_f32_e32 v9, v18, v9
	s_waitcnt vmcnt(12)
	v_and_b32_e32 v15, 0xffff, v51
	v_lshl_add_u64 v[10:11], v[10:11], 1, s[0:1]
	v_mul_f32_e32 v8, v8, v19
	v_mul_f32_e32 v9, v9, v17
	v_mov_b32_e32 v17, v1
	v_cvt_pk_fp8_f32 v17, v8, v9
	global_store_short v[10:11], v13, off
	v_cvt_f32_fp8_e32 v9, v15
	v_cvt_f32_fp8_sdwa v10, v15 src0_sel:BYTE_1
	v_mul_f32_e32 v6, v16, v6
	v_mul_f32_e32 v7, v18, v7
	v_mul_f32_e32 v6, v6, v9
	v_mul_f32_e32 v7, v7, v10
	v_mov_b32_e32 v10, v1
	v_cvt_pk_fp8_f32 v10, v6, v7
	v_cvt_pk_fp8_f32 v17, 0, 0 op_sel:[0,0,1]
	v_add_u32_e32 v8, 0x6000, v0
	v_mov_b32_e32 v9, v1
	v_cvt_pk_fp8_f32 v10, 0, 0 op_sel:[0,0,1]
	v_lshl_add_u64 v[6:7], v[8:9], 1, s[0:1]
	global_store_short v[6:7], v17, off
	v_add_u32_e32 v6, 0x6800, v0
	v_mov_b32_e32 v7, v1
	v_lshl_add_u64 v[6:7], v[6:7], 1, s[0:1]
	global_store_short v[6:7], v10, off
	v_cvt_f32_fp8_e32 v7, v14
	v_cvt_f32_fp8_sdwa v8, v14 src0_sel:BYTE_1
	v_mul_f32_e32 v4, v16, v4
	v_mul_f32_e32 v5, v18, v5
	s_waitcnt vmcnt(14)
	v_and_b32_e32 v12, 0xffff, v46
	v_mul_f32_e32 v4, v4, v7
	v_mul_f32_e32 v5, v5, v8
	v_mov_b32_e32 v8, v1
	v_cvt_f32_fp8_e32 v7, v12
	v_cvt_pk_fp8_f32 v8, v4, v5
	v_cvt_f32_fp8_sdwa v4, v12 src0_sel:BYTE_1
	v_mul_f32_e32 v2, v16, v2
	v_mul_f32_e32 v3, v18, v3
	v_mul_f32_e32 v2, v2, v7
	v_mul_f32_e32 v3, v3, v4
	v_mov_b32_e32 v4, v1
	v_cvt_pk_fp8_f32 v4, v2, v3
	v_cvt_pk_fp8_f32 v8, 0, 0 op_sel:[0,0,1]
	v_add_u32_e32 v6, 0x7000, v0
	v_mov_b32_e32 v7, v1
	v_cvt_pk_fp8_f32 v4, 0, 0 op_sel:[0,0,1]
	v_add_u32_e32 v0, 0x7800, v0
	v_lshl_add_u64 v[2:3], v[6:7], 1, s[0:1]
	v_lshl_add_u64 v[0:1], v[0:1], 1, s[0:1]
	global_store_short v[2:3], v8, off
	global_store_short v[0:1], v4, off
	s_endpgm
	s_nop 0
	s_nop 0
	s_nop 0
	s_nop 0
	s_nop 0
	s_nop 0
	s_nop 0
	s_nop 0
	s_nop 0
	s_nop 0
	s_nop 0
	s_nop 0
	s_nop 0
	s_nop 0
	s_nop 0
	s_nop 0
	s_nop 0
	s_nop 0
	s_nop 0
	s_nop 0
	s_nop 0
	s_nop 0
	s_nop 0
	s_nop 0
	s_nop 0
	s_nop 0
	s_nop 0
	s_nop 0
	s_nop 0
	s_nop 0
	s_nop 0
	s_nop 0
	s_nop 0
	s_nop 0
	s_nop 0
	s_nop 0
	s_nop 0
	s_nop 0
	s_nop 0
	s_nop 0
	s_nop 0
	s_nop 0
	s_nop 0
	s_nop 0
	s_nop 0
	s_nop 0
	s_nop 0
	s_endpgm

.LBB2_7:
	v_fmamk_f32 v126, v126, 0x3a800000, v158
	v_fmamk_f32 v127, v127, 0x3a800000, v159
	v_mov_b32_e32 v178, v163
	v_cvt_pk_fp8_f32 v178, v126, v127
	v_fmamk_f32 v126, v128, 0x3a800000, v160
	v_fmamk_f32 v122, v122, 0x3a800000, v158
	v_fmamk_f32 v123, v123, 0x3a800000, v159
	v_mov_b32_e32 v128, v163
	v_cvt_pk_fp8_f32 v128, v122, v123
	v_fmamk_f32 v124, v124, 0x3a800000, v160
	v_fmamk_f32 v125, v125, 0x3a800000, v161
	v_fmamk_f32 v118, v118, 0x3a800000, v158
	v_cvt_pk_fp8_f32 v128, v124, v125 op_sel:[0,0,1]
	v_fmamk_f32 v119, v119, 0x3a800000, v159
	v_mov_b32_e32 v124, v163
	v_cvt_pk_fp8_f32 v124, v118, v119
	v_fmamk_f32 v114, v114, 0x3a800000, v158
	v_fmamk_f32 v115, v115, 0x3a800000, v159
	v_mov_b32_e32 v118, v163
	v_cvt_pk_fp8_f32 v118, v114, v115
	v_fmamk_f32 v114, v116, 0x3a800000, v160
	v_fmamk_f32 v110, v110, 0x3a800000, v154
	v_fmamk_f32 v111, v111, 0x3a800000, v155
	v_mov_b32_e32 v116, v163
	v_cvt_pk_fp8_f32 v116, v110, v111
	v_fmamk_f32 v112, v112, 0x3a800000, v156
	v_fmamk_f32 v113, v113, 0x3a800000, v157
	v_fmamk_f32 v98, v98, 0x3a800000, v154
	v_cvt_pk_fp8_f32 v116, v112, v113 op_sel:[0,0,1]
	v_fmamk_f32 v99, v99, 0x3a800000, v155
	v_mov_b32_e32 v112, v163
	v_cvt_pk_fp8_f32 v112, v98, v99
	v_fmamk_f32 v100, v100, 0x3a800000, v156
	v_fmamk_f32 v101, v101, 0x3a800000, v157
	v_and_b32_e32 v162, 15, v175
	v_cvt_pk_fp8_f32 v112, v100, v101 op_sel:[0,0,1]
	v_fmamk_f32 v100, v106, 0x3a800000, v154
	v_fmamk_f32 v101, v107, 0x3a800000, v155
	v_fmamk_f32 v106, v108, 0x3a800000, v156
	v_mov_b32_e32 v108, v163
	v_cvt_pk_fp8_f32 v108, v100, v101
	v_fmamk_f32 v100, v102, 0x3a800000, v154
	v_fmamk_f32 v101, v103, 0x3a800000, v155
	v_mov_b32_e32 v102, v163
	v_cvt_pk_fp8_f32 v102, v100, v101
	v_lshrrev_b32_e32 v175, 1, v175
	v_and_b32_e32 v175, 0x60, v175
	v_or3_b32 v162, v175, v162, s50
	v_lshrrev_b32_e32 v175, 2, v173
	v_fmamk_f32 v107, v109, 0x3a800000, v157
	v_fmamk_f32 v100, v104, 0x3a800000, v156
	v_fmac_f32_e32 v157, 0x3a800000, v105
	v_and_b32_e32 v175, 0xf0, v175
	v_cvt_pk_fp8_f32 v102, v100, v157 op_sel:[0,0,1]
	v_fmamk_f32 v86, v86, 0x3a800000, v150
	v_fmamk_f32 v87, v87, 0x3a800000, v151
	v_mov_b32_e32 v100, v163
	s_ashr_i32 s45, s50, 4
	v_or_b32_e32 v175, s56, v175
	v_fmamk_f32 v127, v129, 0x3a800000, v161
	v_fmamk_f32 v121, v121, 0x3a800000, v161
	v_fmac_f32_e32 v161, 0x3a800000, v117
	v_cvt_pk_fp8_f32 v100, v86, v87
	s_and_b32 s45, s45, 0xffffff00
	v_cvt_pk_fp8_f32 v118, v114, v161 op_sel:[0,0,1]
	v_or_b32_e32 v114, 4, v175
	v_add_u32_e32 v176, s45, v175
	v_add_u32_e32 v114, s45, v114
	v_or_b32_e32 v176, v176, v172
	v_or_b32_e32 v114, v114, v172
	v_fmamk_f32 v88, v88, 0x3a800000, v152
	v_fmamk_f32 v89, v89, 0x3a800000, v153
	v_ashrrev_i32_e32 v177, 31, v176
	v_cvt_pk_fp8_f32 v178, v126, v127 op_sel:[0,0,1]
	v_ashrrev_i32_e32 v115, 31, v114
	v_cvt_pk_fp8_f32 v100, v88, v89 op_sel:[0,0,1]
	v_fmamk_f32 v82, v82, 0x3a800000, v150
	v_fmamk_f32 v83, v83, 0x3a800000, v151
	v_mov_b32_e32 v88, v163
	v_lshlrev_b64 v[176:177], 14, v[176:177]
	v_lshlrev_b32_e32 v162, 2, v162
	v_fmamk_f32 v120, v120, 0x3a800000, v160
	v_lshlrev_b64 v[110:111], 14, v[114:115]
	v_cvt_pk_fp8_f32 v88, v82, v83
	v_and_b32_e32 v162, 0x3dbc, v162
	v_lshl_add_u64 v[126:127], s[18:19], 0, v[176:177]
	v_cvt_pk_fp8_f32 v124, v120, v121 op_sel:[0,0,1]
	v_lshl_add_u64 v[110:111], s[18:19], 0, v[110:111]
	v_cvt_pk_fp8_f32 v108, v106, v107 op_sel:[0,0,1]
	v_lshl_add_u64 v[122:123], v[126:127], 0, v[162:163]
	v_lshl_add_u64 v[98:99], v[110:111], 0, v[162:163]
	global_store_dword v[122:123], v178, off
	global_store_dword v[122:123], v128, off offset:64
	global_store_dword v[122:123], v124, off offset:512
	global_store_dword v[122:123], v118, off offset:576
	global_store_dword v[98:99], v116, off
	global_store_dword v[98:99], v112, off offset:64
	global_store_dword v[98:99], v108, off offset:512
	global_store_dword v[98:99], v102, off offset:576
	v_or_b32_e32 v98, 8, v175
	v_fmamk_f32 v84, v84, 0x3a800000, v152
	v_fmamk_f32 v85, v85, 0x3a800000, v153
	v_add_u32_e32 v98, s45, v98
	v_cvt_pk_fp8_f32 v88, v84, v85 op_sel:[0,0,1]
	v_fmamk_f32 v84, v94, 0x3a800000, v150
	v_fmamk_f32 v85, v95, 0x3a800000, v151
	v_mov_b32_e32 v89, v163
	v_or_b32_e32 v98, v98, v172
	v_cvt_pk_fp8_f32 v89, v84, v85
	v_fmamk_f32 v84, v90, 0x3a800000, v150
	v_fmamk_f32 v85, v91, 0x3a800000, v151
	v_mov_b32_e32 v90, v163
	v_ashrrev_i32_e32 v99, 31, v98
	v_cvt_pk_fp8_f32 v90, v84, v85
	v_lshlrev_b64 v[86:87], 14, v[98:99]
	v_lshl_add_u64 v[86:87], s[18:19], 0, v[86:87]
	v_lshl_add_u64 v[82:83], v[86:87], 0, v[162:163]
	v_fmamk_f32 v87, v97, 0x3a800000, v153
	v_fmamk_f32 v84, v92, 0x3a800000, v152
	v_fmac_f32_e32 v153, 0x3a800000, v93
	v_cvt_pk_fp8_f32 v90, v84, v153 op_sel:[0,0,1]
	v_fmamk_f32 v66, v66, 0x3a800000, v146
	v_fmamk_f32 v67, v67, 0x3a800000, v147
	v_mov_b32_e32 v84, v163
	v_cvt_pk_fp8_f32 v84, v66, v67
	v_fmamk_f32 v68, v68, 0x3a800000, v148
	v_fmamk_f32 v69, v69, 0x3a800000, v149
	v_fmamk_f32 v50, v50, 0x3a800000, v146
	v_cvt_pk_fp8_f32 v84, v68, v69 op_sel:[0,0,1]
	v_fmamk_f32 v51, v51, 0x3a800000, v147
	v_mov_b32_e32 v68, v163
	v_fmamk_f32 v86, v96, 0x3a800000, v152
	v_cvt_pk_fp8_f32 v68, v50, v51
	v_cvt_pk_fp8_f32 v89, v86, v87 op_sel:[0,0,1]
	global_store_dword v[82:83], v100, off
	global_store_dword v[82:83], v88, off offset:64
	global_store_dword v[82:83], v89, off offset:512
	global_store_dword v[82:83], v90, off offset:576
	v_or_b32_e32 v82, 12, v175
	v_fmamk_f32 v52, v52, 0x3a800000, v148
	v_fmamk_f32 v53, v53, 0x3a800000, v149
	v_add_u32_e32 v82, s45, v82
	v_cvt_pk_fp8_f32 v68, v52, v53 op_sel:[0,0,1]
	v_fmamk_f32 v52, v78, 0x3a800000, v146
	v_fmamk_f32 v53, v79, 0x3a800000, v147
	v_mov_b32_e32 v69, v163
	v_or_b32_e32 v82, v82, v172
	v_cvt_pk_fp8_f32 v69, v52, v53
	v_fmamk_f32 v52, v74, 0x3a800000, v146
	v_fmamk_f32 v53, v75, 0x3a800000, v147
	v_mov_b32_e32 v74, v163
	v_ashrrev_i32_e32 v83, 31, v82
	v_cvt_pk_fp8_f32 v74, v52, v53
	v_lshlrev_b64 v[66:67], 14, v[82:83]
	v_lshl_add_u64 v[66:67], s[18:19], 0, v[66:67]
	v_lshl_add_u64 v[50:51], v[66:67], 0, v[162:163]
	v_fmamk_f32 v67, v81, 0x3a800000, v149
	v_fmamk_f32 v52, v76, 0x3a800000, v148
	v_fmac_f32_e32 v149, 0x3a800000, v77
	v_cvt_pk_fp8_f32 v74, v52, v149 op_sel:[0,0,1]
	v_fmamk_f32 v52, v62, 0x3a800000, v142
	v_fmamk_f32 v53, v63, 0x3a800000, v143
	v_mov_b32_e32 v62, v163
	v_cvt_pk_fp8_f32 v62, v52, v53
	v_fmamk_f32 v52, v64, 0x3a800000, v144
	v_fmamk_f32 v53, v65, 0x3a800000, v145
	v_fmamk_f32 v66, v80, 0x3a800000, v148
	v_cvt_pk_fp8_f32 v62, v52, v53 op_sel:[0,0,1]
	v_fmamk_f32 v52, v54, 0x3a800000, v142
	v_fmamk_f32 v53, v55, 0x3a800000, v143
	v_mov_b32_e32 v54, v163
	v_cvt_pk_fp8_f32 v54, v52, v53
	v_fmamk_f32 v52, v56, 0x3a800000, v144
	v_fmamk_f32 v53, v57, 0x3a800000, v145
	v_mov_b32_e32 v57, v163
	v_cvt_pk_fp8_f32 v54, v52, v53 op_sel:[0,0,1]
	v_fmamk_f32 v52, v70, 0x3a800000, v142
	v_fmamk_f32 v53, v71, 0x3a800000, v143
	v_cvt_pk_fp8_f32 v69, v66, v67 op_sel:[0,0,1]
	v_cvt_pk_fp8_f32 v57, v52, v53
	v_fmamk_f32 v52, v58, 0x3a800000, v142
	v_fmamk_f32 v53, v59, 0x3a800000, v143
	v_mov_b32_e32 v58, v163
	v_cvt_pk_fp8_f32 v58, v52, v53
	global_store_dword v[50:51], v84, off
	global_store_dword v[50:51], v68, off offset:64
	global_store_dword v[50:51], v69, off offset:512
	global_store_dword v[50:51], v74, off offset:576
	v_lshrrev_b32_e32 v50, 2, v174
	v_and_b32_e32 v50, 0xf0, v50
	v_or_b32_e32 v50, s56, v50
	v_fmamk_f32 v56, v73, 0x3a800000, v145
	v_fmamk_f32 v52, v60, 0x3a800000, v144
	v_fmac_f32_e32 v145, 0x3a800000, v61
	v_add_u32_e32 v50, s45, v50
	v_cvt_pk_fp8_f32 v58, v52, v145 op_sel:[0,0,1]
	v_fmamk_f32 v42, v42, 0x3a800000, v138
	v_fmamk_f32 v43, v43, 0x3a800000, v139
	v_mov_b32_e32 v52, v163
	v_or_b32_e32 v50, v50, v172
	v_cvt_pk_fp8_f32 v52, v42, v43
	v_ashrrev_i32_e32 v51, 31, v50
	v_lshlrev_b64 v[50:51], 14, v[50:51]
	v_fmamk_f32 v55, v72, 0x3a800000, v144
	v_lshl_add_u64 v[50:51], s[18:19], 0, v[50:51]
	v_cvt_pk_fp8_f32 v57, v55, v56 op_sel:[0,0,1]
	v_fmamk_f32 v44, v44, 0x3a800000, v140
	v_fmamk_f32 v45, v45, 0x3a800000, v141
	v_lshl_add_u64 v[50:51], v[50:51], 0, v[162:163]
	v_cvt_pk_fp8_f32 v52, v44, v45 op_sel:[0,0,1]
	v_fmamk_f32 v34, v34, 0x3a800000, v138
	v_fmamk_f32 v35, v35, 0x3a800000, v139
	v_mov_b32_e32 v44, v163
	global_store_dword v[50:51], v62, off
	global_store_dword v[50:51], v54, off offset:64
	global_store_dword v[50:51], v57, off offset:512
	global_store_dword v[50:51], v58, off offset:576
	v_add_u32_e32 v50, 0x90, v173
	v_cvt_pk_fp8_f32 v44, v34, v35
	v_lshrrev_b32_e32 v50, 2, v50
	v_and_b32_e32 v50, 0xf4, v50
	v_or_b32_e32 v50, s56, v50
	v_fmamk_f32 v36, v36, 0x3a800000, v140
	v_fmamk_f32 v37, v37, 0x3a800000, v141
	v_add_u32_e32 v50, s45, v50
	v_cvt_pk_fp8_f32 v44, v36, v37 op_sel:[0,0,1]
	v_fmamk_f32 v36, v46, 0x3a800000, v138
	v_fmamk_f32 v37, v47, 0x3a800000, v139
	v_mov_b32_e32 v45, v163
	v_or_b32_e32 v50, v50, v172
	v_cvt_pk_fp8_f32 v45, v36, v37
	v_fmamk_f32 v36, v38, 0x3a800000, v138
	v_fmamk_f32 v37, v39, 0x3a800000, v139
	v_mov_b32_e32 v38, v163
	v_ashrrev_i32_e32 v51, 31, v50
	v_cvt_pk_fp8_f32 v38, v36, v37
	v_lshlrev_b64 v[42:43], 14, v[50:51]
	v_lshl_add_u64 v[42:43], s[18:19], 0, v[42:43]
	v_lshl_add_u64 v[34:35], v[42:43], 0, v[162:163]
	v_fmamk_f32 v43, v49, 0x3a800000, v141
	v_fmamk_f32 v36, v40, 0x3a800000, v140
	v_fmac_f32_e32 v141, 0x3a800000, v41
	v_cvt_pk_fp8_f32 v38, v36, v141 op_sel:[0,0,1]
	v_fmamk_f32 v26, v26, 0x3a800000, v134
	v_fmamk_f32 v27, v27, 0x3a800000, v135
	v_mov_b32_e32 v36, v163
	v_cvt_pk_fp8_f32 v36, v26, v27
	v_fmamk_f32 v42, v48, 0x3a800000, v140
	v_cvt_pk_fp8_f32 v45, v42, v43 op_sel:[0,0,1]
	v_fmamk_f32 v28, v28, 0x3a800000, v136
	v_fmamk_f32 v29, v29, 0x3a800000, v137
	v_cvt_pk_fp8_f32 v36, v28, v29 op_sel:[0,0,1]
	v_fmamk_f32 v18, v18, 0x3a800000, v134
	v_fmamk_f32 v19, v19, 0x3a800000, v135
	v_mov_b32_e32 v28, v163
	global_store_dword v[34:35], v52, off
	global_store_dword v[34:35], v44, off offset:64
	global_store_dword v[34:35], v45, off offset:512
	global_store_dword v[34:35], v38, off offset:576
	v_add_u32_e32 v34, 0xa0, v173
	v_cvt_pk_fp8_f32 v28, v18, v19
	v_lshrrev_b32_e32 v34, 2, v34
	v_and_b32_e32 v34, 0xf8, v34
	v_or_b32_e32 v34, s56, v34
	v_fmamk_f32 v20, v20, 0x3a800000, v136
	v_fmamk_f32 v21, v21, 0x3a800000, v137
	v_add_u32_e32 v34, s45, v34
	v_cvt_pk_fp8_f32 v28, v20, v21 op_sel:[0,0,1]
	v_fmamk_f32 v20, v30, 0x3a800000, v134
	v_fmamk_f32 v21, v31, 0x3a800000, v135
	v_mov_b32_e32 v29, v163
	v_or_b32_e32 v34, v34, v172
	v_cvt_pk_fp8_f32 v29, v20, v21
	v_fmamk_f32 v20, v22, 0x3a800000, v134
	v_fmamk_f32 v21, v23, 0x3a800000, v135
	v_mov_b32_e32 v22, v163
	v_ashrrev_i32_e32 v35, 31, v34
	v_cvt_pk_fp8_f32 v22, v20, v21
	v_lshlrev_b64 v[26:27], 14, v[34:35]
	v_lshl_add_u64 v[26:27], s[18:19], 0, v[26:27]
	v_lshl_add_u64 v[18:19], v[26:27], 0, v[162:163]
	v_fmamk_f32 v27, v33, 0x3a800000, v137
	v_fmamk_f32 v20, v24, 0x3a800000, v136
	v_fmac_f32_e32 v137, 0x3a800000, v25
	v_cvt_pk_fp8_f32 v22, v20, v137 op_sel:[0,0,1]
	v_fmamk_f32 v10, v10, 0x3a800000, v130
	v_fmamk_f32 v11, v11, 0x3a800000, v131
	v_mov_b32_e32 v20, v163
	v_cvt_pk_fp8_f32 v20, v10, v11
	v_fmamk_f32 v26, v32, 0x3a800000, v136
	v_cvt_pk_fp8_f32 v29, v26, v27 op_sel:[0,0,1]
	v_fmamk_f32 v12, v12, 0x3a800000, v132
	v_fmamk_f32 v13, v13, 0x3a800000, v133
	global_store_dword v[18:19], v36, off
	global_store_dword v[18:19], v28, off offset:64
	global_store_dword v[18:19], v29, off offset:512
	global_store_dword v[18:19], v22, off offset:576
	v_add_u32_e32 v18, 0xb0, v173
	v_cvt_pk_fp8_f32 v20, v12, v13 op_sel:[0,0,1]
	v_fmamk_f32 v2, v2, 0x3a800000, v130
	v_fmamk_f32 v3, v3, 0x3a800000, v131
	v_mov_b32_e32 v12, v163
	v_lshrrev_b32_e32 v18, 2, v18
	v_cvt_pk_fp8_f32 v12, v2, v3
	v_and_b32_e32 v18, 0xfc, v18
	v_or_b32_e32 v18, s56, v18
	v_add_u32_e32 v18, s45, v18
	v_fmamk_f32 v4, v4, 0x3a800000, v132
	v_fmamk_f32 v5, v5, 0x3a800000, v133
	v_or_b32_e32 v18, v18, v172
	v_cvt_pk_fp8_f32 v12, v4, v5 op_sel:[0,0,1]
	v_fmamk_f32 v4, v14, 0x3a800000, v130
	v_fmamk_f32 v5, v15, 0x3a800000, v131
	v_mov_b32_e32 v13, v163
	v_ashrrev_i32_e32 v19, 31, v18
	v_cvt_pk_fp8_f32 v13, v4, v5
	v_fmamk_f32 v4, v6, 0x3a800000, v130
	v_fmamk_f32 v5, v7, 0x3a800000, v131
	v_mov_b32_e32 v6, v163
	v_lshlrev_b64 v[10:11], 14, v[18:19]
	v_cvt_pk_fp8_f32 v6, v4, v5
	v_lshl_add_u64 v[10:11], s[18:19], 0, v[10:11]
	v_lshl_add_u64 v[2:3], v[10:11], 0, v[162:163]
	v_fmamk_f32 v10, v16, 0x3a800000, v132
	v_fmamk_f32 v11, v17, 0x3a800000, v133
	v_cvt_pk_fp8_f32 v13, v10, v11 op_sel:[0,0,1]
	v_fmamk_f32 v4, v8, 0x3a800000, v132
	v_fmac_f32_e32 v133, 0x3a800000, v9
	v_cvt_pk_fp8_f32 v6, v4, v133 op_sel:[0,0,1]
	s_mov_b64 s[56:57], 0
	s_andn2_b64 vcc, exec, s[52:53]
	s_mov_b32 s50, s54
	global_store_dword v[2:3], v20, off
	global_store_dword v[2:3], v12, off offset:64
	global_store_dword v[2:3], v13, off offset:512
	global_store_dword v[2:3], v6, off offset:576
	s_cbranch_vccz .LBB2_26

.LBB2_26:
	s_endpgm
	s_nop 0
	s_nop 0
	s_nop 0
	s_nop 0
	s_nop 0
	s_nop 0
	s_nop 0
	s_nop 0
	s_nop 0
	s_nop 0
	s_nop 0
	s_nop 0
	s_nop 0
	s_nop 0
	s_nop 0
	s_nop 0
	s_nop 0
	s_nop 0
	s_nop 0
	s_nop 0
	s_endpgm
